# v13 + load segments run at s_setprio 2 (above the compute segments' 1) in all GEMM K-loops
# speedup vs baseline: 1.0117x; 1.0117x over previous
.LBB0_286:
	s_lshl_b32 s10, s51, 19
	s_add_u32 s10, s20, s10
	s_addc_u32 s11, s21, 0
	s_and_b64 s[16:17], s[4:5], exec
	s_cselect_b32 s54, s11, s31
	s_cselect_b32 s55, s10, s30
	s_lshl_b32 s14, s50, 19
	s_add_u32 s16, s15, s14
	s_addc_u32 s17, s26, 0
	s_and_b64 s[36:37], s[4:5], exec
	s_cselect_b32 s56, s17, s23
	s_cselect_b32 s57, s16, s22
	s_add_i32 s60, 0, 0x10000
	v_add_u32_e32 v198, s60, v196
	s_add_i32 s62, 0, 0x14000
	v_add_u32_e32 v199, s62, v196
	ds_read_b128 v[160:163], v198
	ds_read_b128 v[152:155], v198 offset:1024
	ds_read_b128 v[156:159], v198 offset:2048
	ds_read_b128 v[148:151], v198 offset:3072
	ds_read_b128 v[144:147], v199
	ds_read_b128 v[136:139], v199 offset:1024
	ds_read_b128 v[140:143], v199 offset:2048
	ds_read_b128 v[132:135], v199 offset:3072
	s_add_u32 s36, s30, 0x40080
	s_addc_u32 s37, s31, 0
	s_add_i32 s58, s41, 0xc000
	v_lshl_add_u64 v[174:175], s[36:37], 0, v[168:169]
	s_mov_b32 m0, s58
	s_add_i32 s59, s41, 0xe000
	ds_read_b128 v[178:181], v197
	ds_read_b128 v[182:185], v197 offset:1024
	ds_read_b128 v[190:193], v197 offset:2048
	ds_read_b128 v[200:203], v197 offset:3072
	ds_read_b128 v[204:207], v197 offset:4096
	ds_read_b128 v[208:211], v197 offset:5120
	ds_read_b128 v[212:215], v197 offset:6144
	ds_read_b128 v[216:219], v197 offset:7168
	global_load_lds_dwordx4 v[174:175], off
	v_lshl_add_u64 v[174:175], s[36:37], 0, v[166:167]
	s_mov_b32 m0, s59
	s_nop 0
	global_load_lds_dwordx4 v[174:175], off
	s_waitcnt vmcnt(8)
	s_waitcnt lgkmcnt(0)
	s_barrier
	s_setprio 1
	s_waitcnt lgkmcnt(0)
	v_mfma_f32_16x16x32_bf16 v[128:131], v[160:163], v[178:181], 0
	v_mfma_f32_16x16x32_bf16 v[124:127], v[156:159], v[178:181], 0
	v_mfma_f32_16x16x32_bf16 v[116:119], v[156:159], v[190:193], 0
	v_mfma_f32_16x16x32_bf16 v[120:123], v[160:163], v[190:193], 0
	v_mfma_f32_16x16x32_bf16 v[112:115], v[160:163], v[204:207], 0
	v_mfma_f32_16x16x32_bf16 v[108:111], v[156:159], v[204:207], 0
	v_mfma_f32_16x16x32_bf16 v[100:103], v[156:159], v[212:215], 0
	v_mfma_f32_16x16x32_bf16 v[104:107], v[160:163], v[212:215], 0
	s_nop 0
	v_mfma_f32_16x16x32_bf16 v[128:131], v[152:155], v[182:185], v[128:131]
	v_mfma_f32_16x16x32_bf16 v[124:127], v[148:151], v[182:185], v[124:127]
	v_mfma_f32_16x16x32_bf16 v[116:119], v[148:151], v[200:203], v[116:119]
	v_mfma_f32_16x16x32_bf16 v[120:123], v[152:155], v[200:203], v[120:123]
	v_mfma_f32_16x16x32_bf16 v[112:115], v[152:155], v[208:211], v[112:115]
	v_mfma_f32_16x16x32_bf16 v[108:111], v[148:151], v[208:211], v[108:111]
	v_mfma_f32_16x16x32_bf16 v[100:103], v[148:151], v[216:219], v[100:103]
	v_mfma_f32_16x16x32_bf16 v[104:107], v[152:155], v[216:219], v[104:107]
	s_setprio 2
	s_setprio 1
	v_mfma_f32_16x16x32_bf16 v[96:99], v[144:147], v[178:181], 0
	v_mfma_f32_16x16x32_bf16 v[92:95], v[140:143], v[178:181], 0
	v_mfma_f32_16x16x32_bf16 v[84:87], v[140:143], v[190:193], 0
	v_mfma_f32_16x16x32_bf16 v[88:91], v[144:147], v[190:193], 0
	v_mfma_f32_16x16x32_bf16 v[80:83], v[144:147], v[204:207], 0
	v_mfma_f32_16x16x32_bf16 v[76:79], v[140:143], v[204:207], 0
	v_mfma_f32_16x16x32_bf16 v[68:71], v[140:143], v[212:215], 0
	v_mfma_f32_16x16x32_bf16 v[72:75], v[144:147], v[212:215], 0
	s_nop 0
	v_mfma_f32_16x16x32_bf16 v[96:99], v[136:139], v[182:185], v[96:99]
	v_mfma_f32_16x16x32_bf16 v[92:95], v[132:135], v[182:185], v[92:95]
	v_mfma_f32_16x16x32_bf16 v[84:87], v[132:135], v[200:203], v[84:87]
	v_mfma_f32_16x16x32_bf16 v[88:91], v[136:139], v[200:203], v[88:91]
	v_mfma_f32_16x16x32_bf16 v[80:83], v[136:139], v[208:211], v[80:83]
	v_mfma_f32_16x16x32_bf16 v[76:79], v[132:135], v[208:211], v[76:79]
	v_mfma_f32_16x16x32_bf16 v[68:71], v[132:135], v[216:219], v[68:71]
	v_mfma_f32_16x16x32_bf16 v[72:75], v[136:139], v[216:219], v[72:75]
	s_setprio 2
	s_barrier
	v_lshl_add_u64 v[174:175], s[22:23], 0, v[34:35]
	s_add_i32 s60, s60, s40
	v_lshl_add_u64 v[190:191], v[174:175], 0, s[28:29]
	s_mov_b32 m0, s60
	s_add_i32 s61, s60, 0x2000
	ds_read_b128 v[178:181], v197 offset:16384
	ds_read_b128 v[182:185], v197 offset:17408
	ds_read_b128 v[200:203], v197 offset:18432
	ds_read_b128 v[204:207], v197 offset:19456
	ds_read_b128 v[208:211], v197 offset:20480
	ds_read_b128 v[212:215], v197 offset:21504
	ds_read_b128 v[216:219], v197 offset:22528
	ds_read_b128 v[222:225], v197 offset:23552
	global_load_lds_dwordx4 v[190:191], off
	v_lshl_add_u64 v[190:191], s[22:23], 0, v[164:165]
	s_add_u32 s36, s22, 0x40100
	v_lshl_add_u64 v[192:193], v[190:191], 0, s[28:29]
	s_mov_b32 m0, s61
	s_addc_u32 s37, s23, 0
	s_add_i32 s62, s62, s40
	global_load_lds_dwordx4 v[192:193], off
	v_lshl_add_u64 v[192:193], s[36:37], 0, v[34:35]
	s_mov_b32 m0, s62
	s_add_i32 s63, s62, 0x2000
	global_load_lds_dwordx4 v[192:193], off
	v_lshl_add_u64 v[192:193], s[36:37], 0, v[164:165]
	s_mov_b32 m0, s63
	s_nop 0
	global_load_lds_dwordx4 v[192:193], off
	v_lshl_add_u64 v[192:193], s[30:31], 0, v[168:169]
	v_lshl_add_u64 v[194:195], v[192:193], 0, s[28:29]
	s_mov_b32 m0, s41
	s_nop 0
	global_load_lds_dwordx4 v[194:195], off
	v_lshl_add_u64 v[194:195], s[30:31], 0, v[166:167]
	v_lshl_add_u64 v[226:227], v[194:195], 0, s[28:29]
	s_mov_b32 m0, s42
	s_nop 0
	global_load_lds_dwordx4 v[226:227], off
	s_waitcnt vmcnt(8)
	s_waitcnt lgkmcnt(0)
	s_barrier
	s_setprio 1
	s_waitcnt lgkmcnt(0)
	v_mfma_f32_16x16x32_bf16 v[64:67], v[160:163], v[178:181], 0
	v_mfma_f32_16x16x32_bf16 v[60:63], v[156:159], v[178:181], 0
	v_mfma_f32_16x16x32_bf16 v[52:55], v[156:159], v[200:203], 0
	v_mfma_f32_16x16x32_bf16 v[56:59], v[160:163], v[200:203], 0
	v_mfma_f32_16x16x32_bf16 v[48:51], v[160:163], v[208:211], 0
	v_mfma_f32_16x16x32_bf16 v[44:47], v[156:159], v[208:211], 0
	v_mfma_f32_16x16x32_bf16 v[36:39], v[156:159], v[216:219], 0
	v_mfma_f32_16x16x32_bf16 v[40:43], v[160:163], v[216:219], 0
	s_nop 0
	v_mfma_f32_16x16x32_bf16 v[64:67], v[152:155], v[182:185], v[64:67]
	v_mfma_f32_16x16x32_bf16 v[60:63], v[148:151], v[182:185], v[60:63]
	v_mfma_f32_16x16x32_bf16 v[52:55], v[148:151], v[204:207], v[52:55]
	v_mfma_f32_16x16x32_bf16 v[56:59], v[152:155], v[204:207], v[56:59]
	v_mfma_f32_16x16x32_bf16 v[48:51], v[152:155], v[212:215], v[48:51]
	v_mfma_f32_16x16x32_bf16 v[44:47], v[148:151], v[212:215], v[44:47]
	v_mfma_f32_16x16x32_bf16 v[36:39], v[148:151], v[222:225], v[36:39]
	v_mfma_f32_16x16x32_bf16 v[40:43], v[152:155], v[222:225], v[40:43]
	s_setprio 2
	s_setprio 1
	v_mfma_f32_16x16x32_bf16 v[30:33], v[144:147], v[178:181], 0
	v_mfma_f32_16x16x32_bf16 v[26:29], v[140:143], v[178:181], 0
	v_mfma_f32_16x16x32_bf16 v[18:21], v[140:143], v[200:203], 0
	v_mfma_f32_16x16x32_bf16 v[22:25], v[144:147], v[200:203], 0
	v_mfma_f32_16x16x32_bf16 v[14:17], v[144:147], v[208:211], 0
	v_mfma_f32_16x16x32_bf16 v[10:13], v[140:143], v[208:211], 0
	v_mfma_f32_16x16x32_bf16 v[2:5], v[140:143], v[216:219], 0
	v_mfma_f32_16x16x32_bf16 v[6:9], v[144:147], v[216:219], 0
	s_nop 0
	v_mfma_f32_16x16x32_bf16 v[30:33], v[136:139], v[182:185], v[30:33]
	v_mfma_f32_16x16x32_bf16 v[26:29], v[132:135], v[182:185], v[26:29]
	v_mfma_f32_16x16x32_bf16 v[18:21], v[132:135], v[204:207], v[18:21]
	v_mfma_f32_16x16x32_bf16 v[22:25], v[136:139], v[204:207], v[22:25]
	v_mfma_f32_16x16x32_bf16 v[14:17], v[136:139], v[212:215], v[14:17]
	v_mfma_f32_16x16x32_bf16 v[10:13], v[132:135], v[212:215], v[10:13]
	v_mfma_f32_16x16x32_bf16 v[2:5], v[132:135], v[222:225], v[2:5]
	v_mfma_f32_16x16x32_bf16 v[6:9], v[136:139], v[222:225], v[6:9]
	s_setprio 2
	s_barrier
	s_add_i32 s64, 0, 0x18000
	s_add_i32 s66, 0, 0x1c000
	v_add_u32_e32 v132, s64, v196
	v_add_u32_e32 v133, s66, v196
	ds_read_b128 v[134:137], v132
	ds_read_b128 v[138:141], v132 offset:1024
	ds_read_b128 v[142:145], v132 offset:2048
	ds_read_b128 v[146:149], v132 offset:3072
	ds_read_b128 v[150:153], v133
	ds_read_b128 v[154:157], v133 offset:1024
	ds_read_b128 v[158:161], v133 offset:2048
	ds_read_b128 v[178:181], v133 offset:3072
	s_add_u32 s36, s30, 0x40100
	s_addc_u32 s37, s31, 0
	s_mov_b32 m0, s43
	v_lshl_add_u64 v[162:163], s[36:37], 0, v[168:169]
	ds_read_b128 v[182:185], v197 offset:32768
	ds_read_b128 v[200:203], v197 offset:33792
	ds_read_b128 v[204:207], v197 offset:34816
	ds_read_b128 v[208:211], v197 offset:35840
	ds_read_b128 v[212:215], v197 offset:36864
	ds_read_b128 v[216:219], v197 offset:37888
	ds_read_b128 v[222:225], v197 offset:38912
	ds_read_b128 v[226:229], v197 offset:39936
	global_load_lds_dwordx4 v[162:163], off
	v_lshl_add_u64 v[162:163], s[36:37], 0, v[166:167]
	s_mov_b32 m0, s44
	s_nop 0
	global_load_lds_dwordx4 v[162:163], off
	s_waitcnt vmcnt(8)
	s_waitcnt lgkmcnt(0)
	s_barrier
	s_setprio 1
	s_waitcnt lgkmcnt(0)
	v_mfma_f32_16x16x32_bf16 v[128:131], v[134:137], v[182:185], v[128:131]
	v_mfma_f32_16x16x32_bf16 v[124:127], v[142:145], v[182:185], v[124:127]
	v_mfma_f32_16x16x32_bf16 v[116:119], v[142:145], v[204:207], v[116:119]
	v_mfma_f32_16x16x32_bf16 v[120:123], v[134:137], v[204:207], v[120:123]
	v_mfma_f32_16x16x32_bf16 v[112:115], v[134:137], v[212:215], v[112:115]
	v_mfma_f32_16x16x32_bf16 v[108:111], v[142:145], v[212:215], v[108:111]
	v_mfma_f32_16x16x32_bf16 v[100:103], v[142:145], v[222:225], v[100:103]
	v_mfma_f32_16x16x32_bf16 v[104:107], v[134:137], v[222:225], v[104:107]
	v_mfma_f32_16x16x32_bf16 v[128:131], v[138:141], v[200:203], v[128:131]
	v_mfma_f32_16x16x32_bf16 v[124:127], v[146:149], v[200:203], v[124:127]
	v_mfma_f32_16x16x32_bf16 v[116:119], v[146:149], v[208:211], v[116:119]
	v_mfma_f32_16x16x32_bf16 v[120:123], v[138:141], v[208:211], v[120:123]
	v_mfma_f32_16x16x32_bf16 v[112:115], v[138:141], v[216:219], v[112:115]
	v_mfma_f32_16x16x32_bf16 v[108:111], v[146:149], v[216:219], v[108:111]
	v_mfma_f32_16x16x32_bf16 v[100:103], v[146:149], v[226:229], v[100:103]
	v_mfma_f32_16x16x32_bf16 v[104:107], v[138:141], v[226:229], v[104:107]
	s_setprio 2
	s_setprio 1
	v_mfma_f32_16x16x32_bf16 v[96:99], v[150:153], v[182:185], v[96:99]
	v_mfma_f32_16x16x32_bf16 v[92:95], v[158:161], v[182:185], v[92:95]
	v_mfma_f32_16x16x32_bf16 v[84:87], v[158:161], v[204:207], v[84:87]
	v_mfma_f32_16x16x32_bf16 v[88:91], v[150:153], v[204:207], v[88:91]
	v_mfma_f32_16x16x32_bf16 v[80:83], v[150:153], v[212:215], v[80:83]
	v_mfma_f32_16x16x32_bf16 v[76:79], v[158:161], v[212:215], v[76:79]
	v_mfma_f32_16x16x32_bf16 v[68:71], v[158:161], v[222:225], v[68:71]
	v_mfma_f32_16x16x32_bf16 v[72:75], v[150:153], v[222:225], v[72:75]
	v_mfma_f32_16x16x32_bf16 v[96:99], v[154:157], v[200:203], v[96:99]
	v_mfma_f32_16x16x32_bf16 v[92:95], v[178:181], v[200:203], v[92:95]
	v_mfma_f32_16x16x32_bf16 v[84:87], v[178:181], v[208:211], v[84:87]
	v_mfma_f32_16x16x32_bf16 v[88:91], v[154:157], v[208:211], v[88:91]
	v_mfma_f32_16x16x32_bf16 v[80:83], v[154:157], v[216:219], v[80:83]
	v_mfma_f32_16x16x32_bf16 v[76:79], v[178:181], v[216:219], v[76:79]
	v_mfma_f32_16x16x32_bf16 v[68:71], v[178:181], v[226:229], v[68:71]
	v_mfma_f32_16x16x32_bf16 v[72:75], v[154:157], v[226:229], v[72:75]
	s_setprio 2
	s_barrier
	s_add_i32 s64, s64, s40
	s_mov_b64 s[24:25], 0x180
	s_add_i32 s65, s64, 0x2000
	v_lshl_add_u64 v[162:163], v[174:175], 0, s[24:25]
	s_mov_b32 m0, s64
	s_add_u32 s36, s22, 0x40180
	ds_read_b128 v[182:185], v197 offset:49152
	ds_read_b128 v[200:203], v197 offset:50176
	ds_read_b128 v[204:207], v197 offset:51200
	ds_read_b128 v[208:211], v197 offset:52224
	ds_read_b128 v[212:215], v197 offset:53248
	ds_read_b128 v[216:219], v197 offset:54272
	ds_read_b128 v[222:225], v197 offset:55296
	ds_read_b128 v[226:229], v197 offset:56320
	global_load_lds_dwordx4 v[162:163], off
	v_lshl_add_u64 v[162:163], v[190:191], 0, s[24:25]
	s_mov_b32 m0, s65
	s_addc_u32 s37, s23, 0
	s_add_i32 s66, s66, s40
	global_load_lds_dwordx4 v[162:163], off
	v_lshl_add_u64 v[162:163], s[36:37], 0, v[34:35]
	s_mov_b32 m0, s66
	s_add_i32 s67, s66, 0x2000
	global_load_lds_dwordx4 v[162:163], off
	v_lshl_add_u64 v[162:163], s[36:37], 0, v[164:165]
	s_mov_b32 m0, s67
	s_nop 0
	global_load_lds_dwordx4 v[162:163], off
	v_lshl_add_u64 v[162:163], v[192:193], 0, s[24:25]
	s_mov_b32 m0, s47
	s_nop 0
	global_load_lds_dwordx4 v[162:163], off
	v_lshl_add_u64 v[162:163], v[194:195], 0, s[24:25]
	s_mov_b32 m0, s48
	s_nop 0
	global_load_lds_dwordx4 v[162:163], off
	s_waitcnt vmcnt(8)
	s_waitcnt lgkmcnt(0)
	s_barrier
	s_setprio 1
	s_waitcnt lgkmcnt(0)
	v_mfma_f32_16x16x32_bf16 v[64:67], v[134:137], v[182:185], v[64:67]
	v_mfma_f32_16x16x32_bf16 v[60:63], v[142:145], v[182:185], v[60:63]
	v_mfma_f32_16x16x32_bf16 v[52:55], v[142:145], v[204:207], v[52:55]
	v_mfma_f32_16x16x32_bf16 v[56:59], v[134:137], v[204:207], v[56:59]
	v_mfma_f32_16x16x32_bf16 v[48:51], v[134:137], v[212:215], v[48:51]
	v_mfma_f32_16x16x32_bf16 v[44:47], v[142:145], v[212:215], v[44:47]
	v_mfma_f32_16x16x32_bf16 v[36:39], v[142:145], v[222:225], v[36:39]
	v_mfma_f32_16x16x32_bf16 v[40:43], v[134:137], v[222:225], v[40:43]
	v_mfma_f32_16x16x32_bf16 v[64:67], v[138:141], v[200:203], v[64:67]
	v_mfma_f32_16x16x32_bf16 v[60:63], v[146:149], v[200:203], v[60:63]
	v_mfma_f32_16x16x32_bf16 v[52:55], v[146:149], v[208:211], v[52:55]
	v_mfma_f32_16x16x32_bf16 v[56:59], v[138:141], v[208:211], v[56:59]
	v_mfma_f32_16x16x32_bf16 v[48:51], v[138:141], v[216:219], v[48:51]
	v_mfma_f32_16x16x32_bf16 v[44:47], v[146:149], v[216:219], v[44:47]
	v_mfma_f32_16x16x32_bf16 v[36:39], v[146:149], v[226:229], v[36:39]
	v_mfma_f32_16x16x32_bf16 v[40:43], v[138:141], v[226:229], v[40:43]
	s_setprio 2
	s_setprio 1
	v_mfma_f32_16x16x32_bf16 v[30:33], v[150:153], v[182:185], v[30:33]
	v_mfma_f32_16x16x32_bf16 v[26:29], v[158:161], v[182:185], v[26:29]
	v_mfma_f32_16x16x32_bf16 v[18:21], v[158:161], v[204:207], v[18:21]
	v_mfma_f32_16x16x32_bf16 v[22:25], v[150:153], v[204:207], v[22:25]
	v_mfma_f32_16x16x32_bf16 v[14:17], v[150:153], v[212:215], v[14:17]
	v_mfma_f32_16x16x32_bf16 v[10:13], v[158:161], v[212:215], v[10:13]
	v_mfma_f32_16x16x32_bf16 v[2:5], v[158:161], v[222:225], v[2:5]
	v_mfma_f32_16x16x32_bf16 v[6:9], v[150:153], v[222:225], v[6:9]
	v_mfma_f32_16x16x32_bf16 v[30:33], v[154:157], v[200:203], v[30:33]
	v_mfma_f32_16x16x32_bf16 v[26:29], v[178:181], v[200:203], v[26:29]
	v_mfma_f32_16x16x32_bf16 v[18:21], v[178:181], v[208:211], v[18:21]
	v_mfma_f32_16x16x32_bf16 v[22:25], v[154:157], v[208:211], v[22:25]
	v_mfma_f32_16x16x32_bf16 v[14:17], v[154:157], v[216:219], v[14:17]
	v_mfma_f32_16x16x32_bf16 v[10:13], v[178:181], v[216:219], v[10:13]
	v_mfma_f32_16x16x32_bf16 v[2:5], v[178:181], v[226:229], v[2:5]
	v_mfma_f32_16x16x32_bf16 v[6:9], v[154:157], v[226:229], v[6:9]
	s_setprio 2
	s_barrier
	s_add_u32 s30, s30, 0x40180
	s_addc_u32 s31, s31, 0
	s_add_u32 s68, s22, 0x200
	s_addc_u32 s69, s23, 0
	s_mov_b32 s70, 0
.LBB0_287:
	ds_read_b128 v[134:137], v198
	ds_read_b128 v[138:141], v198 offset:1024
	ds_read_b128 v[142:145], v198 offset:2048
	ds_read_b128 v[146:149], v198 offset:3072
	ds_read_b128 v[150:153], v199
	ds_read_b128 v[154:157], v199 offset:1024
	ds_read_b128 v[158:161], v199 offset:2048
	ds_read_b128 v[178:181], v199 offset:3072
	s_add_u32 s14, s30, 0xfffc0080
	s_addc_u32 s22, s31, -1
	s_cmp_eq_u32 s70, 12
	s_cselect_b32 s37, s54, s22
	s_cselect_b32 s36, s55, s14
	s_cselect_b32 s23, s56, s69
	s_cselect_b32 s22, s57, s68
	s_mov_b32 m0, s58
	v_lshl_add_u64 v[162:163], s[30:31], 0, v[170:171]
	ds_read_b128 v[182:185], v197
	ds_read_b128 v[190:193], v197 offset:1024
	ds_read_b128 v[200:203], v197 offset:2048
	ds_read_b128 v[204:207], v197 offset:3072
	ds_read_b128 v[208:211], v197 offset:4096
	ds_read_b128 v[212:215], v197 offset:5120
	ds_read_b128 v[216:219], v197 offset:6144
	ds_read_b128 v[222:225], v197 offset:7168
	global_load_lds_dwordx4 v[162:163], off
	v_lshl_add_u64 v[162:163], s[30:31], 0, v[172:173]
	s_mov_b32 m0, s59
	s_nop 0
	global_load_lds_dwordx4 v[162:163], off
	s_waitcnt vmcnt(8)
	s_waitcnt lgkmcnt(0)
	s_barrier
	s_setprio 1
	s_waitcnt lgkmcnt(0)
	v_mfma_f32_16x16x32_bf16 v[128:131], v[134:137], v[182:185], v[128:131]
	v_mfma_f32_16x16x32_bf16 v[124:127], v[142:145], v[182:185], v[124:127]
	v_mfma_f32_16x16x32_bf16 v[116:119], v[142:145], v[200:203], v[116:119]
	v_mfma_f32_16x16x32_bf16 v[120:123], v[134:137], v[200:203], v[120:123]
	v_mfma_f32_16x16x32_bf16 v[112:115], v[134:137], v[208:211], v[112:115]
	v_mfma_f32_16x16x32_bf16 v[108:111], v[142:145], v[208:211], v[108:111]
	v_mfma_f32_16x16x32_bf16 v[100:103], v[142:145], v[216:219], v[100:103]
	v_mfma_f32_16x16x32_bf16 v[104:107], v[134:137], v[216:219], v[104:107]
	v_mfma_f32_16x16x32_bf16 v[128:131], v[138:141], v[190:193], v[128:131]
	v_mfma_f32_16x16x32_bf16 v[124:127], v[146:149], v[190:193], v[124:127]
	v_mfma_f32_16x16x32_bf16 v[116:119], v[146:149], v[204:207], v[116:119]
	v_mfma_f32_16x16x32_bf16 v[120:123], v[138:141], v[204:207], v[120:123]
	v_mfma_f32_16x16x32_bf16 v[112:115], v[138:141], v[212:215], v[112:115]
	v_mfma_f32_16x16x32_bf16 v[108:111], v[146:149], v[212:215], v[108:111]
	v_mfma_f32_16x16x32_bf16 v[100:103], v[146:149], v[222:225], v[100:103]
	v_mfma_f32_16x16x32_bf16 v[104:107], v[138:141], v[222:225], v[104:107]
	s_setprio 2
	s_setprio 1
	v_mfma_f32_16x16x32_bf16 v[96:99], v[150:153], v[182:185], v[96:99]
	v_mfma_f32_16x16x32_bf16 v[92:95], v[158:161], v[182:185], v[92:95]
	v_mfma_f32_16x16x32_bf16 v[84:87], v[158:161], v[200:203], v[84:87]
	v_mfma_f32_16x16x32_bf16 v[88:91], v[150:153], v[200:203], v[88:91]
	v_mfma_f32_16x16x32_bf16 v[80:83], v[150:153], v[208:211], v[80:83]
	v_mfma_f32_16x16x32_bf16 v[76:79], v[158:161], v[208:211], v[76:79]
	v_mfma_f32_16x16x32_bf16 v[68:71], v[158:161], v[216:219], v[68:71]
	v_mfma_f32_16x16x32_bf16 v[72:75], v[150:153], v[216:219], v[72:75]
	v_mfma_f32_16x16x32_bf16 v[96:99], v[154:157], v[190:193], v[96:99]
	v_mfma_f32_16x16x32_bf16 v[92:95], v[178:181], v[190:193], v[92:95]
	v_mfma_f32_16x16x32_bf16 v[84:87], v[178:181], v[204:207], v[84:87]
	v_mfma_f32_16x16x32_bf16 v[88:91], v[154:157], v[204:207], v[88:91]
	v_mfma_f32_16x16x32_bf16 v[80:83], v[154:157], v[212:215], v[80:83]
	v_mfma_f32_16x16x32_bf16 v[76:79], v[178:181], v[212:215], v[76:79]
	v_mfma_f32_16x16x32_bf16 v[68:71], v[178:181], v[222:225], v[68:71]
	v_mfma_f32_16x16x32_bf16 v[72:75], v[154:157], v[222:225], v[72:75]
	s_setprio 2
	s_barrier
	s_mov_b32 m0, s60
	v_lshl_add_u64 v[162:163], s[22:23], 0, v[34:35]
	s_add_u32 s72, s22, 0x40000
	ds_read_b128 v[182:185], v197 offset:16384
	ds_read_b128 v[190:193], v197 offset:17408
	ds_read_b128 v[200:203], v197 offset:18432
	ds_read_b128 v[204:207], v197 offset:19456
	ds_read_b128 v[208:211], v197 offset:20480
	ds_read_b128 v[212:215], v197 offset:21504
	ds_read_b128 v[216:219], v197 offset:22528
	ds_read_b128 v[222:225], v197 offset:23552
	global_load_lds_dwordx4 v[162:163], off
	v_lshl_add_u64 v[174:175], s[22:23], 0, v[164:165]
	s_mov_b32 m0, s61
	s_addc_u32 s73, s23, 0
	global_load_lds_dwordx4 v[174:175], off
	v_lshl_add_u64 v[194:195], s[72:73], 0, v[34:35]
	s_mov_b32 m0, s62
	v_lshl_add_u64 v[226:227], s[36:37], 0, v[166:167]
	global_load_lds_dwordx4 v[194:195], off
	v_lshl_add_u64 v[194:195], s[72:73], 0, v[164:165]
	s_mov_b32 m0, s63
	s_nop 0
	global_load_lds_dwordx4 v[194:195], off
	v_lshl_add_u64 v[194:195], s[36:37], 0, v[168:169]
	s_mov_b32 m0, s41
	s_nop 0
	global_load_lds_dwordx4 v[194:195], off
	s_mov_b32 m0, s42
	s_nop 0
	global_load_lds_dwordx4 v[226:227], off
	s_waitcnt vmcnt(8)
	s_waitcnt lgkmcnt(0)
	s_barrier
	s_setprio 1
	s_waitcnt lgkmcnt(0)
	v_mfma_f32_16x16x32_bf16 v[64:67], v[134:137], v[182:185], v[64:67]
	v_mfma_f32_16x16x32_bf16 v[60:63], v[142:145], v[182:185], v[60:63]
	v_mfma_f32_16x16x32_bf16 v[52:55], v[142:145], v[200:203], v[52:55]
	v_mfma_f32_16x16x32_bf16 v[56:59], v[134:137], v[200:203], v[56:59]
	v_mfma_f32_16x16x32_bf16 v[48:51], v[134:137], v[208:211], v[48:51]
	v_mfma_f32_16x16x32_bf16 v[44:47], v[142:145], v[208:211], v[44:47]
	v_mfma_f32_16x16x32_bf16 v[36:39], v[142:145], v[216:219], v[36:39]
	v_mfma_f32_16x16x32_bf16 v[40:43], v[134:137], v[216:219], v[40:43]
	v_mfma_f32_16x16x32_bf16 v[64:67], v[138:141], v[190:193], v[64:67]
	v_mfma_f32_16x16x32_bf16 v[60:63], v[146:149], v[190:193], v[60:63]
	v_mfma_f32_16x16x32_bf16 v[52:55], v[146:149], v[204:207], v[52:55]
	v_mfma_f32_16x16x32_bf16 v[56:59], v[138:141], v[204:207], v[56:59]
	v_mfma_f32_16x16x32_bf16 v[48:51], v[138:141], v[212:215], v[48:51]
	v_mfma_f32_16x16x32_bf16 v[44:47], v[146:149], v[212:215], v[44:47]
	v_mfma_f32_16x16x32_bf16 v[36:39], v[146:149], v[222:225], v[36:39]
	v_mfma_f32_16x16x32_bf16 v[40:43], v[138:141], v[222:225], v[40:43]
	s_setprio 2
	s_setprio 1
	v_mfma_f32_16x16x32_bf16 v[30:33], v[150:153], v[182:185], v[30:33]
	v_mfma_f32_16x16x32_bf16 v[26:29], v[158:161], v[182:185], v[26:29]
	v_mfma_f32_16x16x32_bf16 v[18:21], v[158:161], v[200:203], v[18:21]
	v_mfma_f32_16x16x32_bf16 v[22:25], v[150:153], v[200:203], v[22:25]
	v_mfma_f32_16x16x32_bf16 v[14:17], v[150:153], v[208:211], v[14:17]
	v_mfma_f32_16x16x32_bf16 v[10:13], v[158:161], v[208:211], v[10:13]
	v_mfma_f32_16x16x32_bf16 v[2:5], v[158:161], v[216:219], v[2:5]
	v_mfma_f32_16x16x32_bf16 v[6:9], v[150:153], v[216:219], v[6:9]
	v_mfma_f32_16x16x32_bf16 v[30:33], v[154:157], v[190:193], v[30:33]
	v_mfma_f32_16x16x32_bf16 v[26:29], v[178:181], v[190:193], v[26:29]
	v_mfma_f32_16x16x32_bf16 v[18:21], v[178:181], v[204:207], v[18:21]
	v_mfma_f32_16x16x32_bf16 v[22:25], v[154:157], v[204:207], v[22:25]
	v_mfma_f32_16x16x32_bf16 v[14:17], v[154:157], v[212:215], v[14:17]
	v_mfma_f32_16x16x32_bf16 v[10:13], v[178:181], v[212:215], v[10:13]
	v_mfma_f32_16x16x32_bf16 v[2:5], v[178:181], v[222:225], v[2:5]
	v_mfma_f32_16x16x32_bf16 v[6:9], v[154:157], v[222:225], v[6:9]
	s_setprio 2
	s_barrier
	ds_read_b128 v[134:137], v132
	ds_read_b128 v[138:141], v132 offset:1024
	ds_read_b128 v[142:145], v132 offset:2048
	ds_read_b128 v[146:149], v132 offset:3072
	ds_read_b128 v[150:153], v133
	ds_read_b128 v[154:157], v133 offset:1024
	ds_read_b128 v[158:161], v133 offset:2048
	ds_read_b128 v[178:181], v133 offset:3072
	s_add_u32 s36, s36, 0x40000
	s_addc_u32 s37, s37, 0
	s_mov_b32 m0, s43
	v_lshl_add_u64 v[228:229], s[36:37], 0, v[168:169]
	ds_read_b128 v[182:185], v197 offset:32768
	ds_read_b128 v[190:193], v197 offset:33792
	ds_read_b128 v[200:203], v197 offset:34816
	ds_read_b128 v[204:207], v197 offset:35840
	ds_read_b128 v[208:211], v197 offset:36864
	ds_read_b128 v[212:215], v197 offset:37888
	ds_read_b128 v[216:219], v197 offset:38912
	ds_read_b128 v[222:225], v197 offset:39936
	global_load_lds_dwordx4 v[228:229], off
	v_lshl_add_u64 v[228:229], s[36:37], 0, v[166:167]
	s_mov_b32 m0, s44
	s_nop 0
	global_load_lds_dwordx4 v[228:229], off
	s_waitcnt vmcnt(8)
	s_waitcnt lgkmcnt(0)
	s_barrier
	s_setprio 1
	s_waitcnt lgkmcnt(0)
	v_mfma_f32_16x16x32_bf16 v[128:131], v[134:137], v[182:185], v[128:131]
	v_mfma_f32_16x16x32_bf16 v[124:127], v[142:145], v[182:185], v[124:127]
	v_mfma_f32_16x16x32_bf16 v[116:119], v[142:145], v[200:203], v[116:119]
	v_mfma_f32_16x16x32_bf16 v[120:123], v[134:137], v[200:203], v[120:123]
	v_mfma_f32_16x16x32_bf16 v[112:115], v[134:137], v[208:211], v[112:115]
	v_mfma_f32_16x16x32_bf16 v[108:111], v[142:145], v[208:211], v[108:111]
	v_mfma_f32_16x16x32_bf16 v[100:103], v[142:145], v[216:219], v[100:103]
	v_mfma_f32_16x16x32_bf16 v[104:107], v[134:137], v[216:219], v[104:107]
	v_mfma_f32_16x16x32_bf16 v[128:131], v[138:141], v[190:193], v[128:131]
	v_mfma_f32_16x16x32_bf16 v[124:127], v[146:149], v[190:193], v[124:127]
	v_mfma_f32_16x16x32_bf16 v[116:119], v[146:149], v[204:207], v[116:119]
	v_mfma_f32_16x16x32_bf16 v[120:123], v[138:141], v[204:207], v[120:123]
	v_mfma_f32_16x16x32_bf16 v[112:115], v[138:141], v[212:215], v[112:115]
	v_mfma_f32_16x16x32_bf16 v[108:111], v[146:149], v[212:215], v[108:111]
	v_mfma_f32_16x16x32_bf16 v[100:103], v[146:149], v[222:225], v[100:103]
	v_mfma_f32_16x16x32_bf16 v[104:107], v[138:141], v[222:225], v[104:107]
	s_setprio 2
	s_setprio 1
	v_mfma_f32_16x16x32_bf16 v[96:99], v[150:153], v[182:185], v[96:99]
	v_mfma_f32_16x16x32_bf16 v[92:95], v[158:161], v[182:185], v[92:95]
	v_mfma_f32_16x16x32_bf16 v[84:87], v[158:161], v[200:203], v[84:87]
	v_mfma_f32_16x16x32_bf16 v[88:91], v[150:153], v[200:203], v[88:91]
	v_mfma_f32_16x16x32_bf16 v[80:83], v[150:153], v[208:211], v[80:83]
	v_mfma_f32_16x16x32_bf16 v[76:79], v[158:161], v[208:211], v[76:79]
	v_mfma_f32_16x16x32_bf16 v[68:71], v[158:161], v[216:219], v[68:71]
	v_mfma_f32_16x16x32_bf16 v[72:75], v[150:153], v[216:219], v[72:75]
	v_mfma_f32_16x16x32_bf16 v[96:99], v[154:157], v[190:193], v[96:99]
	v_mfma_f32_16x16x32_bf16 v[92:95], v[178:181], v[190:193], v[92:95]
	v_mfma_f32_16x16x32_bf16 v[84:87], v[178:181], v[204:207], v[84:87]
	v_mfma_f32_16x16x32_bf16 v[88:91], v[154:157], v[204:207], v[88:91]
	v_mfma_f32_16x16x32_bf16 v[80:83], v[154:157], v[212:215], v[80:83]
	v_mfma_f32_16x16x32_bf16 v[76:79], v[178:181], v[212:215], v[76:79]
	v_mfma_f32_16x16x32_bf16 v[68:71], v[178:181], v[222:225], v[68:71]
	v_mfma_f32_16x16x32_bf16 v[72:75], v[154:157], v[222:225], v[72:75]
	s_setprio 2
	s_barrier
	s_mov_b32 m0, s64
	v_lshl_add_u64 v[162:163], v[162:163], 0, s[18:19]
	s_add_u32 s22, s22, 0x40080
	ds_read_b128 v[182:185], v197 offset:49152
	ds_read_b128 v[190:193], v197 offset:50176
	ds_read_b128 v[200:203], v197 offset:51200
	ds_read_b128 v[204:207], v197 offset:52224
	ds_read_b128 v[208:211], v197 offset:53248
	ds_read_b128 v[212:215], v197 offset:54272
	ds_read_b128 v[216:219], v197 offset:55296
	ds_read_b128 v[222:225], v197 offset:56320
	global_load_lds_dwordx4 v[162:163], off
	v_lshl_add_u64 v[162:163], v[174:175], 0, s[18:19]
	s_mov_b32 m0, s65
	s_addc_u32 s23, s23, 0
	global_load_lds_dwordx4 v[162:163], off
	v_lshl_add_u64 v[162:163], s[22:23], 0, v[34:35]
	s_mov_b32 m0, s66
	s_nop 0
	global_load_lds_dwordx4 v[162:163], off
	v_lshl_add_u64 v[162:163], s[22:23], 0, v[164:165]
	s_mov_b32 m0, s67
	s_nop 0
	global_load_lds_dwordx4 v[162:163], off
	v_lshl_add_u64 v[162:163], v[194:195], 0, s[18:19]
	s_mov_b32 m0, s47
	s_nop 0
	global_load_lds_dwordx4 v[162:163], off
	v_lshl_add_u64 v[162:163], v[226:227], 0, s[18:19]
	s_mov_b32 m0, s48
	s_nop 0
	global_load_lds_dwordx4 v[162:163], off
	s_waitcnt vmcnt(8)
	s_waitcnt lgkmcnt(0)
	s_barrier
	s_setprio 1
	s_waitcnt lgkmcnt(0)
	v_mfma_f32_16x16x32_bf16 v[64:67], v[134:137], v[182:185], v[64:67]
	v_mfma_f32_16x16x32_bf16 v[60:63], v[142:145], v[182:185], v[60:63]
	v_mfma_f32_16x16x32_bf16 v[52:55], v[142:145], v[200:203], v[52:55]
	v_mfma_f32_16x16x32_bf16 v[56:59], v[134:137], v[200:203], v[56:59]
	v_mfma_f32_16x16x32_bf16 v[48:51], v[134:137], v[208:211], v[48:51]
	v_mfma_f32_16x16x32_bf16 v[44:47], v[142:145], v[208:211], v[44:47]
	v_mfma_f32_16x16x32_bf16 v[36:39], v[142:145], v[216:219], v[36:39]
	v_mfma_f32_16x16x32_bf16 v[40:43], v[134:137], v[216:219], v[40:43]
	v_mfma_f32_16x16x32_bf16 v[64:67], v[138:141], v[190:193], v[64:67]
	v_mfma_f32_16x16x32_bf16 v[60:63], v[146:149], v[190:193], v[60:63]
	v_mfma_f32_16x16x32_bf16 v[52:55], v[146:149], v[204:207], v[52:55]
	v_mfma_f32_16x16x32_bf16 v[56:59], v[138:141], v[204:207], v[56:59]
	v_mfma_f32_16x16x32_bf16 v[48:51], v[138:141], v[212:215], v[48:51]
	v_mfma_f32_16x16x32_bf16 v[44:47], v[146:149], v[212:215], v[44:47]
	v_mfma_f32_16x16x32_bf16 v[36:39], v[146:149], v[222:225], v[36:39]
	v_mfma_f32_16x16x32_bf16 v[40:43], v[138:141], v[222:225], v[40:43]
	s_setprio 2
	s_setprio 1
	v_mfma_f32_16x16x32_bf16 v[30:33], v[150:153], v[182:185], v[30:33]
	v_mfma_f32_16x16x32_bf16 v[26:29], v[158:161], v[182:185], v[26:29]
	v_mfma_f32_16x16x32_bf16 v[18:21], v[158:161], v[200:203], v[18:21]
	v_mfma_f32_16x16x32_bf16 v[22:25], v[150:153], v[200:203], v[22:25]
	v_mfma_f32_16x16x32_bf16 v[14:17], v[150:153], v[208:211], v[14:17]
	v_mfma_f32_16x16x32_bf16 v[10:13], v[158:161], v[208:211], v[10:13]
	v_mfma_f32_16x16x32_bf16 v[2:5], v[158:161], v[216:219], v[2:5]
	v_mfma_f32_16x16x32_bf16 v[6:9], v[150:153], v[216:219], v[6:9]
	v_mfma_f32_16x16x32_bf16 v[30:33], v[154:157], v[190:193], v[30:33]
	v_mfma_f32_16x16x32_bf16 v[26:29], v[178:181], v[190:193], v[26:29]
	v_mfma_f32_16x16x32_bf16 v[18:21], v[178:181], v[204:207], v[18:21]
	v_mfma_f32_16x16x32_bf16 v[22:25], v[154:157], v[204:207], v[22:25]
	v_mfma_f32_16x16x32_bf16 v[14:17], v[154:157], v[212:215], v[14:17]
	v_mfma_f32_16x16x32_bf16 v[10:13], v[178:181], v[212:215], v[10:13]
	v_mfma_f32_16x16x32_bf16 v[2:5], v[178:181], v[222:225], v[2:5]
	v_mfma_f32_16x16x32_bf16 v[6:9], v[154:157], v[222:225], v[6:9]
	s_setprio 2
	s_barrier
	s_add_i32 s70, s70, 2
	s_add_u32 s30, s30, 0x100
	s_addc_u32 s31, s31, 0
	s_add_u32 s68, s68, 0x100
	s_addc_u32 s69, s69, 0
	s_cmp_gt_u32 s70, 13
	s_cbranch_scc0 .LBB0_287
	s_and_b64 vcc, exec, s[8:9]
	s_cbranch_vccz .LBB0_290
	s_barrier

.LBB0_540:
	s_lshl_b32 s14, s55, 19
	v_readlane_b32 s16, v253, 53
	v_readlane_b32 s17, v253, 54
	s_add_u32 s16, s16, s14
	s_addc_u32 s17, s17, 0
	s_and_b64 s[22:23], s[4:5], exec
	s_cselect_b32 s58, s17, s37
	s_cselect_b32 s59, s16, s36
	s_lshl_b32 s14, s54, 19
	s_add_u32 s22, s15, s14
	s_addc_u32 s23, s26, 0
	s_and_b64 s[40:41], s[4:5], exec
	s_cselect_b32 s60, s23, s31
	s_cselect_b32 s61, s22, s30
	s_add_i32 s64, 0, 0x10000
	v_add_u32_e32 v172, s64, v222
	s_add_i32 s66, 0, 0x14000
	v_add_u32_e32 v173, s66, v222
	ds_read_b128 v[160:163], v172
	ds_read_b128 v[152:155], v172 offset:1024
	ds_read_b128 v[156:159], v172 offset:2048
	ds_read_b128 v[148:151], v172 offset:3072
	ds_read_b128 v[144:147], v173
	ds_read_b128 v[136:139], v173 offset:1024
	ds_read_b128 v[140:143], v173 offset:2048
	ds_read_b128 v[132:135], v173 offset:3072
	s_add_u32 s40, s36, 0x40080
	s_addc_u32 s41, s37, 0
	s_add_i32 s62, s43, 0xc000
	v_lshl_add_u64 v[174:175], s[40:41], 0, v[194:195]
	s_mov_b32 m0, s62
	s_add_i32 s63, s43, 0xe000
	ds_read_b128 v[164:167], v223
	ds_read_b128 v[168:171], v223 offset:1024
	ds_read_b128 v[178:181], v223 offset:2048
	ds_read_b128 v[182:185], v223 offset:3072
	ds_read_b128 v[200:203], v223 offset:4096
	ds_read_b128 v[204:207], v223 offset:5120
	ds_read_b128 v[208:211], v223 offset:6144
	ds_read_b128 v[212:215], v223 offset:7168
	global_load_lds_dwordx4 v[174:175], off
	v_lshl_add_u64 v[174:175], s[40:41], 0, v[192:193]
	s_mov_b32 m0, s63
	s_nop 0
	global_load_lds_dwordx4 v[174:175], off
	s_waitcnt vmcnt(8)
	s_waitcnt lgkmcnt(0)
	s_barrier
	s_setprio 1
	s_waitcnt lgkmcnt(0)
	v_mfma_f32_16x16x32_bf16 v[128:131], v[160:163], v[164:167], 0
	v_mfma_f32_16x16x32_bf16 v[124:127], v[156:159], v[164:167], 0
	v_mfma_f32_16x16x32_bf16 v[116:119], v[156:159], v[178:181], 0
	v_mfma_f32_16x16x32_bf16 v[120:123], v[160:163], v[178:181], 0
	v_mfma_f32_16x16x32_bf16 v[112:115], v[160:163], v[200:203], 0
	v_mfma_f32_16x16x32_bf16 v[108:111], v[156:159], v[200:203], 0
	v_mfma_f32_16x16x32_bf16 v[100:103], v[156:159], v[208:211], 0
	v_mfma_f32_16x16x32_bf16 v[104:107], v[160:163], v[208:211], 0
	s_nop 0
	v_mfma_f32_16x16x32_bf16 v[128:131], v[152:155], v[168:171], v[128:131]
	v_mfma_f32_16x16x32_bf16 v[124:127], v[148:151], v[168:171], v[124:127]
	v_mfma_f32_16x16x32_bf16 v[116:119], v[148:151], v[182:185], v[116:119]
	v_mfma_f32_16x16x32_bf16 v[120:123], v[152:155], v[182:185], v[120:123]
	v_mfma_f32_16x16x32_bf16 v[112:115], v[152:155], v[204:207], v[112:115]
	v_mfma_f32_16x16x32_bf16 v[108:111], v[148:151], v[204:207], v[108:111]
	v_mfma_f32_16x16x32_bf16 v[100:103], v[148:151], v[212:215], v[100:103]
	v_mfma_f32_16x16x32_bf16 v[104:107], v[152:155], v[212:215], v[104:107]
	s_setprio 2
	s_setprio 1
	v_mfma_f32_16x16x32_bf16 v[96:99], v[144:147], v[164:167], 0
	v_mfma_f32_16x16x32_bf16 v[92:95], v[140:143], v[164:167], 0
	v_mfma_f32_16x16x32_bf16 v[84:87], v[140:143], v[178:181], 0
	v_mfma_f32_16x16x32_bf16 v[88:91], v[144:147], v[178:181], 0
	v_mfma_f32_16x16x32_bf16 v[80:83], v[144:147], v[200:203], 0
	v_mfma_f32_16x16x32_bf16 v[76:79], v[140:143], v[200:203], 0
	v_mfma_f32_16x16x32_bf16 v[68:71], v[140:143], v[208:211], 0
	v_mfma_f32_16x16x32_bf16 v[72:75], v[144:147], v[208:211], 0
	s_nop 0
	v_mfma_f32_16x16x32_bf16 v[96:99], v[136:139], v[168:171], v[96:99]
	v_mfma_f32_16x16x32_bf16 v[92:95], v[132:135], v[168:171], v[92:95]
	v_mfma_f32_16x16x32_bf16 v[84:87], v[132:135], v[182:185], v[84:87]
	v_mfma_f32_16x16x32_bf16 v[88:91], v[136:139], v[182:185], v[88:91]
	v_mfma_f32_16x16x32_bf16 v[80:83], v[136:139], v[204:207], v[80:83]
	v_mfma_f32_16x16x32_bf16 v[76:79], v[132:135], v[204:207], v[76:79]
	v_mfma_f32_16x16x32_bf16 v[68:71], v[132:135], v[212:215], v[68:71]
	v_mfma_f32_16x16x32_bf16 v[72:75], v[136:139], v[212:215], v[72:75]
	s_setprio 2
	s_barrier
	v_lshl_add_u64 v[164:165], s[30:31], 0, v[34:35]
	s_add_i32 s64, s64, s42
	v_lshl_add_u64 v[166:167], v[164:165], 0, s[28:29]
	s_mov_b32 m0, s64
	s_add_i32 s65, s64, 0x2000
	ds_read_b128 v[178:181], v223 offset:16384
	ds_read_b128 v[182:185], v223 offset:17408
	ds_read_b128 v[200:203], v223 offset:18432
	ds_read_b128 v[204:207], v223 offset:19456
	ds_read_b128 v[208:211], v223 offset:20480
	ds_read_b128 v[212:215], v223 offset:21504
	ds_read_b128 v[216:219], v223 offset:22528
	ds_read_b128 v[224:227], v223 offset:23552
	global_load_lds_dwordx4 v[166:167], off
	v_lshl_add_u64 v[166:167], s[30:31], 0, v[190:191]
	s_add_u32 s40, s30, 0x40100
	v_lshl_add_u64 v[168:169], v[166:167], 0, s[28:29]
	s_mov_b32 m0, s65
	s_addc_u32 s41, s31, 0
	s_add_i32 s66, s66, s42
	global_load_lds_dwordx4 v[168:169], off
	v_lshl_add_u64 v[168:169], s[40:41], 0, v[34:35]
	s_mov_b32 m0, s66
	s_add_i32 s67, s66, 0x2000
	global_load_lds_dwordx4 v[168:169], off
	v_lshl_add_u64 v[168:169], s[40:41], 0, v[190:191]
	s_mov_b32 m0, s67
	s_nop 0
	global_load_lds_dwordx4 v[168:169], off
	v_lshl_add_u64 v[168:169], s[36:37], 0, v[194:195]
	v_lshl_add_u64 v[170:171], v[168:169], 0, s[28:29]
	s_mov_b32 m0, s43
	s_nop 0
	global_load_lds_dwordx4 v[170:171], off
	v_lshl_add_u64 v[170:171], s[36:37], 0, v[192:193]
	v_lshl_add_u64 v[174:175], v[170:171], 0, s[28:29]
	s_mov_b32 m0, s44
	s_nop 0
	global_load_lds_dwordx4 v[174:175], off
	s_waitcnt vmcnt(8)
	s_waitcnt lgkmcnt(0)
	s_barrier
	s_setprio 1
	s_waitcnt lgkmcnt(0)
	v_mfma_f32_16x16x32_bf16 v[64:67], v[160:163], v[178:181], 0
	v_mfma_f32_16x16x32_bf16 v[60:63], v[156:159], v[178:181], 0
	v_mfma_f32_16x16x32_bf16 v[52:55], v[156:159], v[200:203], 0
	v_mfma_f32_16x16x32_bf16 v[56:59], v[160:163], v[200:203], 0
	v_mfma_f32_16x16x32_bf16 v[48:51], v[160:163], v[208:211], 0
	v_mfma_f32_16x16x32_bf16 v[44:47], v[156:159], v[208:211], 0
	v_mfma_f32_16x16x32_bf16 v[36:39], v[156:159], v[216:219], 0
	v_mfma_f32_16x16x32_bf16 v[40:43], v[160:163], v[216:219], 0
	s_nop 0
	v_mfma_f32_16x16x32_bf16 v[64:67], v[152:155], v[182:185], v[64:67]
	v_mfma_f32_16x16x32_bf16 v[60:63], v[148:151], v[182:185], v[60:63]
	v_mfma_f32_16x16x32_bf16 v[52:55], v[148:151], v[204:207], v[52:55]
	v_mfma_f32_16x16x32_bf16 v[56:59], v[152:155], v[204:207], v[56:59]
	v_mfma_f32_16x16x32_bf16 v[48:51], v[152:155], v[212:215], v[48:51]
	v_mfma_f32_16x16x32_bf16 v[44:47], v[148:151], v[212:215], v[44:47]
	v_mfma_f32_16x16x32_bf16 v[36:39], v[148:151], v[224:227], v[36:39]
	v_mfma_f32_16x16x32_bf16 v[40:43], v[152:155], v[224:227], v[40:43]
	s_setprio 2
	s_setprio 1
	v_mfma_f32_16x16x32_bf16 v[30:33], v[144:147], v[178:181], 0
	v_mfma_f32_16x16x32_bf16 v[26:29], v[140:143], v[178:181], 0
	v_mfma_f32_16x16x32_bf16 v[18:21], v[140:143], v[200:203], 0
	v_mfma_f32_16x16x32_bf16 v[22:25], v[144:147], v[200:203], 0
	v_mfma_f32_16x16x32_bf16 v[14:17], v[144:147], v[208:211], 0
	v_mfma_f32_16x16x32_bf16 v[10:13], v[140:143], v[208:211], 0
	v_mfma_f32_16x16x32_bf16 v[2:5], v[140:143], v[216:219], 0
	v_mfma_f32_16x16x32_bf16 v[6:9], v[144:147], v[216:219], 0
	s_nop 0
	v_mfma_f32_16x16x32_bf16 v[30:33], v[136:139], v[182:185], v[30:33]
	v_mfma_f32_16x16x32_bf16 v[26:29], v[132:135], v[182:185], v[26:29]
	v_mfma_f32_16x16x32_bf16 v[18:21], v[132:135], v[204:207], v[18:21]
	v_mfma_f32_16x16x32_bf16 v[22:25], v[136:139], v[204:207], v[22:25]
	v_mfma_f32_16x16x32_bf16 v[14:17], v[136:139], v[212:215], v[14:17]
	v_mfma_f32_16x16x32_bf16 v[10:13], v[132:135], v[212:215], v[10:13]
	v_mfma_f32_16x16x32_bf16 v[2:5], v[132:135], v[224:227], v[2:5]
	v_mfma_f32_16x16x32_bf16 v[6:9], v[136:139], v[224:227], v[6:9]
	s_setprio 2
	s_barrier
	s_add_i32 s68, 0, 0x18000
	s_add_i32 s70, 0, 0x1c000
	v_add_u32_e32 v132, s68, v222
	v_add_u32_e32 v133, s70, v222
	ds_read_b128 v[134:137], v132
	ds_read_b128 v[138:141], v132 offset:1024
	ds_read_b128 v[142:145], v132 offset:2048
	ds_read_b128 v[146:149], v132 offset:3072
	ds_read_b128 v[150:153], v133
	ds_read_b128 v[154:157], v133 offset:1024
	ds_read_b128 v[158:161], v133 offset:2048
	ds_read_b128 v[178:181], v133 offset:3072
	s_add_u32 s40, s36, 0x40100
	s_addc_u32 s41, s37, 0
	s_mov_b32 m0, s45
	v_lshl_add_u64 v[162:163], s[40:41], 0, v[194:195]
	ds_read_b128 v[182:185], v223 offset:32768
	ds_read_b128 v[200:203], v223 offset:33792
	ds_read_b128 v[204:207], v223 offset:34816
	ds_read_b128 v[208:211], v223 offset:35840
	ds_read_b128 v[212:215], v223 offset:36864
	ds_read_b128 v[216:219], v223 offset:37888
	ds_read_b128 v[224:227], v223 offset:38912
	ds_read_b128 v[228:231], v223 offset:39936
	global_load_lds_dwordx4 v[162:163], off
	v_lshl_add_u64 v[162:163], s[40:41], 0, v[192:193]
	s_mov_b32 m0, s46
	s_nop 0
	global_load_lds_dwordx4 v[162:163], off
	s_waitcnt vmcnt(8)
	s_waitcnt lgkmcnt(0)
	s_barrier
	s_setprio 1
	s_waitcnt lgkmcnt(0)
	v_mfma_f32_16x16x32_bf16 v[128:131], v[134:137], v[182:185], v[128:131]
	v_mfma_f32_16x16x32_bf16 v[124:127], v[142:145], v[182:185], v[124:127]
	v_mfma_f32_16x16x32_bf16 v[116:119], v[142:145], v[204:207], v[116:119]
	v_mfma_f32_16x16x32_bf16 v[120:123], v[134:137], v[204:207], v[120:123]
	v_mfma_f32_16x16x32_bf16 v[112:115], v[134:137], v[212:215], v[112:115]
	v_mfma_f32_16x16x32_bf16 v[108:111], v[142:145], v[212:215], v[108:111]
	v_mfma_f32_16x16x32_bf16 v[100:103], v[142:145], v[224:227], v[100:103]
	v_mfma_f32_16x16x32_bf16 v[104:107], v[134:137], v[224:227], v[104:107]
	v_mfma_f32_16x16x32_bf16 v[128:131], v[138:141], v[200:203], v[128:131]
	v_mfma_f32_16x16x32_bf16 v[124:127], v[146:149], v[200:203], v[124:127]
	v_mfma_f32_16x16x32_bf16 v[116:119], v[146:149], v[208:211], v[116:119]
	v_mfma_f32_16x16x32_bf16 v[120:123], v[138:141], v[208:211], v[120:123]
	v_mfma_f32_16x16x32_bf16 v[112:115], v[138:141], v[216:219], v[112:115]
	v_mfma_f32_16x16x32_bf16 v[108:111], v[146:149], v[216:219], v[108:111]
	v_mfma_f32_16x16x32_bf16 v[100:103], v[146:149], v[228:231], v[100:103]
	v_mfma_f32_16x16x32_bf16 v[104:107], v[138:141], v[228:231], v[104:107]
	s_setprio 2
	s_setprio 1
	v_mfma_f32_16x16x32_bf16 v[96:99], v[150:153], v[182:185], v[96:99]
	v_mfma_f32_16x16x32_bf16 v[92:95], v[158:161], v[182:185], v[92:95]
	v_mfma_f32_16x16x32_bf16 v[84:87], v[158:161], v[204:207], v[84:87]
	v_mfma_f32_16x16x32_bf16 v[88:91], v[150:153], v[204:207], v[88:91]
	v_mfma_f32_16x16x32_bf16 v[80:83], v[150:153], v[212:215], v[80:83]
	v_mfma_f32_16x16x32_bf16 v[76:79], v[158:161], v[212:215], v[76:79]
	v_mfma_f32_16x16x32_bf16 v[68:71], v[158:161], v[224:227], v[68:71]
	v_mfma_f32_16x16x32_bf16 v[72:75], v[150:153], v[224:227], v[72:75]
	v_mfma_f32_16x16x32_bf16 v[96:99], v[154:157], v[200:203], v[96:99]
	v_mfma_f32_16x16x32_bf16 v[92:95], v[178:181], v[200:203], v[92:95]
	v_mfma_f32_16x16x32_bf16 v[84:87], v[178:181], v[208:211], v[84:87]
	v_mfma_f32_16x16x32_bf16 v[88:91], v[154:157], v[208:211], v[88:91]
	v_mfma_f32_16x16x32_bf16 v[80:83], v[154:157], v[216:219], v[80:83]
	v_mfma_f32_16x16x32_bf16 v[76:79], v[178:181], v[216:219], v[76:79]
	v_mfma_f32_16x16x32_bf16 v[68:71], v[178:181], v[228:231], v[68:71]
	v_mfma_f32_16x16x32_bf16 v[72:75], v[154:157], v[228:231], v[72:75]
	s_setprio 2
	s_barrier
	s_add_i32 s68, s68, s42
	s_mov_b64 s[24:25], 0x180
	s_add_i32 s69, s68, 0x2000
	v_lshl_add_u64 v[162:163], v[164:165], 0, s[24:25]
	s_mov_b32 m0, s68
	s_add_u32 s40, s30, 0x40180
	ds_read_b128 v[182:185], v223 offset:49152
	ds_read_b128 v[200:203], v223 offset:50176
	ds_read_b128 v[204:207], v223 offset:51200
	ds_read_b128 v[208:211], v223 offset:52224
	ds_read_b128 v[212:215], v223 offset:53248
	ds_read_b128 v[216:219], v223 offset:54272
	ds_read_b128 v[224:227], v223 offset:55296
	ds_read_b128 v[228:231], v223 offset:56320
	global_load_lds_dwordx4 v[162:163], off
	v_lshl_add_u64 v[162:163], v[166:167], 0, s[24:25]
	s_mov_b32 m0, s69
	s_addc_u32 s41, s31, 0
	s_add_i32 s70, s70, s42
	global_load_lds_dwordx4 v[162:163], off
	v_lshl_add_u64 v[162:163], s[40:41], 0, v[34:35]
	s_mov_b32 m0, s70
	s_add_i32 s71, s70, 0x2000
	global_load_lds_dwordx4 v[162:163], off
	v_lshl_add_u64 v[162:163], s[40:41], 0, v[190:191]
	s_mov_b32 m0, s71
	s_nop 0
	global_load_lds_dwordx4 v[162:163], off
	v_lshl_add_u64 v[162:163], v[168:169], 0, s[24:25]
	s_mov_b32 m0, s51
	s_nop 0
	global_load_lds_dwordx4 v[162:163], off
	v_lshl_add_u64 v[162:163], v[170:171], 0, s[24:25]
	s_mov_b32 m0, s52
	s_nop 0
	global_load_lds_dwordx4 v[162:163], off
	s_waitcnt vmcnt(8)
	s_waitcnt lgkmcnt(0)
	s_barrier
	s_setprio 1
	s_waitcnt lgkmcnt(0)
	v_mfma_f32_16x16x32_bf16 v[64:67], v[134:137], v[182:185], v[64:67]
	v_mfma_f32_16x16x32_bf16 v[60:63], v[142:145], v[182:185], v[60:63]
	v_mfma_f32_16x16x32_bf16 v[52:55], v[142:145], v[204:207], v[52:55]
	v_mfma_f32_16x16x32_bf16 v[56:59], v[134:137], v[204:207], v[56:59]
	v_mfma_f32_16x16x32_bf16 v[48:51], v[134:137], v[212:215], v[48:51]
	v_mfma_f32_16x16x32_bf16 v[44:47], v[142:145], v[212:215], v[44:47]
	v_mfma_f32_16x16x32_bf16 v[36:39], v[142:145], v[224:227], v[36:39]
	v_mfma_f32_16x16x32_bf16 v[40:43], v[134:137], v[224:227], v[40:43]
	v_mfma_f32_16x16x32_bf16 v[64:67], v[138:141], v[200:203], v[64:67]
	v_mfma_f32_16x16x32_bf16 v[60:63], v[146:149], v[200:203], v[60:63]
	v_mfma_f32_16x16x32_bf16 v[52:55], v[146:149], v[208:211], v[52:55]
	v_mfma_f32_16x16x32_bf16 v[56:59], v[138:141], v[208:211], v[56:59]
	v_mfma_f32_16x16x32_bf16 v[48:51], v[138:141], v[216:219], v[48:51]
	v_mfma_f32_16x16x32_bf16 v[44:47], v[146:149], v[216:219], v[44:47]
	v_mfma_f32_16x16x32_bf16 v[36:39], v[146:149], v[228:231], v[36:39]
	v_mfma_f32_16x16x32_bf16 v[40:43], v[138:141], v[228:231], v[40:43]
	s_setprio 2
	s_setprio 1
	v_mfma_f32_16x16x32_bf16 v[30:33], v[150:153], v[182:185], v[30:33]
	v_mfma_f32_16x16x32_bf16 v[26:29], v[158:161], v[182:185], v[26:29]
	v_mfma_f32_16x16x32_bf16 v[18:21], v[158:161], v[204:207], v[18:21]
	v_mfma_f32_16x16x32_bf16 v[22:25], v[150:153], v[204:207], v[22:25]
	v_mfma_f32_16x16x32_bf16 v[14:17], v[150:153], v[212:215], v[14:17]
	v_mfma_f32_16x16x32_bf16 v[10:13], v[158:161], v[212:215], v[10:13]
	v_mfma_f32_16x16x32_bf16 v[2:5], v[158:161], v[224:227], v[2:5]
	v_mfma_f32_16x16x32_bf16 v[6:9], v[150:153], v[224:227], v[6:9]
	v_mfma_f32_16x16x32_bf16 v[30:33], v[154:157], v[200:203], v[30:33]
	v_mfma_f32_16x16x32_bf16 v[26:29], v[178:181], v[200:203], v[26:29]
	v_mfma_f32_16x16x32_bf16 v[18:21], v[178:181], v[208:211], v[18:21]
	v_mfma_f32_16x16x32_bf16 v[22:25], v[154:157], v[208:211], v[22:25]
	v_mfma_f32_16x16x32_bf16 v[14:17], v[154:157], v[216:219], v[14:17]
	v_mfma_f32_16x16x32_bf16 v[10:13], v[178:181], v[216:219], v[10:13]
	v_mfma_f32_16x16x32_bf16 v[2:5], v[178:181], v[228:231], v[2:5]
	v_mfma_f32_16x16x32_bf16 v[6:9], v[154:157], v[228:231], v[6:9]
	s_setprio 2
	s_barrier
	s_add_u32 s36, s36, 0x40180
	s_addc_u32 s37, s37, 0
	s_add_u32 s72, s30, 0x200
	s_addc_u32 s73, s31, 0
	s_mov_b32 s74, 0
.LBB0_541:
	ds_read_b128 v[134:137], v172
	ds_read_b128 v[138:141], v172 offset:1024
	ds_read_b128 v[142:145], v172 offset:2048
	ds_read_b128 v[146:149], v172 offset:3072
	ds_read_b128 v[150:153], v173
	ds_read_b128 v[154:157], v173 offset:1024
	ds_read_b128 v[158:161], v173 offset:2048
	ds_read_b128 v[162:165], v173 offset:3072
	s_add_u32 s14, s36, 0xfffc0080
	s_addc_u32 s30, s37, -1
	s_cmp_eq_u32 s74, 12
	s_cselect_b32 s41, s58, s30
	s_cselect_b32 s40, s59, s14
	s_cselect_b32 s31, s60, s73
	s_cselect_b32 s30, s61, s72
	s_mov_b32 m0, s62
	v_lshl_add_u64 v[170:171], s[36:37], 0, v[196:197]
	ds_read_b128 v[166:169], v223
	ds_read_b128 v[178:181], v223 offset:1024
	ds_read_b128 v[182:185], v223 offset:2048
	ds_read_b128 v[200:203], v223 offset:3072
	ds_read_b128 v[204:207], v223 offset:4096
	ds_read_b128 v[208:211], v223 offset:5120
	ds_read_b128 v[212:215], v223 offset:6144
	ds_read_b128 v[216:219], v223 offset:7168
	global_load_lds_dwordx4 v[170:171], off
	v_lshl_add_u64 v[170:171], s[36:37], 0, v[198:199]
	s_mov_b32 m0, s63
	s_nop 0
	global_load_lds_dwordx4 v[170:171], off
	s_waitcnt vmcnt(8)
	s_waitcnt lgkmcnt(0)
	s_barrier
	s_setprio 1
	s_waitcnt lgkmcnt(0)
	v_mfma_f32_16x16x32_bf16 v[128:131], v[134:137], v[166:169], v[128:131]
	v_mfma_f32_16x16x32_bf16 v[124:127], v[142:145], v[166:169], v[124:127]
	v_mfma_f32_16x16x32_bf16 v[116:119], v[142:145], v[182:185], v[116:119]
	v_mfma_f32_16x16x32_bf16 v[120:123], v[134:137], v[182:185], v[120:123]
	v_mfma_f32_16x16x32_bf16 v[112:115], v[134:137], v[204:207], v[112:115]
	v_mfma_f32_16x16x32_bf16 v[108:111], v[142:145], v[204:207], v[108:111]
	v_mfma_f32_16x16x32_bf16 v[100:103], v[142:145], v[212:215], v[100:103]
	v_mfma_f32_16x16x32_bf16 v[104:107], v[134:137], v[212:215], v[104:107]
	v_mfma_f32_16x16x32_bf16 v[128:131], v[138:141], v[178:181], v[128:131]
	v_mfma_f32_16x16x32_bf16 v[124:127], v[146:149], v[178:181], v[124:127]
	v_mfma_f32_16x16x32_bf16 v[116:119], v[146:149], v[200:203], v[116:119]
	v_mfma_f32_16x16x32_bf16 v[120:123], v[138:141], v[200:203], v[120:123]
	v_mfma_f32_16x16x32_bf16 v[112:115], v[138:141], v[208:211], v[112:115]
	v_mfma_f32_16x16x32_bf16 v[108:111], v[146:149], v[208:211], v[108:111]
	v_mfma_f32_16x16x32_bf16 v[100:103], v[146:149], v[216:219], v[100:103]
	v_mfma_f32_16x16x32_bf16 v[104:107], v[138:141], v[216:219], v[104:107]
	s_setprio 2
	s_setprio 1
	v_mfma_f32_16x16x32_bf16 v[96:99], v[150:153], v[166:169], v[96:99]
	v_mfma_f32_16x16x32_bf16 v[92:95], v[158:161], v[166:169], v[92:95]
	v_mfma_f32_16x16x32_bf16 v[84:87], v[158:161], v[182:185], v[84:87]
	v_mfma_f32_16x16x32_bf16 v[88:91], v[150:153], v[182:185], v[88:91]
	v_mfma_f32_16x16x32_bf16 v[80:83], v[150:153], v[204:207], v[80:83]
	v_mfma_f32_16x16x32_bf16 v[76:79], v[158:161], v[204:207], v[76:79]
	v_mfma_f32_16x16x32_bf16 v[68:71], v[158:161], v[212:215], v[68:71]
	v_mfma_f32_16x16x32_bf16 v[72:75], v[150:153], v[212:215], v[72:75]
	v_mfma_f32_16x16x32_bf16 v[96:99], v[154:157], v[178:181], v[96:99]
	v_mfma_f32_16x16x32_bf16 v[92:95], v[162:165], v[178:181], v[92:95]
	v_mfma_f32_16x16x32_bf16 v[84:87], v[162:165], v[200:203], v[84:87]
	v_mfma_f32_16x16x32_bf16 v[88:91], v[154:157], v[200:203], v[88:91]
	v_mfma_f32_16x16x32_bf16 v[80:83], v[154:157], v[208:211], v[80:83]
	v_mfma_f32_16x16x32_bf16 v[76:79], v[162:165], v[208:211], v[76:79]
	v_mfma_f32_16x16x32_bf16 v[68:71], v[162:165], v[216:219], v[68:71]
	v_mfma_f32_16x16x32_bf16 v[72:75], v[154:157], v[216:219], v[72:75]
	s_setprio 2
	s_barrier
	s_mov_b32 m0, s64
	v_lshl_add_u64 v[170:171], s[30:31], 0, v[34:35]
	s_add_u32 s76, s30, 0x40000
	ds_read_b128 v[166:169], v223 offset:16384
	ds_read_b128 v[178:181], v223 offset:17408
	ds_read_b128 v[182:185], v223 offset:18432
	ds_read_b128 v[200:203], v223 offset:19456
	ds_read_b128 v[204:207], v223 offset:20480
	ds_read_b128 v[208:211], v223 offset:21504
	ds_read_b128 v[212:215], v223 offset:22528
	ds_read_b128 v[216:219], v223 offset:23552
	global_load_lds_dwordx4 v[170:171], off
	v_lshl_add_u64 v[174:175], s[30:31], 0, v[190:191]
	s_mov_b32 m0, s65
	s_addc_u32 s77, s31, 0
	global_load_lds_dwordx4 v[174:175], off
	v_lshl_add_u64 v[224:225], s[76:77], 0, v[34:35]
	s_mov_b32 m0, s66
	v_lshl_add_u64 v[226:227], s[40:41], 0, v[192:193]
	global_load_lds_dwordx4 v[224:225], off
	v_lshl_add_u64 v[224:225], s[76:77], 0, v[190:191]
	s_mov_b32 m0, s67
	s_nop 0
	global_load_lds_dwordx4 v[224:225], off
	v_lshl_add_u64 v[224:225], s[40:41], 0, v[194:195]
	s_mov_b32 m0, s43
	s_nop 0
	global_load_lds_dwordx4 v[224:225], off
	s_mov_b32 m0, s44
	s_nop 0
	global_load_lds_dwordx4 v[226:227], off
	s_waitcnt vmcnt(8)
	s_waitcnt lgkmcnt(0)
	s_barrier
	s_setprio 1
	s_waitcnt lgkmcnt(0)
	v_mfma_f32_16x16x32_bf16 v[64:67], v[134:137], v[166:169], v[64:67]
	v_mfma_f32_16x16x32_bf16 v[60:63], v[142:145], v[166:169], v[60:63]
	v_mfma_f32_16x16x32_bf16 v[52:55], v[142:145], v[182:185], v[52:55]
	v_mfma_f32_16x16x32_bf16 v[56:59], v[134:137], v[182:185], v[56:59]
	v_mfma_f32_16x16x32_bf16 v[48:51], v[134:137], v[204:207], v[48:51]
	v_mfma_f32_16x16x32_bf16 v[44:47], v[142:145], v[204:207], v[44:47]
	v_mfma_f32_16x16x32_bf16 v[36:39], v[142:145], v[212:215], v[36:39]
	v_mfma_f32_16x16x32_bf16 v[40:43], v[134:137], v[212:215], v[40:43]
	v_mfma_f32_16x16x32_bf16 v[64:67], v[138:141], v[178:181], v[64:67]
	v_mfma_f32_16x16x32_bf16 v[60:63], v[146:149], v[178:181], v[60:63]
	v_mfma_f32_16x16x32_bf16 v[52:55], v[146:149], v[200:203], v[52:55]
	v_mfma_f32_16x16x32_bf16 v[56:59], v[138:141], v[200:203], v[56:59]
	v_mfma_f32_16x16x32_bf16 v[48:51], v[138:141], v[208:211], v[48:51]
	v_mfma_f32_16x16x32_bf16 v[44:47], v[146:149], v[208:211], v[44:47]
	v_mfma_f32_16x16x32_bf16 v[36:39], v[146:149], v[216:219], v[36:39]
	v_mfma_f32_16x16x32_bf16 v[40:43], v[138:141], v[216:219], v[40:43]
	s_setprio 2
	s_setprio 1
	v_mfma_f32_16x16x32_bf16 v[30:33], v[150:153], v[166:169], v[30:33]
	v_mfma_f32_16x16x32_bf16 v[26:29], v[158:161], v[166:169], v[26:29]
	v_mfma_f32_16x16x32_bf16 v[18:21], v[158:161], v[182:185], v[18:21]
	v_mfma_f32_16x16x32_bf16 v[22:25], v[150:153], v[182:185], v[22:25]
	v_mfma_f32_16x16x32_bf16 v[14:17], v[150:153], v[204:207], v[14:17]
	v_mfma_f32_16x16x32_bf16 v[10:13], v[158:161], v[204:207], v[10:13]
	v_mfma_f32_16x16x32_bf16 v[2:5], v[158:161], v[212:215], v[2:5]
	v_mfma_f32_16x16x32_bf16 v[6:9], v[150:153], v[212:215], v[6:9]
	v_mfma_f32_16x16x32_bf16 v[30:33], v[154:157], v[178:181], v[30:33]
	v_mfma_f32_16x16x32_bf16 v[26:29], v[162:165], v[178:181], v[26:29]
	v_mfma_f32_16x16x32_bf16 v[18:21], v[162:165], v[200:203], v[18:21]
	v_mfma_f32_16x16x32_bf16 v[22:25], v[154:157], v[200:203], v[22:25]
	v_mfma_f32_16x16x32_bf16 v[14:17], v[154:157], v[208:211], v[14:17]
	v_mfma_f32_16x16x32_bf16 v[10:13], v[162:165], v[208:211], v[10:13]
	v_mfma_f32_16x16x32_bf16 v[2:5], v[162:165], v[216:219], v[2:5]
	v_mfma_f32_16x16x32_bf16 v[6:9], v[154:157], v[216:219], v[6:9]
	s_setprio 2
	s_barrier
	ds_read_b128 v[134:137], v132
	ds_read_b128 v[138:141], v132 offset:1024
	ds_read_b128 v[142:145], v132 offset:2048
	ds_read_b128 v[146:149], v132 offset:3072
	ds_read_b128 v[150:153], v133
	ds_read_b128 v[154:157], v133 offset:1024
	ds_read_b128 v[158:161], v133 offset:2048
	ds_read_b128 v[162:165], v133 offset:3072
	s_add_u32 s40, s40, 0x40000
	s_addc_u32 s41, s41, 0
	s_mov_b32 m0, s45
	v_lshl_add_u64 v[228:229], s[40:41], 0, v[194:195]
	ds_read_b128 v[166:169], v223 offset:32768
	ds_read_b128 v[178:181], v223 offset:33792
	ds_read_b128 v[182:185], v223 offset:34816
	ds_read_b128 v[200:203], v223 offset:35840
	ds_read_b128 v[204:207], v223 offset:36864
	ds_read_b128 v[208:211], v223 offset:37888
	ds_read_b128 v[212:215], v223 offset:38912
	ds_read_b128 v[216:219], v223 offset:39936
	global_load_lds_dwordx4 v[228:229], off
	v_lshl_add_u64 v[228:229], s[40:41], 0, v[192:193]
	s_mov_b32 m0, s46
	s_nop 0
	global_load_lds_dwordx4 v[228:229], off
	s_waitcnt vmcnt(8)
	s_waitcnt lgkmcnt(0)
	s_barrier
	s_setprio 1
	s_waitcnt lgkmcnt(0)
	v_mfma_f32_16x16x32_bf16 v[128:131], v[134:137], v[166:169], v[128:131]
	v_mfma_f32_16x16x32_bf16 v[124:127], v[142:145], v[166:169], v[124:127]
	v_mfma_f32_16x16x32_bf16 v[116:119], v[142:145], v[182:185], v[116:119]
	v_mfma_f32_16x16x32_bf16 v[120:123], v[134:137], v[182:185], v[120:123]
	v_mfma_f32_16x16x32_bf16 v[112:115], v[134:137], v[204:207], v[112:115]
	v_mfma_f32_16x16x32_bf16 v[108:111], v[142:145], v[204:207], v[108:111]
	v_mfma_f32_16x16x32_bf16 v[100:103], v[142:145], v[212:215], v[100:103]
	v_mfma_f32_16x16x32_bf16 v[104:107], v[134:137], v[212:215], v[104:107]
	v_mfma_f32_16x16x32_bf16 v[128:131], v[138:141], v[178:181], v[128:131]
	v_mfma_f32_16x16x32_bf16 v[124:127], v[146:149], v[178:181], v[124:127]
	v_mfma_f32_16x16x32_bf16 v[116:119], v[146:149], v[200:203], v[116:119]
	v_mfma_f32_16x16x32_bf16 v[120:123], v[138:141], v[200:203], v[120:123]
	v_mfma_f32_16x16x32_bf16 v[112:115], v[138:141], v[208:211], v[112:115]
	v_mfma_f32_16x16x32_bf16 v[108:111], v[146:149], v[208:211], v[108:111]
	v_mfma_f32_16x16x32_bf16 v[100:103], v[146:149], v[216:219], v[100:103]
	v_mfma_f32_16x16x32_bf16 v[104:107], v[138:141], v[216:219], v[104:107]
	s_setprio 2
	s_setprio 1
	v_mfma_f32_16x16x32_bf16 v[96:99], v[150:153], v[166:169], v[96:99]
	v_mfma_f32_16x16x32_bf16 v[92:95], v[158:161], v[166:169], v[92:95]
	v_mfma_f32_16x16x32_bf16 v[84:87], v[158:161], v[182:185], v[84:87]
	v_mfma_f32_16x16x32_bf16 v[88:91], v[150:153], v[182:185], v[88:91]
	v_mfma_f32_16x16x32_bf16 v[80:83], v[150:153], v[204:207], v[80:83]
	v_mfma_f32_16x16x32_bf16 v[76:79], v[158:161], v[204:207], v[76:79]
	v_mfma_f32_16x16x32_bf16 v[68:71], v[158:161], v[212:215], v[68:71]
	v_mfma_f32_16x16x32_bf16 v[72:75], v[150:153], v[212:215], v[72:75]
	v_mfma_f32_16x16x32_bf16 v[96:99], v[154:157], v[178:181], v[96:99]
	v_mfma_f32_16x16x32_bf16 v[92:95], v[162:165], v[178:181], v[92:95]
	v_mfma_f32_16x16x32_bf16 v[84:87], v[162:165], v[200:203], v[84:87]
	v_mfma_f32_16x16x32_bf16 v[88:91], v[154:157], v[200:203], v[88:91]
	v_mfma_f32_16x16x32_bf16 v[80:83], v[154:157], v[208:211], v[80:83]
	v_mfma_f32_16x16x32_bf16 v[76:79], v[162:165], v[208:211], v[76:79]
	v_mfma_f32_16x16x32_bf16 v[68:71], v[162:165], v[216:219], v[68:71]
	v_mfma_f32_16x16x32_bf16 v[72:75], v[154:157], v[216:219], v[72:75]
	s_setprio 2
	s_barrier
	s_mov_b32 m0, s68
	v_lshl_add_u64 v[170:171], v[170:171], 0, s[18:19]
	s_add_u32 s30, s30, 0x40080
	ds_read_b128 v[166:169], v223 offset:49152
	ds_read_b128 v[178:181], v223 offset:50176
	ds_read_b128 v[182:185], v223 offset:51200
	ds_read_b128 v[200:203], v223 offset:52224
	ds_read_b128 v[204:207], v223 offset:53248
	ds_read_b128 v[208:211], v223 offset:54272
	ds_read_b128 v[212:215], v223 offset:55296
	ds_read_b128 v[216:219], v223 offset:56320
	global_load_lds_dwordx4 v[170:171], off
	v_lshl_add_u64 v[170:171], v[174:175], 0, s[18:19]
	s_mov_b32 m0, s69
	s_addc_u32 s31, s31, 0
	global_load_lds_dwordx4 v[170:171], off
	v_lshl_add_u64 v[170:171], s[30:31], 0, v[34:35]
	s_mov_b32 m0, s70
	s_nop 0
	global_load_lds_dwordx4 v[170:171], off
	v_lshl_add_u64 v[170:171], s[30:31], 0, v[190:191]
	s_mov_b32 m0, s71
	s_nop 0
	global_load_lds_dwordx4 v[170:171], off
	v_lshl_add_u64 v[170:171], v[224:225], 0, s[18:19]
	s_mov_b32 m0, s51
	s_nop 0
	global_load_lds_dwordx4 v[170:171], off
	v_lshl_add_u64 v[170:171], v[226:227], 0, s[18:19]
	s_mov_b32 m0, s52
	s_nop 0
	global_load_lds_dwordx4 v[170:171], off
	s_waitcnt vmcnt(8)
	s_waitcnt lgkmcnt(0)
	s_barrier
	s_setprio 1
	s_waitcnt lgkmcnt(0)
	v_mfma_f32_16x16x32_bf16 v[64:67], v[134:137], v[166:169], v[64:67]
	v_mfma_f32_16x16x32_bf16 v[60:63], v[142:145], v[166:169], v[60:63]
	v_mfma_f32_16x16x32_bf16 v[52:55], v[142:145], v[182:185], v[52:55]
	v_mfma_f32_16x16x32_bf16 v[56:59], v[134:137], v[182:185], v[56:59]
	v_mfma_f32_16x16x32_bf16 v[48:51], v[134:137], v[204:207], v[48:51]
	v_mfma_f32_16x16x32_bf16 v[44:47], v[142:145], v[204:207], v[44:47]
	v_mfma_f32_16x16x32_bf16 v[36:39], v[142:145], v[212:215], v[36:39]
	v_mfma_f32_16x16x32_bf16 v[40:43], v[134:137], v[212:215], v[40:43]
	v_mfma_f32_16x16x32_bf16 v[64:67], v[138:141], v[178:181], v[64:67]
	v_mfma_f32_16x16x32_bf16 v[60:63], v[146:149], v[178:181], v[60:63]
	v_mfma_f32_16x16x32_bf16 v[52:55], v[146:149], v[200:203], v[52:55]
	v_mfma_f32_16x16x32_bf16 v[56:59], v[138:141], v[200:203], v[56:59]
	v_mfma_f32_16x16x32_bf16 v[48:51], v[138:141], v[208:211], v[48:51]
	v_mfma_f32_16x16x32_bf16 v[44:47], v[146:149], v[208:211], v[44:47]
	v_mfma_f32_16x16x32_bf16 v[36:39], v[146:149], v[216:219], v[36:39]
	v_mfma_f32_16x16x32_bf16 v[40:43], v[138:141], v[216:219], v[40:43]
	s_setprio 2
	s_setprio 1
	v_mfma_f32_16x16x32_bf16 v[30:33], v[150:153], v[166:169], v[30:33]
	v_mfma_f32_16x16x32_bf16 v[26:29], v[158:161], v[166:169], v[26:29]
	v_mfma_f32_16x16x32_bf16 v[18:21], v[158:161], v[182:185], v[18:21]
	v_mfma_f32_16x16x32_bf16 v[22:25], v[150:153], v[182:185], v[22:25]
	v_mfma_f32_16x16x32_bf16 v[14:17], v[150:153], v[204:207], v[14:17]
	v_mfma_f32_16x16x32_bf16 v[10:13], v[158:161], v[204:207], v[10:13]
	v_mfma_f32_16x16x32_bf16 v[2:5], v[158:161], v[212:215], v[2:5]
	v_mfma_f32_16x16x32_bf16 v[6:9], v[150:153], v[212:215], v[6:9]
	v_mfma_f32_16x16x32_bf16 v[30:33], v[154:157], v[178:181], v[30:33]
	v_mfma_f32_16x16x32_bf16 v[26:29], v[162:165], v[178:181], v[26:29]
	v_mfma_f32_16x16x32_bf16 v[18:21], v[162:165], v[200:203], v[18:21]
	v_mfma_f32_16x16x32_bf16 v[22:25], v[154:157], v[200:203], v[22:25]
	v_mfma_f32_16x16x32_bf16 v[14:17], v[154:157], v[208:211], v[14:17]
	v_mfma_f32_16x16x32_bf16 v[10:13], v[162:165], v[208:211], v[10:13]
	v_mfma_f32_16x16x32_bf16 v[2:5], v[162:165], v[216:219], v[2:5]
	v_mfma_f32_16x16x32_bf16 v[6:9], v[154:157], v[216:219], v[6:9]
	s_setprio 2
	s_barrier
	s_add_i32 s74, s74, 2
	s_add_u32 s36, s36, 0x100
	s_addc_u32 s37, s37, 0
	s_add_u32 s72, s72, 0x100
	s_addc_u32 s73, s73, 0
	s_cmp_gt_u32 s74, 13
	s_cbranch_scc0 .LBB0_541
	v_readlane_b32 s74, v255, 3
	s_and_b64 vcc, exec, s[10:11]
	v_readlane_b32 s75, v255, 4
	s_mov_b32 s58, 0x19b00000
	v_readlane_b32 s59, v255, 10
	s_mov_b32 s60, 0xff61b1e6
	s_mov_b64 s[62:63], 0x800
	s_mov_b32 s64, 0x3b000000
	s_cbranch_vccz .LBB0_544
	s_barrier

.LBB0_819:
	s_add_u32 s81, s30, 0x200
	s_addc_u32 s82, s31, 0
	s_add_i32 s55, 0, 0x14000
	s_add_i32 s52, 0, 0x10000
	v_add_u32_e32 v199, s55, v167
	v_add_u32_e32 v200, s52, v167
	ds_read_b128 v[10:13], v199
	ds_read_b128 v[14:17], v199 offset:1024
	ds_read_b128 v[2:5], v199 offset:2048
	ds_read_b128 v[6:9], v199 offset:3072
	ds_read_b128 v[22:25], v200 offset:3072
	ds_read_b128 v[18:21], v200 offset:2048
	ds_read_b128 v[30:33], v200 offset:1024
	ds_read_b128 v[26:29], v200
	s_lshl_b32 s14, s80, 10
	s_add_i32 s83, s14, 0
	s_add_i32 s83, s83, 0x20400
	v_mov_b32_e32 v191, v35
	v_mov_b32_e32 v175, v35
	s_add_i32 s84, s69, 0xc000
	v_readlane_b32 s26, v253, 28
	s_mov_b32 m0, s84
	v_readlane_b32 s27, v253, 29
	s_add_i32 s53, s69, 0xe000
	ds_read_b128 v[202:205], v169
	ds_read_b128 v[206:209], v169 offset:1024
	ds_read_b128 v[222:225], v169 offset:2048
	ds_read_b128 v[226:229], v169 offset:3072
	ds_read_b128 v[230:233], v169 offset:4096
	ds_read_b128 v[234:237], v169 offset:5120
	ds_read_b128 v[238:241], v169 offset:6144
	ds_read_b128 v[242:245], v169 offset:7168
	global_load_lds_dwordx4 v190, s[26:27]
	s_mov_b32 m0, s53
	s_nop 0
	global_load_lds_dwordx4 v174, s[26:27]
	s_waitcnt vmcnt(8)
	s_waitcnt lgkmcnt(0)
	s_barrier
	s_setprio 1
	s_waitcnt lgkmcnt(0)
	v_mfma_f32_16x16x128_f8f6f4 v[160:163], v[26:33], v[202:209], 0
	v_mfma_f32_16x16x128_f8f6f4 v[156:159], v[18:25], v[202:209], 0
	v_mfma_f32_16x16x128_f8f6f4 v[148:151], v[18:25], v[222:229], 0
	v_mfma_f32_16x16x128_f8f6f4 v[152:155], v[26:33], v[222:229], 0
	v_mfma_f32_16x16x128_f8f6f4 v[144:147], v[26:33], v[230:237], 0
	v_mfma_f32_16x16x128_f8f6f4 v[140:143], v[18:25], v[230:237], 0
	v_mfma_f32_16x16x128_f8f6f4 v[132:135], v[18:25], v[238:245], 0
	v_mfma_f32_16x16x128_f8f6f4 v[136:139], v[26:33], v[238:245], 0
	s_setprio 2
	s_setprio 1
	v_mfma_f32_16x16x128_f8f6f4 v[128:131], v[10:17], v[202:209], 0
	v_mfma_f32_16x16x128_f8f6f4 v[124:127], v[2:9], v[202:209], 0
	v_mfma_f32_16x16x128_f8f6f4 v[116:119], v[2:9], v[222:229], 0
	v_mfma_f32_16x16x128_f8f6f4 v[120:123], v[10:17], v[222:229], 0
	v_mfma_f32_16x16x128_f8f6f4 v[112:115], v[10:17], v[230:237], 0
	v_mfma_f32_16x16x128_f8f6f4 v[108:111], v[2:9], v[230:237], 0
	v_mfma_f32_16x16x128_f8f6f4 v[100:103], v[2:9], v[238:245], 0
	v_mfma_f32_16x16x128_f8f6f4 v[104:107], v[10:17], v[238:245], 0
	s_setprio 2
	s_barrier
	s_add_i32 s52, s52, s68
	v_lshl_add_u64 v[194:195], s[30:31], 0, v[170:171]
	s_add_i32 s85, s52, 0x2000
	v_lshl_add_u64 v[178:179], v[194:195], 0, s[28:29]
	s_mov_b32 m0, s52
	v_lshl_add_u64 v[196:197], s[30:31], 0, v[172:173]
	s_add_u32 s36, s30, 0x20100
	ds_read_b128 v[202:205], v169 offset:16384
	ds_read_b128 v[206:209], v169 offset:17408
	ds_read_b128 v[222:225], v169 offset:18432
	ds_read_b128 v[226:229], v169 offset:19456
	ds_read_b128 v[230:233], v169 offset:20480
	ds_read_b128 v[234:237], v169 offset:21504
	ds_read_b128 v[238:241], v169 offset:22528
	ds_read_b128 v[242:245], v169 offset:23552
	global_load_lds_dwordx4 v[178:179], off
	v_lshl_add_u64 v[178:179], v[196:197], 0, s[28:29]
	s_mov_b32 m0, s85
	s_addc_u32 s37, s31, 0
	s_add_i32 s55, s55, s68
	global_load_lds_dwordx4 v[178:179], off
	v_lshl_add_u64 v[178:179], s[36:37], 0, v[170:171]
	s_mov_b32 m0, s55
	s_add_i32 s65, s55, 0x2000
	global_load_lds_dwordx4 v[178:179], off
	v_lshl_add_u64 v[178:179], s[36:37], 0, v[172:173]
	s_mov_b32 m0, s65
	v_readlane_b32 s26, v253, 37
	global_load_lds_dwordx4 v[178:179], off
	s_mov_b32 m0, s69
	v_readlane_b32 s27, v253, 38
	s_nop 4
	global_load_lds_dwordx4 v34, s[26:27]
	s_mov_b32 m0, s70
	s_nop 0
	global_load_lds_dwordx4 v192, s[26:27]
	s_waitcnt vmcnt(8)
	s_waitcnt lgkmcnt(0)
	s_barrier
	s_setprio 1
	s_waitcnt lgkmcnt(0)
	v_mfma_f32_16x16x128_f8f6f4 v[96:99], v[26:33], v[202:209], 0
	v_mfma_f32_16x16x128_f8f6f4 v[92:95], v[18:25], v[202:209], 0
	v_mfma_f32_16x16x128_f8f6f4 v[84:87], v[18:25], v[222:229], 0
	v_mfma_f32_16x16x128_f8f6f4 v[88:91], v[26:33], v[222:229], 0
	v_mfma_f32_16x16x128_f8f6f4 v[80:83], v[26:33], v[230:237], 0
	v_mfma_f32_16x16x128_f8f6f4 v[76:79], v[18:25], v[230:237], 0
	v_mfma_f32_16x16x128_f8f6f4 v[68:71], v[18:25], v[238:245], 0
	v_mfma_f32_16x16x128_f8f6f4 v[72:75], v[26:33], v[238:245], 0
	s_setprio 2
	s_setprio 1
	v_mfma_f32_16x16x128_f8f6f4 v[64:67], v[10:17], v[202:209], 0
	v_mfma_f32_16x16x128_f8f6f4 v[60:63], v[2:9], v[202:209], 0
	v_mfma_f32_16x16x128_f8f6f4 v[52:55], v[2:9], v[222:229], 0
	v_mfma_f32_16x16x128_f8f6f4 v[56:59], v[10:17], v[222:229], 0
	v_mfma_f32_16x16x128_f8f6f4 v[48:51], v[10:17], v[230:237], 0
	v_mfma_f32_16x16x128_f8f6f4 v[44:47], v[2:9], v[230:237], 0
	v_mfma_f32_16x16x128_f8f6f4 v[36:39], v[2:9], v[238:245], 0
	v_mfma_f32_16x16x128_f8f6f4 v[40:43], v[10:17], v[238:245], 0
	s_setprio 2
	s_barrier
	s_add_i32 s54, 0, 0x18000
	s_add_i32 s51, 0, 0x1c000
	v_add_u32_e32 v201, s54, v167
	v_add_u32_e32 v202, s51, v167
	ds_read_b128 v[26:29], v201
	ds_read_b128 v[30:33], v201 offset:1024
	ds_read_b128 v[18:21], v201 offset:2048
	ds_read_b128 v[22:25], v201 offset:3072
	ds_read_b128 v[10:13], v202
	ds_read_b128 v[14:17], v202 offset:1024
	ds_read_b128 v[2:5], v202 offset:2048
	ds_read_b128 v[6:9], v202 offset:3072
	s_mov_b32 m0, s71
	ds_read_b128 v[204:207], v169 offset:32768
	ds_read_b128 v[208:211], v169 offset:33792
	ds_read_b128 v[222:225], v169 offset:34816
	ds_read_b128 v[226:229], v169 offset:35840
	ds_read_b128 v[230:233], v169 offset:36864
	ds_read_b128 v[234:237], v169 offset:37888
	ds_read_b128 v[238:241], v169 offset:38912
	ds_read_b128 v[242:245], v169 offset:39936
	global_load_lds_dwordx4 v189, s[26:27]
	s_mov_b32 m0, s72
	s_nop 0
	global_load_lds_dwordx4 v198, s[26:27]
	s_waitcnt vmcnt(8)
	s_waitcnt lgkmcnt(0)
	s_barrier
	s_setprio 1
	s_waitcnt lgkmcnt(0)
	v_mfma_f32_16x16x128_f8f6f4 v[160:163], v[26:33], v[204:211], v[160:163]
	v_mfma_f32_16x16x128_f8f6f4 v[156:159], v[18:25], v[204:211], v[156:159]
	v_mfma_f32_16x16x128_f8f6f4 v[148:151], v[18:25], v[222:229], v[148:151]
	v_mfma_f32_16x16x128_f8f6f4 v[152:155], v[26:33], v[222:229], v[152:155]
	v_mfma_f32_16x16x128_f8f6f4 v[144:147], v[26:33], v[230:237], v[144:147]
	v_mfma_f32_16x16x128_f8f6f4 v[140:143], v[18:25], v[230:237], v[140:143]
	v_mfma_f32_16x16x128_f8f6f4 v[132:135], v[18:25], v[238:245], v[132:135]
	v_mfma_f32_16x16x128_f8f6f4 v[136:139], v[26:33], v[238:245], v[136:139]
	s_setprio 2
	s_setprio 1
	v_mfma_f32_16x16x128_f8f6f4 v[128:131], v[10:17], v[204:211], v[128:131]
	v_mfma_f32_16x16x128_f8f6f4 v[124:127], v[2:9], v[204:211], v[124:127]
	v_mfma_f32_16x16x128_f8f6f4 v[116:119], v[2:9], v[222:229], v[116:119]
	v_mfma_f32_16x16x128_f8f6f4 v[120:123], v[10:17], v[222:229], v[120:123]
	v_mfma_f32_16x16x128_f8f6f4 v[112:115], v[10:17], v[230:237], v[112:115]
	v_mfma_f32_16x16x128_f8f6f4 v[108:111], v[2:9], v[230:237], v[108:111]
	v_mfma_f32_16x16x128_f8f6f4 v[100:103], v[2:9], v[238:245], v[100:103]
	v_mfma_f32_16x16x128_f8f6f4 v[104:107], v[10:17], v[238:245], v[104:107]
	s_setprio 2
	s_barrier
	s_add_i32 s54, s54, s68
	s_mov_b64 s[26:27], 0x180
	s_add_i32 s50, s54, 0x2000
	v_lshl_add_u64 v[178:179], v[194:195], 0, s[26:27]
	s_mov_b32 m0, s54
	s_add_u32 s30, s30, 0x20180
	ds_read_b128 v[204:207], v169 offset:49152
	ds_read_b128 v[208:211], v169 offset:50176
	ds_read_b128 v[222:225], v169 offset:51200
	ds_read_b128 v[226:229], v169 offset:52224
	ds_read_b128 v[230:233], v169 offset:53248
	ds_read_b128 v[234:237], v169 offset:54272
	ds_read_b128 v[238:241], v169 offset:55296
	ds_read_b128 v[242:245], v169 offset:56320
	global_load_lds_dwordx4 v[178:179], off
	v_lshl_add_u64 v[178:179], v[196:197], 0, s[26:27]
	s_mov_b32 m0, s50
	s_addc_u32 s31, s31, 0
	s_add_i32 s51, s51, s68
	global_load_lds_dwordx4 v[178:179], off
	v_lshl_add_u64 v[178:179], s[30:31], 0, v[170:171]
	s_mov_b32 m0, s51
	s_add_i32 s64, s51, 0x2000
	global_load_lds_dwordx4 v[178:179], off
	v_lshl_add_u64 v[178:179], s[30:31], 0, v[172:173]
	s_mov_b32 m0, s64
	v_readlane_b32 s26, v253, 39
	global_load_lds_dwordx4 v[178:179], off
	s_mov_b32 m0, s75
	v_readlane_b32 s27, v253, 40
	s_nop 4
	global_load_lds_dwordx4 v34, s[26:27]
	s_mov_b32 m0, s76
	s_nop 0
	global_load_lds_dwordx4 v192, s[26:27]
	s_waitcnt vmcnt(8)
	s_waitcnt lgkmcnt(0)
	s_barrier
	s_setprio 1
	s_waitcnt lgkmcnt(0)
	v_mfma_f32_16x16x128_f8f6f4 v[96:99], v[26:33], v[204:211], v[96:99]
	v_mfma_f32_16x16x128_f8f6f4 v[92:95], v[18:25], v[204:211], v[92:95]
	v_mfma_f32_16x16x128_f8f6f4 v[84:87], v[18:25], v[222:229], v[84:87]
	v_mfma_f32_16x16x128_f8f6f4 v[88:91], v[26:33], v[222:229], v[88:91]
	v_mfma_f32_16x16x128_f8f6f4 v[80:83], v[26:33], v[230:237], v[80:83]
	v_mfma_f32_16x16x128_f8f6f4 v[76:79], v[18:25], v[230:237], v[76:79]
	v_mfma_f32_16x16x128_f8f6f4 v[68:71], v[18:25], v[238:245], v[68:71]
	v_mfma_f32_16x16x128_f8f6f4 v[72:75], v[26:33], v[238:245], v[72:75]
	s_setprio 2
	s_setprio 1
	v_mfma_f32_16x16x128_f8f6f4 v[64:67], v[10:17], v[204:211], v[64:67]
	v_mfma_f32_16x16x128_f8f6f4 v[60:63], v[2:9], v[204:211], v[60:63]
	v_mfma_f32_16x16x128_f8f6f4 v[52:55], v[2:9], v[222:229], v[52:55]
	v_mfma_f32_16x16x128_f8f6f4 v[56:59], v[10:17], v[222:229], v[56:59]
	v_mfma_f32_16x16x128_f8f6f4 v[48:51], v[10:17], v[230:237], v[48:51]
	v_mfma_f32_16x16x128_f8f6f4 v[44:47], v[2:9], v[230:237], v[44:47]
	v_mfma_f32_16x16x128_f8f6f4 v[36:39], v[2:9], v[238:245], v[36:39]
	v_mfma_f32_16x16x128_f8f6f4 v[40:43], v[10:17], v[238:245], v[40:43]
	s_setprio 2
	s_barrier
	v_lshl_add_u64 v[18:19], s[26:27], 0, v[174:175]
	v_lshl_add_u64 v[20:21], s[26:27], 0, v[190:191]
	s_mov_b32 s63, 0
	s_mov_b64 s[30:31], 0
	s_branch .LBB0_821
.LBB0_820:
	ds_read_b128 v[204:207], v200
	ds_read_b128 v[208:211], v200 offset:1024
	ds_read_b128 v[222:225], v200 offset:2048
	ds_read_b128 v[226:229], v200 offset:3072
	ds_read_b128 v[10:13], v199
	ds_read_b128 v[14:17], v199 offset:1024
	ds_read_b128 v[2:5], v199 offset:2048
	ds_read_b128 v[6:9], v199 offset:3072
	s_add_u32 s14, s30, 0x200
	s_addc_u32 s86, s31, 0
	s_and_b64 s[40:41], s[36:37], exec
	s_cselect_b32 s14, 0, s14
	s_cselect_b32 s41, 0, s86
	s_add_u32 s40, s20, s14
	s_addc_u32 s41, s21, s41
	s_add_u32 s14, s81, s30
	s_addc_u32 s86, s82, s31
	s_and_b64 s[36:37], s[36:37], exec
	s_cselect_b32 s37, s23, s86
	s_cselect_b32 s36, s22, s14
	s_mov_b32 m0, s84
	v_lshl_add_u64 v[30:31], v[20:21], 0, s[30:31]
	ds_read_b128 v[22:25], v169
	ds_read_b128 v[26:29], v169 offset:1024
	ds_read_b128 v[230:233], v169 offset:2048
	ds_read_b128 v[234:237], v169 offset:3072
	ds_read_b128 v[238:241], v169 offset:4096
	ds_read_b128 v[242:245], v169 offset:5120
	ds_read_b128 v[178:181], v169 offset:6144
	ds_read_b128 v[182:185], v169 offset:7168
	global_load_lds_dwordx4 v[30:31], off
	v_lshl_add_u64 v[30:31], v[18:19], 0, s[30:31]
	s_mov_b32 m0, s53
	s_nop 0
	global_load_lds_dwordx4 v[30:31], off
	s_waitcnt vmcnt(8)
	s_waitcnt lgkmcnt(0)
	s_barrier
	s_setprio 1
	s_waitcnt lgkmcnt(0)
	v_mfma_f32_16x16x128_f8f6f4 v[160:163], v[204:211], v[22:29], v[160:163]
	v_mfma_f32_16x16x128_f8f6f4 v[156:159], v[222:229], v[22:29], v[156:159]
	v_mfma_f32_16x16x128_f8f6f4 v[148:151], v[222:229], v[230:237], v[148:151]
	v_mfma_f32_16x16x128_f8f6f4 v[152:155], v[204:211], v[230:237], v[152:155]
	v_mfma_f32_16x16x128_f8f6f4 v[144:147], v[204:211], v[238:245], v[144:147]
	v_mfma_f32_16x16x128_f8f6f4 v[140:143], v[222:229], v[238:245], v[140:143]
	v_mfma_f32_16x16x128_f8f6f4 v[132:135], v[222:229], v[178:185], v[132:135]
	v_mfma_f32_16x16x128_f8f6f4 v[136:139], v[204:211], v[178:185], v[136:139]
	s_setprio 2
	s_setprio 1
	v_mfma_f32_16x16x128_f8f6f4 v[128:131], v[10:17], v[22:29], v[128:131]
	v_mfma_f32_16x16x128_f8f6f4 v[124:127], v[2:9], v[22:29], v[124:127]
	v_mfma_f32_16x16x128_f8f6f4 v[116:119], v[2:9], v[230:237], v[116:119]
	v_mfma_f32_16x16x128_f8f6f4 v[120:123], v[10:17], v[230:237], v[120:123]
	v_mfma_f32_16x16x128_f8f6f4 v[112:115], v[10:17], v[238:245], v[112:115]
	v_mfma_f32_16x16x128_f8f6f4 v[108:111], v[2:9], v[238:245], v[108:111]
	v_mfma_f32_16x16x128_f8f6f4 v[100:103], v[2:9], v[178:185], v[100:103]
	v_mfma_f32_16x16x128_f8f6f4 v[104:107], v[10:17], v[178:185], v[104:107]
	s_setprio 2
	s_barrier
	s_mov_b32 m0, s52
	v_lshl_add_u64 v[22:23], s[36:37], 0, v[170:171]
	s_add_u32 s86, s36, 0x20000
	ds_read_b128 v[178:181], v169 offset:16384
	ds_read_b128 v[182:185], v169 offset:17408
	ds_read_b128 v[230:233], v169 offset:18432
	ds_read_b128 v[234:237], v169 offset:19456
	ds_read_b128 v[238:241], v169 offset:20480
	ds_read_b128 v[242:245], v169 offset:21504
	ds_read_b128 v[212:215], v169 offset:22528
	ds_read_b128 v[216:219], v169 offset:23552
	global_load_lds_dwordx4 v[22:23], off
	v_lshl_add_u64 v[24:25], s[36:37], 0, v[172:173]
	s_mov_b32 m0, s85
	s_addc_u32 s87, s37, 0
	global_load_lds_dwordx4 v[24:25], off
	v_lshl_add_u64 v[26:27], s[86:87], 0, v[170:171]
	s_mov_b32 m0, s55
	v_mov_b32_e32 v193, v35
	global_load_lds_dwordx4 v[26:27], off
	v_lshl_add_u64 v[26:27], s[86:87], 0, v[172:173]
	s_mov_b32 m0, s65
	v_lshl_add_u64 v[28:29], s[40:41], 0, v[34:35]
	global_load_lds_dwordx4 v[26:27], off
	s_mov_b32 m0, s69
	v_lshl_add_u64 v[26:27], s[40:41], 0, v[192:193]
	global_load_lds_dwordx4 v34, s[40:41]
	s_mov_b32 m0, s70
	s_nop 0
	global_load_lds_dwordx4 v192, s[40:41]
	s_waitcnt vmcnt(8)
	s_waitcnt lgkmcnt(0)
	s_barrier
	s_setprio 1
	s_waitcnt lgkmcnt(0)
	v_mfma_f32_16x16x128_f8f6f4 v[96:99], v[204:211], v[178:185], v[96:99]
	v_mfma_f32_16x16x128_f8f6f4 v[92:95], v[222:229], v[178:185], v[92:95]
	v_mfma_f32_16x16x128_f8f6f4 v[84:87], v[222:229], v[230:237], v[84:87]
	v_mfma_f32_16x16x128_f8f6f4 v[88:91], v[204:211], v[230:237], v[88:91]
	v_mfma_f32_16x16x128_f8f6f4 v[80:83], v[204:211], v[238:245], v[80:83]
	v_mfma_f32_16x16x128_f8f6f4 v[76:79], v[222:229], v[238:245], v[76:79]
	v_mfma_f32_16x16x128_f8f6f4 v[68:71], v[222:229], v[212:219], v[68:71]
	v_mfma_f32_16x16x128_f8f6f4 v[72:75], v[204:211], v[212:219], v[72:75]
	s_setprio 2
	s_setprio 1
	v_mfma_f32_16x16x128_f8f6f4 v[64:67], v[10:17], v[178:185], v[64:67]
	v_mfma_f32_16x16x128_f8f6f4 v[60:63], v[2:9], v[178:185], v[60:63]
	v_mfma_f32_16x16x128_f8f6f4 v[52:55], v[2:9], v[230:237], v[52:55]
	v_mfma_f32_16x16x128_f8f6f4 v[56:59], v[10:17], v[230:237], v[56:59]
	v_mfma_f32_16x16x128_f8f6f4 v[48:51], v[10:17], v[238:245], v[48:51]
	v_mfma_f32_16x16x128_f8f6f4 v[44:47], v[2:9], v[238:245], v[44:47]
	v_mfma_f32_16x16x128_f8f6f4 v[36:39], v[2:9], v[212:219], v[36:39]
	v_mfma_f32_16x16x128_f8f6f4 v[40:43], v[10:17], v[212:219], v[40:43]
	s_setprio 2
	s_barrier
	ds_read_b128 v[178:181], v201
	ds_read_b128 v[182:185], v201 offset:1024
	ds_read_b128 v[204:207], v201 offset:2048
	ds_read_b128 v[208:211], v201 offset:3072
	ds_read_b128 v[10:13], v202
	ds_read_b128 v[14:17], v202 offset:1024
	ds_read_b128 v[2:5], v202 offset:2048
	ds_read_b128 v[6:9], v202 offset:3072
	s_mov_b32 m0, s71
	ds_read_b128 v[212:215], v169 offset:32768
	ds_read_b128 v[216:219], v169 offset:33792
	ds_read_b128 v[222:225], v169 offset:34816
	ds_read_b128 v[226:229], v169 offset:35840
	ds_read_b128 v[230:233], v169 offset:36864
	ds_read_b128 v[234:237], v169 offset:37888
	ds_read_b128 v[238:241], v169 offset:38912
	ds_read_b128 v[242:245], v169 offset:39936
	global_load_lds_dwordx4 v189, s[40:41]
	s_mov_b32 m0, s72
	s_nop 0
	global_load_lds_dwordx4 v198, s[40:41]
	s_waitcnt vmcnt(8)
	s_waitcnt lgkmcnt(0)
	s_barrier
	s_setprio 1
	s_waitcnt lgkmcnt(0)
	v_mfma_f32_16x16x128_f8f6f4 v[160:163], v[178:185], v[212:219], v[160:163]
	v_mfma_f32_16x16x128_f8f6f4 v[156:159], v[204:211], v[212:219], v[156:159]
	v_mfma_f32_16x16x128_f8f6f4 v[148:151], v[204:211], v[222:229], v[148:151]
	v_mfma_f32_16x16x128_f8f6f4 v[152:155], v[178:185], v[222:229], v[152:155]
	v_mfma_f32_16x16x128_f8f6f4 v[144:147], v[178:185], v[230:237], v[144:147]
	v_mfma_f32_16x16x128_f8f6f4 v[140:143], v[204:211], v[230:237], v[140:143]
	v_mfma_f32_16x16x128_f8f6f4 v[132:135], v[204:211], v[238:245], v[132:135]
	v_mfma_f32_16x16x128_f8f6f4 v[136:139], v[178:185], v[238:245], v[136:139]
	s_setprio 2
	s_setprio 1
	v_mfma_f32_16x16x128_f8f6f4 v[128:131], v[10:17], v[212:219], v[128:131]
	v_mfma_f32_16x16x128_f8f6f4 v[124:127], v[2:9], v[212:219], v[124:127]
	v_mfma_f32_16x16x128_f8f6f4 v[116:119], v[2:9], v[222:229], v[116:119]
	v_mfma_f32_16x16x128_f8f6f4 v[120:123], v[10:17], v[222:229], v[120:123]
	v_mfma_f32_16x16x128_f8f6f4 v[112:115], v[10:17], v[230:237], v[112:115]
	v_mfma_f32_16x16x128_f8f6f4 v[108:111], v[2:9], v[230:237], v[108:111]
	v_mfma_f32_16x16x128_f8f6f4 v[100:103], v[2:9], v[238:245], v[100:103]
	v_mfma_f32_16x16x128_f8f6f4 v[104:107], v[10:17], v[238:245], v[104:107]
	s_setprio 2
	s_barrier
	s_mov_b32 m0, s54
	v_lshl_add_u64 v[22:23], v[22:23], 0, s[18:19]
	s_add_u32 s36, s36, 0x20080
	ds_read_b128 v[212:215], v169 offset:49152
	ds_read_b128 v[216:219], v169 offset:50176
	ds_read_b128 v[222:225], v169 offset:51200
	ds_read_b128 v[226:229], v169 offset:52224
	ds_read_b128 v[230:233], v169 offset:53248
	ds_read_b128 v[234:237], v169 offset:54272
	ds_read_b128 v[238:241], v169 offset:55296
	ds_read_b128 v[242:245], v169 offset:56320
	global_load_lds_dwordx4 v[22:23], off
	v_lshl_add_u64 v[22:23], v[24:25], 0, s[18:19]
	s_mov_b32 m0, s50
	s_addc_u32 s37, s37, 0
	global_load_lds_dwordx4 v[22:23], off
	v_lshl_add_u64 v[22:23], s[36:37], 0, v[170:171]
	s_mov_b32 m0, s51
	s_nop 0
	global_load_lds_dwordx4 v[22:23], off
	v_lshl_add_u64 v[22:23], s[36:37], 0, v[172:173]
	s_mov_b32 m0, s64
	s_nop 0
	global_load_lds_dwordx4 v[22:23], off
	v_lshl_add_u64 v[22:23], v[28:29], 0, s[18:19]
	s_mov_b32 m0, s75
	s_nop 0
	global_load_lds_dwordx4 v[22:23], off
	v_lshl_add_u64 v[22:23], v[26:27], 0, s[18:19]
	s_mov_b32 m0, s76
	s_nop 0
	global_load_lds_dwordx4 v[22:23], off
	s_waitcnt vmcnt(8)
	s_waitcnt lgkmcnt(0)
	s_barrier
	s_setprio 1
	s_waitcnt lgkmcnt(0)
	v_mfma_f32_16x16x128_f8f6f4 v[96:99], v[178:185], v[212:219], v[96:99]
	v_mfma_f32_16x16x128_f8f6f4 v[92:95], v[204:211], v[212:219], v[92:95]
	v_mfma_f32_16x16x128_f8f6f4 v[84:87], v[204:211], v[222:229], v[84:87]
	v_mfma_f32_16x16x128_f8f6f4 v[88:91], v[178:185], v[222:229], v[88:91]
	v_mfma_f32_16x16x128_f8f6f4 v[80:83], v[178:185], v[230:237], v[80:83]
	v_mfma_f32_16x16x128_f8f6f4 v[76:79], v[204:211], v[230:237], v[76:79]
	v_mfma_f32_16x16x128_f8f6f4 v[68:71], v[204:211], v[238:245], v[68:71]
	v_mfma_f32_16x16x128_f8f6f4 v[72:75], v[178:185], v[238:245], v[72:75]
	s_setprio 2
	s_setprio 1
	v_mfma_f32_16x16x128_f8f6f4 v[64:67], v[10:17], v[212:219], v[64:67]
	v_mfma_f32_16x16x128_f8f6f4 v[60:63], v[2:9], v[212:219], v[60:63]
	v_mfma_f32_16x16x128_f8f6f4 v[52:55], v[2:9], v[222:229], v[52:55]
	v_mfma_f32_16x16x128_f8f6f4 v[56:59], v[10:17], v[222:229], v[56:59]
	v_mfma_f32_16x16x128_f8f6f4 v[48:51], v[10:17], v[230:237], v[48:51]
	v_mfma_f32_16x16x128_f8f6f4 v[44:47], v[2:9], v[230:237], v[44:47]
	v_mfma_f32_16x16x128_f8f6f4 v[36:39], v[2:9], v[238:245], v[36:39]
	v_mfma_f32_16x16x128_f8f6f4 v[40:43], v[10:17], v[238:245], v[40:43]
	s_setprio 2
	s_barrier
	s_add_i32 s63, s63, 2
	s_add_u32 s30, s30, 0x100
	s_addc_u32 s31, s31, 0
	s_cmp_gt_u32 s63, 5
	s_cbranch_scc1 .LBB0_823

.LBB0_899:
	s_mul_i32 s14, s81, 0xe0000
	s_add_u32 s40, s44, s14
	s_addc_u32 s41, s45, 0
	s_and_b64 s[6:7], s[6:7], exec
	s_cselect_b32 s52, s41, s43
	s_cselect_b32 s53, s40, s42
	s_add_i32 s54, 0, 0x10000
	s_add_i32 s65, 0, 0x14000
	v_add_u32_e32 v34, s54, v167
	v_add_u32_e32 v206, s65, v167
	ds_read_b128 v[26:29], v34
	ds_read_b128 v[30:33], v34 offset:1024
	ds_read_b128 v[18:21], v34 offset:2048
	ds_read_b128 v[22:25], v34 offset:3072
	ds_read_b128 v[10:13], v206
	ds_read_b128 v[14:17], v206 offset:1024
	ds_read_b128 v[2:5], v206 offset:2048
	ds_read_b128 v[6:9], v206 offset:3072
	s_add_u32 s6, s42, 0x70080
	s_addc_u32 s7, s43, 0
	s_add_i32 s84, s72, 0xc000
	v_lshl_add_u64 v[216:217], s[6:7], 0, v[174:175]
	s_mov_b32 m0, s84
	s_add_i32 s85, s72, 0xe000
	ds_read_b128 v[178:181], v189
	ds_read_b128 v[182:185], v189 offset:1024
	ds_read_b128 v[198:201], v189 offset:2048
	ds_read_b128 v[202:205], v189 offset:3072
	ds_read_b128 v[208:211], v189 offset:4096
	ds_read_b128 v[212:215], v189 offset:5120
	ds_read_b128 v[222:225], v189 offset:6144
	ds_read_b128 v[226:229], v189 offset:7168
	global_load_lds_dwordx4 v[216:217], off
	v_lshl_add_u64 v[216:217], s[6:7], 0, v[170:171]
	s_mov_b32 m0, s85
	s_nop 0
	global_load_lds_dwordx4 v[216:217], off
	s_waitcnt vmcnt(8)
	s_waitcnt lgkmcnt(0)
	s_barrier
	s_setprio 1
	s_waitcnt lgkmcnt(0)
	v_mfma_f32_16x16x128_f8f6f4 v[160:163], v[26:33], v[178:185], 0
	v_mfma_f32_16x16x128_f8f6f4 v[156:159], v[18:25], v[178:185], 0
	v_mfma_f32_16x16x128_f8f6f4 v[148:151], v[18:25], v[198:205], 0
	v_mfma_f32_16x16x128_f8f6f4 v[152:155], v[26:33], v[198:205], 0
	v_mfma_f32_16x16x128_f8f6f4 v[144:147], v[26:33], v[208:215], 0
	v_mfma_f32_16x16x128_f8f6f4 v[140:143], v[18:25], v[208:215], 0
	v_mfma_f32_16x16x128_f8f6f4 v[132:135], v[18:25], v[222:229], 0
	v_mfma_f32_16x16x128_f8f6f4 v[136:139], v[26:33], v[222:229], 0
	s_setprio 2
	s_setprio 1
	v_mfma_f32_16x16x128_f8f6f4 v[128:131], v[10:17], v[178:185], 0
	v_mfma_f32_16x16x128_f8f6f4 v[124:127], v[2:9], v[178:185], 0
	v_mfma_f32_16x16x128_f8f6f4 v[116:119], v[2:9], v[198:205], 0
	v_mfma_f32_16x16x128_f8f6f4 v[120:123], v[10:17], v[198:205], 0
	v_mfma_f32_16x16x128_f8f6f4 v[112:115], v[10:17], v[208:215], 0
	v_mfma_f32_16x16x128_f8f6f4 v[108:111], v[2:9], v[208:215], 0
	v_mfma_f32_16x16x128_f8f6f4 v[100:103], v[2:9], v[222:229], 0
	v_mfma_f32_16x16x128_f8f6f4 v[104:107], v[10:17], v[222:229], 0
	s_setprio 2
	s_barrier
	v_lshl_add_u64 v[198:199], v[196:197], 0, v[172:173]
	s_add_i32 s54, s54, s71
	v_lshl_add_u64 v[200:201], v[198:199], 0, s[28:29]
	s_mov_b32 m0, s54
	ds_read_b128 v[178:181], v189 offset:16384
	ds_read_b128 v[182:185], v189 offset:17408
	ds_read_b128 v[208:211], v189 offset:18432
	ds_read_b128 v[212:215], v189 offset:19456
	ds_read_b128 v[222:225], v189 offset:20480
	ds_read_b128 v[226:229], v189 offset:21504
	ds_read_b128 v[230:233], v189 offset:22528
	ds_read_b128 v[234:237], v189 offset:23552
	global_load_lds_dwordx4 v[200:201], off
	v_lshl_add_u64 v[200:201], v[196:197], 0, v[168:169]
	s_add_i32 s55, s54, 0x2000
	v_lshl_add_u64 v[202:203], v[200:201], 0, s[28:29]
	s_mov_b32 m0, s55
	s_mov_b64 s[6:7], 0x70100
	global_load_lds_dwordx4 v[202:203], off
	v_lshl_add_u64 v[202:203], v[196:197], 0, s[6:7]
	s_add_i32 s65, s65, s71
	v_lshl_add_u64 v[204:205], v[202:203], 0, v[172:173]
	s_mov_b32 m0, s65
	s_add_i32 s67, s65, 0x2000
	global_load_lds_dwordx4 v[204:205], off
	v_lshl_add_u64 v[202:203], v[202:203], 0, v[168:169]
	s_mov_b32 m0, s67
	s_nop 0
	global_load_lds_dwordx4 v[202:203], off
	v_lshl_add_u64 v[202:203], s[42:43], 0, v[174:175]
	v_lshl_add_u64 v[204:205], v[202:203], 0, s[28:29]
	s_mov_b32 m0, s72
	s_nop 0
	global_load_lds_dwordx4 v[204:205], off
	v_lshl_add_u64 v[204:205], s[42:43], 0, v[170:171]
	v_lshl_add_u64 v[216:217], v[204:205], 0, s[28:29]
	s_mov_b32 m0, s73
	s_nop 0
	global_load_lds_dwordx4 v[216:217], off
	s_waitcnt vmcnt(8)
	s_waitcnt lgkmcnt(0)
	s_barrier
	s_setprio 1
	s_waitcnt lgkmcnt(0)
	v_mfma_f32_16x16x128_f8f6f4 v[96:99], v[26:33], v[178:185], 0
	v_mfma_f32_16x16x128_f8f6f4 v[92:95], v[18:25], v[178:185], 0
	v_mfma_f32_16x16x128_f8f6f4 v[84:87], v[18:25], v[208:215], 0
	v_mfma_f32_16x16x128_f8f6f4 v[88:91], v[26:33], v[208:215], 0
	v_mfma_f32_16x16x128_f8f6f4 v[80:83], v[26:33], v[222:229], 0
	v_mfma_f32_16x16x128_f8f6f4 v[76:79], v[18:25], v[222:229], 0
	v_mfma_f32_16x16x128_f8f6f4 v[68:71], v[18:25], v[230:237], 0
	v_mfma_f32_16x16x128_f8f6f4 v[72:75], v[26:33], v[230:237], 0
	s_setprio 2
	s_setprio 1
	v_mfma_f32_16x16x128_f8f6f4 v[64:67], v[10:17], v[178:185], 0
	v_mfma_f32_16x16x128_f8f6f4 v[60:63], v[2:9], v[178:185], 0
	v_mfma_f32_16x16x128_f8f6f4 v[52:55], v[2:9], v[208:215], 0
	v_mfma_f32_16x16x128_f8f6f4 v[56:59], v[10:17], v[208:215], 0
	v_mfma_f32_16x16x128_f8f6f4 v[48:51], v[10:17], v[222:229], 0
	v_mfma_f32_16x16x128_f8f6f4 v[44:47], v[2:9], v[222:229], 0
	v_mfma_f32_16x16x128_f8f6f4 v[36:39], v[2:9], v[230:237], 0
	v_mfma_f32_16x16x128_f8f6f4 v[40:43], v[10:17], v[230:237], 0
	s_setprio 2
	s_barrier
	s_add_i32 s50, 0, 0x18000
	s_add_i32 s63, 0, 0x1c000
	v_add_u32_e32 v207, s50, v167
	v_add_u32_e32 v208, s63, v167
	ds_read_b128 v[26:29], v207
	ds_read_b128 v[30:33], v207 offset:1024
	ds_read_b128 v[18:21], v207 offset:2048
	ds_read_b128 v[22:25], v207 offset:3072
	ds_read_b128 v[10:13], v208
	ds_read_b128 v[14:17], v208 offset:1024
	ds_read_b128 v[2:5], v208 offset:2048
	ds_read_b128 v[6:9], v208 offset:3072
	s_add_u32 s6, s42, 0x70100
	s_addc_u32 s7, s43, 0
	s_mov_b32 m0, s74
	v_lshl_add_u64 v[218:219], s[6:7], 0, v[174:175]
	ds_read_b128 v[178:181], v189 offset:32768
	ds_read_b128 v[182:185], v189 offset:33792
	ds_read_b128 v[210:213], v189 offset:34816
	ds_read_b128 v[214:217], v189 offset:35840
	ds_read_b128 v[222:225], v189 offset:36864
	ds_read_b128 v[226:229], v189 offset:37888
	ds_read_b128 v[230:233], v189 offset:38912
	ds_read_b128 v[234:237], v189 offset:39936
	global_load_lds_dwordx4 v[218:219], off
	v_lshl_add_u64 v[218:219], s[6:7], 0, v[170:171]
	s_mov_b32 m0, s75
	s_nop 0
	global_load_lds_dwordx4 v[218:219], off
	s_waitcnt vmcnt(8)
	s_waitcnt lgkmcnt(0)
	s_barrier
	s_setprio 1
	s_waitcnt lgkmcnt(0)
	v_mfma_f32_16x16x128_f8f6f4 v[160:163], v[26:33], v[178:185], v[160:163]
	v_mfma_f32_16x16x128_f8f6f4 v[156:159], v[18:25], v[178:185], v[156:159]
	v_mfma_f32_16x16x128_f8f6f4 v[148:151], v[18:25], v[210:217], v[148:151]
	v_mfma_f32_16x16x128_f8f6f4 v[152:155], v[26:33], v[210:217], v[152:155]
	v_mfma_f32_16x16x128_f8f6f4 v[144:147], v[26:33], v[222:229], v[144:147]
	v_mfma_f32_16x16x128_f8f6f4 v[140:143], v[18:25], v[222:229], v[140:143]
	v_mfma_f32_16x16x128_f8f6f4 v[132:135], v[18:25], v[230:237], v[132:135]
	v_mfma_f32_16x16x128_f8f6f4 v[136:139], v[26:33], v[230:237], v[136:139]
	s_setprio 2
	s_setprio 1
	v_mfma_f32_16x16x128_f8f6f4 v[128:131], v[10:17], v[178:185], v[128:131]
	v_mfma_f32_16x16x128_f8f6f4 v[124:127], v[2:9], v[178:185], v[124:127]
	v_mfma_f32_16x16x128_f8f6f4 v[116:119], v[2:9], v[210:217], v[116:119]
	v_mfma_f32_16x16x128_f8f6f4 v[120:123], v[10:17], v[210:217], v[120:123]
	v_mfma_f32_16x16x128_f8f6f4 v[112:115], v[10:17], v[222:229], v[112:115]
	v_mfma_f32_16x16x128_f8f6f4 v[108:111], v[2:9], v[222:229], v[108:111]
	v_mfma_f32_16x16x128_f8f6f4 v[100:103], v[2:9], v[230:237], v[100:103]
	v_mfma_f32_16x16x128_f8f6f4 v[104:107], v[10:17], v[230:237], v[104:107]
	s_setprio 2
	s_barrier
	s_mov_b64 s[6:7], 0x180
	s_add_i32 s50, s50, s71
	v_lshl_add_u64 v[198:199], v[198:199], 0, s[6:7]
	s_mov_b32 m0, s50
	s_add_i32 s51, s50, 0x2000
	ds_read_b128 v[178:181], v189 offset:49152
	ds_read_b128 v[182:185], v189 offset:50176
	ds_read_b128 v[210:213], v189 offset:51200
	ds_read_b128 v[214:217], v189 offset:52224
	ds_read_b128 v[222:225], v189 offset:53248
	ds_read_b128 v[226:229], v189 offset:54272
	ds_read_b128 v[230:233], v189 offset:55296
	ds_read_b128 v[234:237], v189 offset:56320
	global_load_lds_dwordx4 v[198:199], off
	v_lshl_add_u64 v[198:199], v[200:201], 0, s[6:7]
	s_mov_b32 m0, s51
	s_add_i32 s63, s63, s71
	global_load_lds_dwordx4 v[198:199], off
	v_lshl_add_u64 v[198:199], v[196:197], 0, s[26:27]
	v_lshl_add_u64 v[200:201], v[198:199], 0, v[172:173]
	s_mov_b32 m0, s63
	s_add_i32 s64, s63, 0x2000
	global_load_lds_dwordx4 v[200:201], off
	v_lshl_add_u64 v[198:199], v[198:199], 0, v[168:169]
	s_mov_b32 m0, s64
	s_nop 0
	global_load_lds_dwordx4 v[198:199], off
	v_lshl_add_u64 v[198:199], v[202:203], 0, s[6:7]
	s_mov_b32 m0, s77
	s_nop 0
	global_load_lds_dwordx4 v[198:199], off
	v_lshl_add_u64 v[198:199], v[204:205], 0, s[6:7]
	s_mov_b32 m0, s78
	s_nop 0
	global_load_lds_dwordx4 v[198:199], off
	s_waitcnt vmcnt(8)
	s_waitcnt lgkmcnt(0)
	s_barrier
	s_setprio 1
	s_waitcnt lgkmcnt(0)
	v_mfma_f32_16x16x128_f8f6f4 v[96:99], v[26:33], v[178:185], v[96:99]
	v_mfma_f32_16x16x128_f8f6f4 v[92:95], v[18:25], v[178:185], v[92:95]
	v_mfma_f32_16x16x128_f8f6f4 v[84:87], v[18:25], v[210:217], v[84:87]
	v_mfma_f32_16x16x128_f8f6f4 v[88:91], v[26:33], v[210:217], v[88:91]
	v_mfma_f32_16x16x128_f8f6f4 v[80:83], v[26:33], v[222:229], v[80:83]
	v_mfma_f32_16x16x128_f8f6f4 v[76:79], v[18:25], v[222:229], v[76:79]
	v_mfma_f32_16x16x128_f8f6f4 v[68:71], v[18:25], v[230:237], v[68:71]
	v_mfma_f32_16x16x128_f8f6f4 v[72:75], v[26:33], v[230:237], v[72:75]
	s_setprio 2
	s_setprio 1
	v_mfma_f32_16x16x128_f8f6f4 v[64:67], v[10:17], v[178:185], v[64:67]
	v_mfma_f32_16x16x128_f8f6f4 v[60:63], v[2:9], v[178:185], v[60:63]
	v_mfma_f32_16x16x128_f8f6f4 v[52:55], v[2:9], v[210:217], v[52:55]
	v_mfma_f32_16x16x128_f8f6f4 v[56:59], v[10:17], v[210:217], v[56:59]
	v_mfma_f32_16x16x128_f8f6f4 v[48:51], v[10:17], v[222:229], v[48:51]
	v_mfma_f32_16x16x128_f8f6f4 v[44:47], v[2:9], v[222:229], v[44:47]
	v_mfma_f32_16x16x128_f8f6f4 v[36:39], v[2:9], v[230:237], v[36:39]
	v_mfma_f32_16x16x128_f8f6f4 v[40:43], v[10:17], v[230:237], v[40:43]
	s_setprio 2
	s_barrier
	s_mov_b64 s[6:7], 0x200
	v_lshl_add_u64 v[18:19], v[196:197], 0, s[6:7]
	s_mov_b32 s86, 0
.LBB0_900:
	ds_read_b128 v[2:5], v34
	ds_read_b128 v[6:9], v34 offset:1024
	ds_read_b128 v[10:13], v34 offset:2048
	ds_read_b128 v[14:17], v34 offset:3072
	ds_read_b128 v[178:181], v206
	ds_read_b128 v[182:185], v206 offset:1024
	ds_read_b128 v[196:199], v206 offset:2048
	ds_read_b128 v[200:203], v206 offset:3072
	s_add_u32 s6, s42, 0x200
	s_addc_u32 s7, s43, 0
	s_cmp_eq_u32 s86, 24
	s_cselect_b64 vcc, -1, 0
	s_cselect_b32 s7, s52, s7
	s_cselect_b32 s6, s53, s6
	v_cndmask_b32_e32 v21, v19, v195, vcc
	v_cndmask_b32_e32 v20, v18, v194, vcc
	s_mov_b32 m0, s84
	v_lshl_add_u64 v[30:31], s[42:43], 0, v[190:191]
	ds_read_b128 v[22:25], v189
	ds_read_b128 v[26:29], v189 offset:1024
	ds_read_b128 v[210:213], v189 offset:2048
	ds_read_b128 v[214:217], v189 offset:3072
	ds_read_b128 v[222:225], v189 offset:4096
	ds_read_b128 v[226:229], v189 offset:5120
	ds_read_b128 v[230:233], v189 offset:6144
	ds_read_b128 v[234:237], v189 offset:7168
	global_load_lds_dwordx4 v[30:31], off
	v_lshl_add_u64 v[30:31], s[42:43], 0, v[192:193]
	s_mov_b32 m0, s85
	s_nop 0
	global_load_lds_dwordx4 v[30:31], off
	s_waitcnt vmcnt(8)
	s_waitcnt lgkmcnt(0)
	s_barrier
	s_setprio 1
	s_waitcnt lgkmcnt(0)
	v_mfma_f32_16x16x128_f8f6f4 v[160:163], v[2:9], v[22:29], v[160:163]
	v_mfma_f32_16x16x128_f8f6f4 v[156:159], v[10:17], v[22:29], v[156:159]
	v_mfma_f32_16x16x128_f8f6f4 v[148:151], v[10:17], v[210:217], v[148:151]
	v_mfma_f32_16x16x128_f8f6f4 v[152:155], v[2:9], v[210:217], v[152:155]
	v_mfma_f32_16x16x128_f8f6f4 v[144:147], v[2:9], v[222:229], v[144:147]
	v_mfma_f32_16x16x128_f8f6f4 v[140:143], v[10:17], v[222:229], v[140:143]
	v_mfma_f32_16x16x128_f8f6f4 v[132:135], v[10:17], v[230:237], v[132:135]
	v_mfma_f32_16x16x128_f8f6f4 v[136:139], v[2:9], v[230:237], v[136:139]
	s_setprio 2
	s_setprio 1
	v_mfma_f32_16x16x128_f8f6f4 v[128:131], v[178:185], v[22:29], v[128:131]
	v_mfma_f32_16x16x128_f8f6f4 v[124:127], v[196:203], v[22:29], v[124:127]
	v_mfma_f32_16x16x128_f8f6f4 v[116:119], v[196:203], v[210:217], v[116:119]
	v_mfma_f32_16x16x128_f8f6f4 v[120:123], v[178:185], v[210:217], v[120:123]
	v_mfma_f32_16x16x128_f8f6f4 v[112:115], v[178:185], v[222:229], v[112:115]
	v_mfma_f32_16x16x128_f8f6f4 v[108:111], v[196:203], v[222:229], v[108:111]
	v_mfma_f32_16x16x128_f8f6f4 v[100:103], v[196:203], v[230:237], v[100:103]
	v_mfma_f32_16x16x128_f8f6f4 v[104:107], v[178:185], v[230:237], v[104:107]
	s_setprio 2
	s_barrier
	s_mov_b32 m0, s54
	v_lshl_add_u64 v[22:23], v[20:21], 0, v[172:173]
	ds_read_b128 v[210:213], v189 offset:16384
	ds_read_b128 v[214:217], v189 offset:17408
	ds_read_b128 v[222:225], v189 offset:18432
	ds_read_b128 v[226:229], v189 offset:19456
	ds_read_b128 v[230:233], v189 offset:20480
	ds_read_b128 v[234:237], v189 offset:21504
	ds_read_b128 v[238:241], v189 offset:22528
	ds_read_b128 v[242:245], v189 offset:23552
	global_load_lds_dwordx4 v[22:23], off
	v_lshl_add_u64 v[24:25], v[20:21], 0, v[168:169]
	s_mov_b32 m0, s55
	v_lshl_add_u64 v[26:27], v[20:21], 0, s[2:3]
	global_load_lds_dwordx4 v[24:25], off
	v_lshl_add_u64 v[28:29], v[26:27], 0, v[172:173]
	s_mov_b32 m0, s65
	v_lshl_add_u64 v[26:27], v[26:27], 0, v[168:169]
	global_load_lds_dwordx4 v[28:29], off
	s_mov_b32 m0, s67
	v_lshl_add_u64 v[28:29], s[6:7], 0, v[170:171]
	global_load_lds_dwordx4 v[26:27], off
	v_lshl_add_u64 v[26:27], s[6:7], 0, v[174:175]
	s_mov_b32 m0, s72
	s_nop 0
	global_load_lds_dwordx4 v[26:27], off
	s_mov_b32 m0, s73
	s_nop 0
	global_load_lds_dwordx4 v[28:29], off
	s_waitcnt vmcnt(8)
	s_waitcnt lgkmcnt(0)
	s_barrier
	s_setprio 1
	s_waitcnt lgkmcnt(0)
	v_mfma_f32_16x16x128_f8f6f4 v[96:99], v[2:9], v[210:217], v[96:99]
	v_mfma_f32_16x16x128_f8f6f4 v[92:95], v[10:17], v[210:217], v[92:95]
	v_mfma_f32_16x16x128_f8f6f4 v[84:87], v[10:17], v[222:229], v[84:87]
	v_mfma_f32_16x16x128_f8f6f4 v[88:91], v[2:9], v[222:229], v[88:91]
	v_mfma_f32_16x16x128_f8f6f4 v[80:83], v[2:9], v[230:237], v[80:83]
	v_mfma_f32_16x16x128_f8f6f4 v[76:79], v[10:17], v[230:237], v[76:79]
	v_mfma_f32_16x16x128_f8f6f4 v[68:71], v[10:17], v[238:245], v[68:71]
	v_mfma_f32_16x16x128_f8f6f4 v[72:75], v[2:9], v[238:245], v[72:75]
	s_setprio 2
	s_setprio 1
	v_mfma_f32_16x16x128_f8f6f4 v[64:67], v[178:185], v[210:217], v[64:67]
	v_mfma_f32_16x16x128_f8f6f4 v[60:63], v[196:203], v[210:217], v[60:63]
	v_mfma_f32_16x16x128_f8f6f4 v[52:55], v[196:203], v[222:229], v[52:55]
	v_mfma_f32_16x16x128_f8f6f4 v[56:59], v[178:185], v[222:229], v[56:59]
	v_mfma_f32_16x16x128_f8f6f4 v[48:51], v[178:185], v[230:237], v[48:51]
	v_mfma_f32_16x16x128_f8f6f4 v[44:47], v[196:203], v[230:237], v[44:47]
	v_mfma_f32_16x16x128_f8f6f4 v[36:39], v[196:203], v[238:245], v[36:39]
	v_mfma_f32_16x16x128_f8f6f4 v[40:43], v[178:185], v[238:245], v[40:43]
	s_setprio 2
	s_barrier
	ds_read_b128 v[178:181], v207
	ds_read_b128 v[182:185], v207 offset:1024
	ds_read_b128 v[196:199], v207 offset:2048
	ds_read_b128 v[200:203], v207 offset:3072
	ds_read_b128 v[10:13], v208
	ds_read_b128 v[14:17], v208 offset:1024
	ds_read_b128 v[2:5], v208 offset:2048
	ds_read_b128 v[6:9], v208 offset:3072
	s_add_u32 s6, s6, 0x70000
	s_addc_u32 s7, s7, 0
	s_mov_b32 m0, s74
	v_lshl_add_u64 v[30:31], s[6:7], 0, v[174:175]
	ds_read_b128 v[210:213], v189 offset:32768
	ds_read_b128 v[214:217], v189 offset:33792
	ds_read_b128 v[222:225], v189 offset:34816
	ds_read_b128 v[226:229], v189 offset:35840
	ds_read_b128 v[230:233], v189 offset:36864
	ds_read_b128 v[234:237], v189 offset:37888
	ds_read_b128 v[238:241], v189 offset:38912
	ds_read_b128 v[242:245], v189 offset:39936
	global_load_lds_dwordx4 v[30:31], off
	v_lshl_add_u64 v[30:31], s[6:7], 0, v[170:171]
	s_mov_b32 m0, s75
	s_nop 0
	global_load_lds_dwordx4 v[30:31], off
	s_waitcnt vmcnt(8)
	s_waitcnt lgkmcnt(0)
	s_barrier
	s_setprio 1
	s_waitcnt lgkmcnt(0)
	v_mfma_f32_16x16x128_f8f6f4 v[160:163], v[178:185], v[210:217], v[160:163]
	v_mfma_f32_16x16x128_f8f6f4 v[156:159], v[196:203], v[210:217], v[156:159]
	v_mfma_f32_16x16x128_f8f6f4 v[148:151], v[196:203], v[222:229], v[148:151]
	v_mfma_f32_16x16x128_f8f6f4 v[152:155], v[178:185], v[222:229], v[152:155]
	v_mfma_f32_16x16x128_f8f6f4 v[144:147], v[178:185], v[230:237], v[144:147]
	v_mfma_f32_16x16x128_f8f6f4 v[140:143], v[196:203], v[230:237], v[140:143]
	v_mfma_f32_16x16x128_f8f6f4 v[132:135], v[196:203], v[238:245], v[132:135]
	v_mfma_f32_16x16x128_f8f6f4 v[136:139], v[178:185], v[238:245], v[136:139]
	s_setprio 2
	s_setprio 1
	v_mfma_f32_16x16x128_f8f6f4 v[128:131], v[10:17], v[210:217], v[128:131]
	v_mfma_f32_16x16x128_f8f6f4 v[124:127], v[2:9], v[210:217], v[124:127]
	v_mfma_f32_16x16x128_f8f6f4 v[116:119], v[2:9], v[222:229], v[116:119]
	v_mfma_f32_16x16x128_f8f6f4 v[120:123], v[10:17], v[222:229], v[120:123]
	v_mfma_f32_16x16x128_f8f6f4 v[112:115], v[10:17], v[230:237], v[112:115]
	v_mfma_f32_16x16x128_f8f6f4 v[108:111], v[2:9], v[230:237], v[108:111]
	v_mfma_f32_16x16x128_f8f6f4 v[100:103], v[2:9], v[238:245], v[100:103]
	v_mfma_f32_16x16x128_f8f6f4 v[104:107], v[10:17], v[238:245], v[104:107]
	s_setprio 2
	s_barrier
	s_mov_b32 m0, s50
	v_lshl_add_u64 v[22:23], v[22:23], 0, s[18:19]
	ds_read_b128 v[210:213], v189 offset:49152
	ds_read_b128 v[214:217], v189 offset:50176
	ds_read_b128 v[222:225], v189 offset:51200
	ds_read_b128 v[226:229], v189 offset:52224
	ds_read_b128 v[230:233], v189 offset:53248
	ds_read_b128 v[234:237], v189 offset:54272
	ds_read_b128 v[238:241], v189 offset:55296
	ds_read_b128 v[242:245], v189 offset:56320
	global_load_lds_dwordx4 v[22:23], off
	v_lshl_add_u64 v[22:23], v[24:25], 0, s[18:19]
	s_mov_b32 m0, s51
	v_lshl_add_u64 v[20:21], v[20:21], 0, s[34:35]
	global_load_lds_dwordx4 v[22:23], off
	v_lshl_add_u64 v[22:23], v[20:21], 0, v[172:173]
	s_mov_b32 m0, s63
	v_lshl_add_u64 v[20:21], v[20:21], 0, v[168:169]
	global_load_lds_dwordx4 v[22:23], off
	s_mov_b32 m0, s64
	s_nop 0
	global_load_lds_dwordx4 v[20:21], off
	v_lshl_add_u64 v[20:21], v[26:27], 0, s[18:19]
	s_mov_b32 m0, s77
	s_nop 0
	global_load_lds_dwordx4 v[20:21], off
	v_lshl_add_u64 v[20:21], v[28:29], 0, s[18:19]
	s_mov_b32 m0, s78
	s_nop 0
	global_load_lds_dwordx4 v[20:21], off
	s_waitcnt vmcnt(8)
	s_waitcnt lgkmcnt(0)
	s_barrier
	s_setprio 1
	s_waitcnt lgkmcnt(0)
	v_mfma_f32_16x16x128_f8f6f4 v[96:99], v[178:185], v[210:217], v[96:99]
	v_mfma_f32_16x16x128_f8f6f4 v[92:95], v[196:203], v[210:217], v[92:95]
	v_mfma_f32_16x16x128_f8f6f4 v[84:87], v[196:203], v[222:229], v[84:87]
	v_mfma_f32_16x16x128_f8f6f4 v[88:91], v[178:185], v[222:229], v[88:91]
	v_mfma_f32_16x16x128_f8f6f4 v[80:83], v[178:185], v[230:237], v[80:83]
	v_mfma_f32_16x16x128_f8f6f4 v[76:79], v[196:203], v[230:237], v[76:79]
	v_mfma_f32_16x16x128_f8f6f4 v[68:71], v[196:203], v[238:245], v[68:71]
	v_mfma_f32_16x16x128_f8f6f4 v[72:75], v[178:185], v[238:245], v[72:75]
	s_setprio 2
	s_setprio 1
	v_mfma_f32_16x16x128_f8f6f4 v[64:67], v[10:17], v[210:217], v[64:67]
	v_mfma_f32_16x16x128_f8f6f4 v[60:63], v[2:9], v[210:217], v[60:63]
	v_mfma_f32_16x16x128_f8f6f4 v[52:55], v[2:9], v[222:229], v[52:55]
	v_mfma_f32_16x16x128_f8f6f4 v[56:59], v[10:17], v[222:229], v[56:59]
	v_mfma_f32_16x16x128_f8f6f4 v[48:51], v[10:17], v[230:237], v[48:51]
	v_mfma_f32_16x16x128_f8f6f4 v[44:47], v[2:9], v[230:237], v[44:47]
	v_mfma_f32_16x16x128_f8f6f4 v[36:39], v[2:9], v[238:245], v[36:39]
	v_mfma_f32_16x16x128_f8f6f4 v[40:43], v[10:17], v[238:245], v[40:43]
	s_setprio 2
	s_barrier
	s_add_i32 s86, s86, 2
	s_add_u32 s42, s42, 0x100
	s_addc_u32 s43, s43, 0
	s_cmp_gt_u32 s86, 25
	v_lshl_add_u64 v[18:19], v[18:19], 0, s[28:29]
	s_cbranch_scc0 .LBB0_900
	s_and_b64 vcc, exec, s[36:37]
	s_mov_b64 s[84:85], s[24:25]
	s_cbranch_vccz .LBB0_903
	s_barrier

.LBB0_953:
	s_add_u32 s95, s30, 0x200
	s_addc_u32 s96, s31, 0
	s_add_i32 s65, 0, 0x14000
	s_add_i32 s67, 0, 0x10000
	v_add_u32_e32 v199, s65, v167
	v_add_u32_e32 v200, s67, v167
	ds_read_b128 v[10:13], v199
	ds_read_b128 v[14:17], v199 offset:1024
	ds_read_b128 v[2:5], v199 offset:2048
	ds_read_b128 v[6:9], v199 offset:3072
	ds_read_b128 v[22:25], v200 offset:3072
	ds_read_b128 v[18:21], v200 offset:2048
	ds_read_b128 v[30:33], v200 offset:1024
	ds_read_b128 v[26:29], v200
	s_lshl_b32 s14, s94, 10
	s_add_i32 s97, s14, 0
	s_add_i32 s97, s97, 0x20400
	v_mov_b32_e32 v191, v35
	v_mov_b32_e32 v175, v35
	s_add_i32 s83, s52, 0xc000
	v_readlane_b32 s26, v253, 28
	s_mov_b32 m0, s83
	v_readlane_b32 s27, v253, 29
	s_add_i32 s53, s52, 0xe000
	ds_read_b128 v[178:181], v169
	ds_read_b128 v[182:185], v169 offset:1024
	ds_read_b128 v[202:205], v169 offset:2048
	ds_read_b128 v[206:209], v169 offset:3072
	ds_read_b128 v[210:213], v169 offset:4096
	ds_read_b128 v[214:217], v169 offset:5120
	ds_read_b128 v[222:225], v169 offset:6144
	ds_read_b128 v[226:229], v169 offset:7168
	global_load_lds_dwordx4 v190, s[26:27]
	s_mov_b32 m0, s53
	s_nop 0
	global_load_lds_dwordx4 v174, s[26:27]
	s_waitcnt vmcnt(8)
	s_waitcnt lgkmcnt(0)
	s_barrier
	s_setprio 1
	s_waitcnt lgkmcnt(0)
	v_mfma_f32_16x16x128_f8f6f4 v[160:163], v[26:33], v[178:185], 0
	v_mfma_f32_16x16x128_f8f6f4 v[156:159], v[18:25], v[178:185], 0
	v_mfma_f32_16x16x128_f8f6f4 v[148:151], v[18:25], v[202:209], 0
	v_mfma_f32_16x16x128_f8f6f4 v[152:155], v[26:33], v[202:209], 0
	v_mfma_f32_16x16x128_f8f6f4 v[144:147], v[26:33], v[210:217], 0
	v_mfma_f32_16x16x128_f8f6f4 v[140:143], v[18:25], v[210:217], 0
	v_mfma_f32_16x16x128_f8f6f4 v[132:135], v[18:25], v[222:229], 0
	v_mfma_f32_16x16x128_f8f6f4 v[136:139], v[26:33], v[222:229], 0
	s_setprio 2
	s_setprio 1
	v_mfma_f32_16x16x128_f8f6f4 v[128:131], v[10:17], v[178:185], 0
	v_mfma_f32_16x16x128_f8f6f4 v[124:127], v[2:9], v[178:185], 0
	v_mfma_f32_16x16x128_f8f6f4 v[116:119], v[2:9], v[202:209], 0
	v_mfma_f32_16x16x128_f8f6f4 v[120:123], v[10:17], v[202:209], 0
	v_mfma_f32_16x16x128_f8f6f4 v[112:115], v[10:17], v[210:217], 0
	v_mfma_f32_16x16x128_f8f6f4 v[108:111], v[2:9], v[210:217], 0
	v_mfma_f32_16x16x128_f8f6f4 v[100:103], v[2:9], v[222:229], 0
	v_mfma_f32_16x16x128_f8f6f4 v[104:107], v[10:17], v[222:229], 0
	s_setprio 2
	s_barrier
	v_lshl_add_u64 v[194:195], s[30:31], 0, v[170:171]
	s_add_i32 s67, s67, s82
	v_lshl_add_u64 v[196:197], v[194:195], 0, s[28:29]
	s_mov_b32 m0, s67
	s_add_i32 s55, s67, 0x2000
	ds_read_b128 v[178:181], v169 offset:16384
	ds_read_b128 v[182:185], v169 offset:17408
	ds_read_b128 v[202:205], v169 offset:18432
	ds_read_b128 v[206:209], v169 offset:19456
	ds_read_b128 v[210:213], v169 offset:20480
	ds_read_b128 v[214:217], v169 offset:21504
	ds_read_b128 v[222:225], v169 offset:22528
	ds_read_b128 v[226:229], v169 offset:23552
	global_load_lds_dwordx4 v[196:197], off
	v_lshl_add_u64 v[196:197], s[30:31], 0, v[172:173]
	s_add_u32 s46, s30, 0x20100
	v_lshl_add_u64 v[218:219], v[196:197], 0, s[28:29]
	s_mov_b32 m0, s55
	s_addc_u32 s47, s31, 0
	s_add_i32 s65, s65, s82
	global_load_lds_dwordx4 v[218:219], off
	v_lshl_add_u64 v[218:219], s[46:47], 0, v[170:171]
	s_mov_b32 m0, s65
	s_add_i32 s54, s65, 0x2000
	global_load_lds_dwordx4 v[218:219], off
	v_lshl_add_u64 v[218:219], s[46:47], 0, v[172:173]
	s_mov_b32 m0, s54
	v_readlane_b32 s26, v253, 37
	global_load_lds_dwordx4 v[218:219], off
	s_mov_b32 m0, s52
	v_readlane_b32 s27, v253, 38
	s_nop 4
	global_load_lds_dwordx4 v34, s[26:27]
	s_mov_b32 m0, s84
	s_nop 0
	global_load_lds_dwordx4 v192, s[26:27]
	s_waitcnt vmcnt(8)
	s_waitcnt lgkmcnt(0)
	s_barrier
	s_setprio 1
	s_waitcnt lgkmcnt(0)
	v_mfma_f32_16x16x128_f8f6f4 v[96:99], v[26:33], v[178:185], 0
	v_mfma_f32_16x16x128_f8f6f4 v[92:95], v[18:25], v[178:185], 0
	v_mfma_f32_16x16x128_f8f6f4 v[84:87], v[18:25], v[202:209], 0
	v_mfma_f32_16x16x128_f8f6f4 v[88:91], v[26:33], v[202:209], 0
	v_mfma_f32_16x16x128_f8f6f4 v[80:83], v[26:33], v[210:217], 0
	v_mfma_f32_16x16x128_f8f6f4 v[76:79], v[18:25], v[210:217], 0
	v_mfma_f32_16x16x128_f8f6f4 v[68:71], v[18:25], v[222:229], 0
	v_mfma_f32_16x16x128_f8f6f4 v[72:75], v[26:33], v[222:229], 0
	s_setprio 2
	s_setprio 1
	v_mfma_f32_16x16x128_f8f6f4 v[64:67], v[10:17], v[178:185], 0
	v_mfma_f32_16x16x128_f8f6f4 v[60:63], v[2:9], v[178:185], 0
	v_mfma_f32_16x16x128_f8f6f4 v[52:55], v[2:9], v[202:209], 0
	v_mfma_f32_16x16x128_f8f6f4 v[56:59], v[10:17], v[202:209], 0
	v_mfma_f32_16x16x128_f8f6f4 v[48:51], v[10:17], v[210:217], 0
	v_mfma_f32_16x16x128_f8f6f4 v[44:47], v[2:9], v[210:217], 0
	v_mfma_f32_16x16x128_f8f6f4 v[36:39], v[2:9], v[222:229], 0
	v_mfma_f32_16x16x128_f8f6f4 v[40:43], v[10:17], v[222:229], 0
	s_setprio 2
	s_barrier
	s_add_i32 s50, 0, 0x18000
	s_add_i32 s64, 0, 0x1c000
	v_add_u32_e32 v201, s50, v167
	v_add_u32_e32 v202, s64, v167
	ds_read_b128 v[26:29], v201
	ds_read_b128 v[30:33], v201 offset:1024
	ds_read_b128 v[18:21], v201 offset:2048
	ds_read_b128 v[22:25], v201 offset:3072
	ds_read_b128 v[10:13], v202
	ds_read_b128 v[14:17], v202 offset:1024
	ds_read_b128 v[2:5], v202 offset:2048
	ds_read_b128 v[6:9], v202 offset:3072
	s_mov_b32 m0, s85
	ds_read_b128 v[178:181], v169 offset:32768
	ds_read_b128 v[182:185], v169 offset:33792
	ds_read_b128 v[204:207], v169 offset:34816
	ds_read_b128 v[208:211], v169 offset:35840
	ds_read_b128 v[212:215], v169 offset:36864
	ds_read_b128 v[216:219], v169 offset:37888
	ds_read_b128 v[222:225], v169 offset:38912
	ds_read_b128 v[226:229], v169 offset:39936
	global_load_lds_dwordx4 v189, s[26:27]
	s_mov_b32 m0, s86
	s_nop 0
	global_load_lds_dwordx4 v198, s[26:27]
	s_waitcnt vmcnt(8)
	s_waitcnt lgkmcnt(0)
	s_barrier
	s_setprio 1
	s_waitcnt lgkmcnt(0)
	v_mfma_f32_16x16x128_f8f6f4 v[160:163], v[26:33], v[178:185], v[160:163]
	v_mfma_f32_16x16x128_f8f6f4 v[156:159], v[18:25], v[178:185], v[156:159]
	v_mfma_f32_16x16x128_f8f6f4 v[148:151], v[18:25], v[204:211], v[148:151]
	v_mfma_f32_16x16x128_f8f6f4 v[152:155], v[26:33], v[204:211], v[152:155]
	v_mfma_f32_16x16x128_f8f6f4 v[144:147], v[26:33], v[212:219], v[144:147]
	v_mfma_f32_16x16x128_f8f6f4 v[140:143], v[18:25], v[212:219], v[140:143]
	v_mfma_f32_16x16x128_f8f6f4 v[132:135], v[18:25], v[222:229], v[132:135]
	v_mfma_f32_16x16x128_f8f6f4 v[136:139], v[26:33], v[222:229], v[136:139]
	s_setprio 2
	s_setprio 1
	v_mfma_f32_16x16x128_f8f6f4 v[128:131], v[10:17], v[178:185], v[128:131]
	v_mfma_f32_16x16x128_f8f6f4 v[124:127], v[2:9], v[178:185], v[124:127]
	v_mfma_f32_16x16x128_f8f6f4 v[116:119], v[2:9], v[204:211], v[116:119]
	v_mfma_f32_16x16x128_f8f6f4 v[120:123], v[10:17], v[204:211], v[120:123]
	v_mfma_f32_16x16x128_f8f6f4 v[112:115], v[10:17], v[212:219], v[112:115]
	v_mfma_f32_16x16x128_f8f6f4 v[108:111], v[2:9], v[212:219], v[108:111]
	v_mfma_f32_16x16x128_f8f6f4 v[100:103], v[2:9], v[222:229], v[100:103]
	v_mfma_f32_16x16x128_f8f6f4 v[104:107], v[10:17], v[222:229], v[104:107]
	s_setprio 2
	s_barrier
	s_add_i32 s50, s50, s82
	s_mov_b64 s[26:27], 0x180
	s_add_i32 s51, s50, 0x2000
	v_lshl_add_u64 v[194:195], v[194:195], 0, s[26:27]
	s_mov_b32 m0, s50
	s_add_u32 s30, s30, 0x20180
	ds_read_b128 v[178:181], v169 offset:49152
	ds_read_b128 v[182:185], v169 offset:50176
	ds_read_b128 v[204:207], v169 offset:51200
	ds_read_b128 v[208:211], v169 offset:52224
	ds_read_b128 v[212:215], v169 offset:53248
	ds_read_b128 v[216:219], v169 offset:54272
	ds_read_b128 v[222:225], v169 offset:55296
	ds_read_b128 v[226:229], v169 offset:56320
	global_load_lds_dwordx4 v[194:195], off
	v_lshl_add_u64 v[194:195], v[196:197], 0, s[26:27]
	s_mov_b32 m0, s51
	s_addc_u32 s31, s31, 0
	s_add_i32 s64, s64, s82
	global_load_lds_dwordx4 v[194:195], off
	v_lshl_add_u64 v[194:195], s[30:31], 0, v[170:171]
	s_mov_b32 m0, s64
	s_add_i32 s63, s64, 0x2000
	global_load_lds_dwordx4 v[194:195], off
	v_lshl_add_u64 v[194:195], s[30:31], 0, v[172:173]
	s_mov_b32 m0, s63
	v_readlane_b32 s26, v253, 39
	global_load_lds_dwordx4 v[194:195], off
	s_mov_b32 m0, s90
	v_readlane_b32 s27, v253, 40
	s_nop 4
	global_load_lds_dwordx4 v34, s[26:27]
	s_mov_b32 m0, s91
	s_nop 0
	global_load_lds_dwordx4 v192, s[26:27]
	s_waitcnt vmcnt(8)
	s_waitcnt lgkmcnt(0)
	s_barrier
	s_setprio 1
	s_waitcnt lgkmcnt(0)
	v_mfma_f32_16x16x128_f8f6f4 v[96:99], v[26:33], v[178:185], v[96:99]
	v_mfma_f32_16x16x128_f8f6f4 v[92:95], v[18:25], v[178:185], v[92:95]
	v_mfma_f32_16x16x128_f8f6f4 v[84:87], v[18:25], v[204:211], v[84:87]
	v_mfma_f32_16x16x128_f8f6f4 v[88:91], v[26:33], v[204:211], v[88:91]
	v_mfma_f32_16x16x128_f8f6f4 v[80:83], v[26:33], v[212:219], v[80:83]
	v_mfma_f32_16x16x128_f8f6f4 v[76:79], v[18:25], v[212:219], v[76:79]
	v_mfma_f32_16x16x128_f8f6f4 v[68:71], v[18:25], v[222:229], v[68:71]
	v_mfma_f32_16x16x128_f8f6f4 v[72:75], v[26:33], v[222:229], v[72:75]
	s_setprio 2
	s_setprio 1
	v_mfma_f32_16x16x128_f8f6f4 v[64:67], v[10:17], v[178:185], v[64:67]
	v_mfma_f32_16x16x128_f8f6f4 v[60:63], v[2:9], v[178:185], v[60:63]
	v_mfma_f32_16x16x128_f8f6f4 v[52:55], v[2:9], v[204:211], v[52:55]
	v_mfma_f32_16x16x128_f8f6f4 v[56:59], v[10:17], v[204:211], v[56:59]
	v_mfma_f32_16x16x128_f8f6f4 v[48:51], v[10:17], v[212:219], v[48:51]
	v_mfma_f32_16x16x128_f8f6f4 v[44:47], v[2:9], v[212:219], v[44:47]
	v_mfma_f32_16x16x128_f8f6f4 v[36:39], v[2:9], v[222:229], v[36:39]
	v_mfma_f32_16x16x128_f8f6f4 v[40:43], v[10:17], v[222:229], v[40:43]
	s_setprio 2
	s_barrier
	v_lshl_add_u64 v[18:19], s[26:27], 0, v[174:175]
	v_lshl_add_u64 v[20:21], s[26:27], 0, v[190:191]
	s_mov_b32 s75, 0
	s_mov_b64 s[30:31], 0
	s_branch .LBB0_955
.LBB0_954:
	ds_read_b128 v[178:181], v200
	ds_read_b128 v[182:185], v200 offset:1024
	ds_read_b128 v[204:207], v200 offset:2048
	ds_read_b128 v[208:211], v200 offset:3072
	ds_read_b128 v[10:13], v199
	ds_read_b128 v[14:17], v199 offset:1024
	ds_read_b128 v[2:5], v199 offset:2048
	ds_read_b128 v[6:9], v199 offset:3072
	s_add_u32 s14, s30, 0x200
	s_addc_u32 vcc_lo, s31, 0
	s_and_b64 s[48:49], s[46:47], exec
	s_cselect_b32 s14, 0, s14
	s_cselect_b32 s49, 0, vcc_lo
	s_add_u32 s48, s20, s14
	s_addc_u32 s49, s21, s49
	s_add_u32 s14, s95, s30
	s_addc_u32 vcc_lo, s96, s31
	s_and_b64 s[46:47], s[46:47], exec
	s_cselect_b32 s47, s43, vcc_lo
	s_cselect_b32 s46, s42, s14
	s_mov_b32 m0, s83
	v_lshl_add_u64 v[30:31], v[20:21], 0, s[30:31]
	ds_read_b128 v[22:25], v169
	ds_read_b128 v[26:29], v169 offset:1024
	ds_read_b128 v[212:215], v169 offset:2048
	ds_read_b128 v[216:219], v169 offset:3072
	ds_read_b128 v[222:225], v169 offset:4096
	ds_read_b128 v[226:229], v169 offset:5120
	ds_read_b128 v[230:233], v169 offset:6144
	ds_read_b128 v[234:237], v169 offset:7168
	global_load_lds_dwordx4 v[30:31], off
	v_lshl_add_u64 v[30:31], v[18:19], 0, s[30:31]
	s_mov_b32 m0, s53
	s_nop 0
	global_load_lds_dwordx4 v[30:31], off
	s_waitcnt vmcnt(8)
	s_waitcnt lgkmcnt(0)
	s_barrier
	s_setprio 1
	s_waitcnt lgkmcnt(0)
	v_mfma_f32_16x16x128_f8f6f4 v[160:163], v[178:185], v[22:29], v[160:163]
	v_mfma_f32_16x16x128_f8f6f4 v[156:159], v[204:211], v[22:29], v[156:159]
	v_mfma_f32_16x16x128_f8f6f4 v[148:151], v[204:211], v[212:219], v[148:151]
	v_mfma_f32_16x16x128_f8f6f4 v[152:155], v[178:185], v[212:219], v[152:155]
	v_mfma_f32_16x16x128_f8f6f4 v[144:147], v[178:185], v[222:229], v[144:147]
	v_mfma_f32_16x16x128_f8f6f4 v[140:143], v[204:211], v[222:229], v[140:143]
	v_mfma_f32_16x16x128_f8f6f4 v[132:135], v[204:211], v[230:237], v[132:135]
	v_mfma_f32_16x16x128_f8f6f4 v[136:139], v[178:185], v[230:237], v[136:139]
	s_setprio 2
	s_setprio 1
	v_mfma_f32_16x16x128_f8f6f4 v[128:131], v[10:17], v[22:29], v[128:131]
	v_mfma_f32_16x16x128_f8f6f4 v[124:127], v[2:9], v[22:29], v[124:127]
	v_mfma_f32_16x16x128_f8f6f4 v[116:119], v[2:9], v[212:219], v[116:119]
	v_mfma_f32_16x16x128_f8f6f4 v[120:123], v[10:17], v[212:219], v[120:123]
	v_mfma_f32_16x16x128_f8f6f4 v[112:115], v[10:17], v[222:229], v[112:115]
	v_mfma_f32_16x16x128_f8f6f4 v[108:111], v[2:9], v[222:229], v[108:111]
	v_mfma_f32_16x16x128_f8f6f4 v[100:103], v[2:9], v[230:237], v[100:103]
	v_mfma_f32_16x16x128_f8f6f4 v[104:107], v[10:17], v[230:237], v[104:107]
	s_setprio 2
	s_barrier
	s_mov_b32 m0, s67
	v_lshl_add_u64 v[22:23], s[46:47], 0, v[170:171]
	s_add_u32 vcc_lo, s46, 0x20000
	ds_read_b128 v[212:215], v169 offset:16384
	ds_read_b128 v[216:219], v169 offset:17408
	ds_read_b128 v[222:225], v169 offset:18432
	ds_read_b128 v[226:229], v169 offset:19456
	ds_read_b128 v[230:233], v169 offset:20480
	ds_read_b128 v[234:237], v169 offset:21504
	ds_read_b128 v[238:241], v169 offset:22528
	ds_read_b128 v[242:245], v169 offset:23552
	global_load_lds_dwordx4 v[22:23], off
	v_lshl_add_u64 v[24:25], s[46:47], 0, v[172:173]
	s_mov_b32 m0, s55
	s_addc_u32 vcc_hi, s47, 0
	global_load_lds_dwordx4 v[24:25], off
	v_lshl_add_u64 v[26:27], vcc, 0, v[170:171]
	s_mov_b32 m0, s65
	v_mov_b32_e32 v193, v35
	global_load_lds_dwordx4 v[26:27], off
	v_lshl_add_u64 v[26:27], vcc, 0, v[172:173]
	s_mov_b32 m0, s54
	v_lshl_add_u64 v[28:29], s[48:49], 0, v[34:35]
	global_load_lds_dwordx4 v[26:27], off
	s_mov_b32 m0, s52
	v_lshl_add_u64 v[26:27], s[48:49], 0, v[192:193]
	global_load_lds_dwordx4 v34, s[48:49]
	s_mov_b32 m0, s84
	s_nop 0
	global_load_lds_dwordx4 v192, s[48:49]
	s_waitcnt vmcnt(8)
	s_waitcnt lgkmcnt(0)
	s_barrier
	s_setprio 1
	s_waitcnt lgkmcnt(0)
	v_mfma_f32_16x16x128_f8f6f4 v[96:99], v[178:185], v[212:219], v[96:99]
	v_mfma_f32_16x16x128_f8f6f4 v[92:95], v[204:211], v[212:219], v[92:95]
	v_mfma_f32_16x16x128_f8f6f4 v[84:87], v[204:211], v[222:229], v[84:87]
	v_mfma_f32_16x16x128_f8f6f4 v[88:91], v[178:185], v[222:229], v[88:91]
	v_mfma_f32_16x16x128_f8f6f4 v[80:83], v[178:185], v[230:237], v[80:83]
	v_mfma_f32_16x16x128_f8f6f4 v[76:79], v[204:211], v[230:237], v[76:79]
	v_mfma_f32_16x16x128_f8f6f4 v[68:71], v[204:211], v[238:245], v[68:71]
	v_mfma_f32_16x16x128_f8f6f4 v[72:75], v[178:185], v[238:245], v[72:75]
	s_setprio 2
	s_setprio 1
	v_mfma_f32_16x16x128_f8f6f4 v[64:67], v[10:17], v[212:219], v[64:67]
	v_mfma_f32_16x16x128_f8f6f4 v[60:63], v[2:9], v[212:219], v[60:63]
	v_mfma_f32_16x16x128_f8f6f4 v[52:55], v[2:9], v[222:229], v[52:55]
	v_mfma_f32_16x16x128_f8f6f4 v[56:59], v[10:17], v[222:229], v[56:59]
	v_mfma_f32_16x16x128_f8f6f4 v[48:51], v[10:17], v[230:237], v[48:51]
	v_mfma_f32_16x16x128_f8f6f4 v[44:47], v[2:9], v[230:237], v[44:47]
	v_mfma_f32_16x16x128_f8f6f4 v[36:39], v[2:9], v[238:245], v[36:39]
	v_mfma_f32_16x16x128_f8f6f4 v[40:43], v[10:17], v[238:245], v[40:43]
	s_setprio 2
	s_barrier
	ds_read_b128 v[178:181], v201
	ds_read_b128 v[182:185], v201 offset:1024
	ds_read_b128 v[204:207], v201 offset:2048
	ds_read_b128 v[208:211], v201 offset:3072
	ds_read_b128 v[10:13], v202
	ds_read_b128 v[14:17], v202 offset:1024
	ds_read_b128 v[2:5], v202 offset:2048
	ds_read_b128 v[6:9], v202 offset:3072
	s_mov_b32 m0, s85
	ds_read_b128 v[212:215], v169 offset:32768
	ds_read_b128 v[216:219], v169 offset:33792
	ds_read_b128 v[222:225], v169 offset:34816
	ds_read_b128 v[226:229], v169 offset:35840
	ds_read_b128 v[230:233], v169 offset:36864
	ds_read_b128 v[234:237], v169 offset:37888
	ds_read_b128 v[238:241], v169 offset:38912
	ds_read_b128 v[242:245], v169 offset:39936
	global_load_lds_dwordx4 v189, s[48:49]
	s_mov_b32 m0, s86
	s_nop 0
	global_load_lds_dwordx4 v198, s[48:49]
	s_waitcnt vmcnt(8)
	s_waitcnt lgkmcnt(0)
	s_barrier
	s_setprio 1
	s_waitcnt lgkmcnt(0)
	v_mfma_f32_16x16x128_f8f6f4 v[160:163], v[178:185], v[212:219], v[160:163]
	v_mfma_f32_16x16x128_f8f6f4 v[156:159], v[204:211], v[212:219], v[156:159]
	v_mfma_f32_16x16x128_f8f6f4 v[148:151], v[204:211], v[222:229], v[148:151]
	v_mfma_f32_16x16x128_f8f6f4 v[152:155], v[178:185], v[222:229], v[152:155]
	v_mfma_f32_16x16x128_f8f6f4 v[144:147], v[178:185], v[230:237], v[144:147]
	v_mfma_f32_16x16x128_f8f6f4 v[140:143], v[204:211], v[230:237], v[140:143]
	v_mfma_f32_16x16x128_f8f6f4 v[132:135], v[204:211], v[238:245], v[132:135]
	v_mfma_f32_16x16x128_f8f6f4 v[136:139], v[178:185], v[238:245], v[136:139]
	s_setprio 2
	s_setprio 1
	v_mfma_f32_16x16x128_f8f6f4 v[128:131], v[10:17], v[212:219], v[128:131]
	v_mfma_f32_16x16x128_f8f6f4 v[124:127], v[2:9], v[212:219], v[124:127]
	v_mfma_f32_16x16x128_f8f6f4 v[116:119], v[2:9], v[222:229], v[116:119]
	v_mfma_f32_16x16x128_f8f6f4 v[120:123], v[10:17], v[222:229], v[120:123]
	v_mfma_f32_16x16x128_f8f6f4 v[112:115], v[10:17], v[230:237], v[112:115]
	v_mfma_f32_16x16x128_f8f6f4 v[108:111], v[2:9], v[230:237], v[108:111]
	v_mfma_f32_16x16x128_f8f6f4 v[100:103], v[2:9], v[238:245], v[100:103]
	v_mfma_f32_16x16x128_f8f6f4 v[104:107], v[10:17], v[238:245], v[104:107]
	s_setprio 2
	s_barrier
	s_mov_b32 m0, s50
	v_lshl_add_u64 v[22:23], v[22:23], 0, s[18:19]
	s_add_u32 s46, s46, 0x20080
	ds_read_b128 v[212:215], v169 offset:49152
	ds_read_b128 v[216:219], v169 offset:50176
	ds_read_b128 v[222:225], v169 offset:51200
	ds_read_b128 v[226:229], v169 offset:52224
	ds_read_b128 v[230:233], v169 offset:53248
	ds_read_b128 v[234:237], v169 offset:54272
	ds_read_b128 v[238:241], v169 offset:55296
	ds_read_b128 v[242:245], v169 offset:56320
	global_load_lds_dwordx4 v[22:23], off
	v_lshl_add_u64 v[22:23], v[24:25], 0, s[18:19]
	s_mov_b32 m0, s51
	s_addc_u32 s47, s47, 0
	global_load_lds_dwordx4 v[22:23], off
	v_lshl_add_u64 v[22:23], s[46:47], 0, v[170:171]
	s_mov_b32 m0, s64
	s_nop 0
	global_load_lds_dwordx4 v[22:23], off
	v_lshl_add_u64 v[22:23], s[46:47], 0, v[172:173]
	s_mov_b32 m0, s63
	s_nop 0
	global_load_lds_dwordx4 v[22:23], off
	v_lshl_add_u64 v[22:23], v[28:29], 0, s[18:19]
	s_mov_b32 m0, s90
	s_nop 0
	global_load_lds_dwordx4 v[22:23], off
	v_lshl_add_u64 v[22:23], v[26:27], 0, s[18:19]
	s_mov_b32 m0, s91
	s_nop 0
	global_load_lds_dwordx4 v[22:23], off
	s_waitcnt vmcnt(8)
	s_waitcnt lgkmcnt(0)
	s_barrier
	s_setprio 1
	s_waitcnt lgkmcnt(0)
	v_mfma_f32_16x16x128_f8f6f4 v[96:99], v[178:185], v[212:219], v[96:99]
	v_mfma_f32_16x16x128_f8f6f4 v[92:95], v[204:211], v[212:219], v[92:95]
	v_mfma_f32_16x16x128_f8f6f4 v[84:87], v[204:211], v[222:229], v[84:87]
	v_mfma_f32_16x16x128_f8f6f4 v[88:91], v[178:185], v[222:229], v[88:91]
	v_mfma_f32_16x16x128_f8f6f4 v[80:83], v[178:185], v[230:237], v[80:83]
	v_mfma_f32_16x16x128_f8f6f4 v[76:79], v[204:211], v[230:237], v[76:79]
	v_mfma_f32_16x16x128_f8f6f4 v[68:71], v[204:211], v[238:245], v[68:71]
	v_mfma_f32_16x16x128_f8f6f4 v[72:75], v[178:185], v[238:245], v[72:75]
	s_setprio 2
	s_setprio 1
	v_mfma_f32_16x16x128_f8f6f4 v[64:67], v[10:17], v[212:219], v[64:67]
	v_mfma_f32_16x16x128_f8f6f4 v[60:63], v[2:9], v[212:219], v[60:63]
	v_mfma_f32_16x16x128_f8f6f4 v[52:55], v[2:9], v[222:229], v[52:55]
	v_mfma_f32_16x16x128_f8f6f4 v[56:59], v[10:17], v[222:229], v[56:59]
	v_mfma_f32_16x16x128_f8f6f4 v[48:51], v[10:17], v[230:237], v[48:51]
	v_mfma_f32_16x16x128_f8f6f4 v[44:47], v[2:9], v[230:237], v[44:47]
	v_mfma_f32_16x16x128_f8f6f4 v[36:39], v[2:9], v[238:245], v[36:39]
	v_mfma_f32_16x16x128_f8f6f4 v[40:43], v[10:17], v[238:245], v[40:43]
	s_setprio 2
	s_barrier
	s_add_i32 s75, s75, 2
	s_add_u32 s30, s30, 0x100
	s_addc_u32 s31, s31, 0
	s_cmp_gt_u32 s75, 5
	s_cbranch_scc1 .LBB0_957

.LBB0_1086:
	s_lshl_b32 s10, s51, 18
	s_add_u32 s10, s20, s10
	s_addc_u32 s11, s21, 0
	s_and_b64 s[16:17], s[4:5], exec
	s_cselect_b32 s54, s11, s31
	s_cselect_b32 s55, s10, s30
	s_lshl_b32 s14, s50, 18
	s_add_u32 s16, s15, s14
	s_addc_u32 s17, s26, 0
	s_and_b64 s[36:37], s[4:5], exec
	s_cselect_b32 s56, s17, s23
	s_cselect_b32 s57, s16, s22
	s_add_i32 s60, 0, 0x10000
	s_add_i32 s62, 0, 0x14000
	v_add_u32_e32 v198, s60, v196
	v_add_u32_e32 v199, s62, v196
	ds_read_b128 v[26:29], v198
	ds_read_b128 v[30:33], v198 offset:1024
	ds_read_b128 v[18:21], v198 offset:2048
	ds_read_b128 v[22:25], v198 offset:3072
	ds_read_b128 v[10:13], v199
	ds_read_b128 v[14:17], v199 offset:1024
	ds_read_b128 v[2:5], v199 offset:2048
	ds_read_b128 v[6:9], v199 offset:3072
	s_add_u32 s36, s30, 0x20080
	s_addc_u32 s37, s31, 0
	s_add_i32 s58, s41, 0xc000
	v_lshl_add_u64 v[174:175], s[36:37], 0, v[168:169]
	s_mov_b32 m0, s58
	s_add_i32 s59, s41, 0xe000
	ds_read_b128 v[200:203], v197
	ds_read_b128 v[204:207], v197 offset:1024
	ds_read_b128 v[222:225], v197 offset:2048
	ds_read_b128 v[226:229], v197 offset:3072
	ds_read_b128 v[230:233], v197 offset:4096
	ds_read_b128 v[234:237], v197 offset:5120
	ds_read_b128 v[238:241], v197 offset:6144
	ds_read_b128 v[242:245], v197 offset:7168
	global_load_lds_dwordx4 v[174:175], off
	v_lshl_add_u64 v[174:175], s[36:37], 0, v[166:167]
	s_mov_b32 m0, s59
	s_nop 0
	global_load_lds_dwordx4 v[174:175], off
	s_waitcnt vmcnt(8)
	s_waitcnt lgkmcnt(0)
	s_barrier
	s_setprio 1
	s_waitcnt lgkmcnt(0)
	v_mfma_f32_16x16x128_f8f6f4 v[160:163], v[26:33], v[200:207], 0
	v_mfma_f32_16x16x128_f8f6f4 v[156:159], v[18:25], v[200:207], 0
	v_mfma_f32_16x16x128_f8f6f4 v[148:151], v[18:25], v[222:229], 0
	v_mfma_f32_16x16x128_f8f6f4 v[152:155], v[26:33], v[222:229], 0
	v_mfma_f32_16x16x128_f8f6f4 v[144:147], v[26:33], v[230:237], 0
	v_mfma_f32_16x16x128_f8f6f4 v[140:143], v[18:25], v[230:237], 0
	v_mfma_f32_16x16x128_f8f6f4 v[132:135], v[18:25], v[238:245], 0
	v_mfma_f32_16x16x128_f8f6f4 v[136:139], v[26:33], v[238:245], 0
	s_setprio 2
	s_setprio 1
	v_mfma_f32_16x16x128_f8f6f4 v[128:131], v[10:17], v[200:207], 0
	v_mfma_f32_16x16x128_f8f6f4 v[124:127], v[2:9], v[200:207], 0
	v_mfma_f32_16x16x128_f8f6f4 v[116:119], v[2:9], v[222:229], 0
	v_mfma_f32_16x16x128_f8f6f4 v[120:123], v[10:17], v[222:229], 0
	v_mfma_f32_16x16x128_f8f6f4 v[112:115], v[10:17], v[230:237], 0
	v_mfma_f32_16x16x128_f8f6f4 v[108:111], v[2:9], v[230:237], 0
	v_mfma_f32_16x16x128_f8f6f4 v[100:103], v[2:9], v[238:245], 0
	v_mfma_f32_16x16x128_f8f6f4 v[104:107], v[10:17], v[238:245], 0
	s_setprio 2
	s_barrier
	s_add_i32 s60, s60, s40
	v_lshl_add_u64 v[174:175], s[22:23], 0, v[34:35]
	s_add_i32 s61, s60, 0x2000
	v_lshl_add_u64 v[178:179], v[174:175], 0, s[28:29]
	s_mov_b32 m0, s60
	v_lshl_add_u64 v[190:191], s[22:23], 0, v[164:165]
	s_add_u32 s36, s22, 0x20100
	ds_read_b128 v[200:203], v197 offset:16384
	ds_read_b128 v[204:207], v197 offset:17408
	ds_read_b128 v[222:225], v197 offset:18432
	ds_read_b128 v[226:229], v197 offset:19456
	ds_read_b128 v[230:233], v197 offset:20480
	ds_read_b128 v[234:237], v197 offset:21504
	ds_read_b128 v[238:241], v197 offset:22528
	ds_read_b128 v[242:245], v197 offset:23552
	global_load_lds_dwordx4 v[178:179], off
	v_lshl_add_u64 v[178:179], v[190:191], 0, s[28:29]
	s_mov_b32 m0, s61
	s_addc_u32 s37, s23, 0
	s_add_i32 s62, s62, s40
	global_load_lds_dwordx4 v[178:179], off
	v_lshl_add_u64 v[178:179], s[36:37], 0, v[34:35]
	s_mov_b32 m0, s62
	s_add_i32 s63, s62, 0x2000
	global_load_lds_dwordx4 v[178:179], off
	v_lshl_add_u64 v[178:179], s[36:37], 0, v[164:165]
	s_mov_b32 m0, s63
	v_lshl_add_u64 v[192:193], s[30:31], 0, v[168:169]
	global_load_lds_dwordx4 v[178:179], off
	v_lshl_add_u64 v[178:179], v[192:193], 0, s[28:29]
	s_mov_b32 m0, s41
	v_lshl_add_u64 v[194:195], s[30:31], 0, v[166:167]
	global_load_lds_dwordx4 v[178:179], off
	v_lshl_add_u64 v[178:179], v[194:195], 0, s[28:29]
	s_mov_b32 m0, s42
	s_nop 0
	global_load_lds_dwordx4 v[178:179], off
	s_waitcnt vmcnt(8)
	s_waitcnt lgkmcnt(0)
	s_barrier
	s_setprio 1
	s_waitcnt lgkmcnt(0)
	v_mfma_f32_16x16x128_f8f6f4 v[96:99], v[26:33], v[200:207], 0
	v_mfma_f32_16x16x128_f8f6f4 v[92:95], v[18:25], v[200:207], 0
	v_mfma_f32_16x16x128_f8f6f4 v[84:87], v[18:25], v[222:229], 0
	v_mfma_f32_16x16x128_f8f6f4 v[88:91], v[26:33], v[222:229], 0
	v_mfma_f32_16x16x128_f8f6f4 v[80:83], v[26:33], v[230:237], 0
	v_mfma_f32_16x16x128_f8f6f4 v[76:79], v[18:25], v[230:237], 0
	v_mfma_f32_16x16x128_f8f6f4 v[68:71], v[18:25], v[238:245], 0
	v_mfma_f32_16x16x128_f8f6f4 v[72:75], v[26:33], v[238:245], 0
	s_setprio 2
	s_setprio 1
	v_mfma_f32_16x16x128_f8f6f4 v[64:67], v[10:17], v[200:207], 0
	v_mfma_f32_16x16x128_f8f6f4 v[60:63], v[2:9], v[200:207], 0
	v_mfma_f32_16x16x128_f8f6f4 v[52:55], v[2:9], v[222:229], 0
	v_mfma_f32_16x16x128_f8f6f4 v[56:59], v[10:17], v[222:229], 0
	v_mfma_f32_16x16x128_f8f6f4 v[48:51], v[10:17], v[230:237], 0
	v_mfma_f32_16x16x128_f8f6f4 v[44:47], v[2:9], v[230:237], 0
	v_mfma_f32_16x16x128_f8f6f4 v[36:39], v[2:9], v[238:245], 0
	v_mfma_f32_16x16x128_f8f6f4 v[40:43], v[10:17], v[238:245], 0
	s_setprio 2
	s_barrier
	s_add_i32 s64, 0, 0x18000
	s_add_i32 s66, 0, 0x1c000
	v_add_u32_e32 v200, s64, v196
	v_add_u32_e32 v201, s66, v196
	ds_read_b128 v[26:29], v200
	ds_read_b128 v[30:33], v200 offset:1024
	ds_read_b128 v[18:21], v200 offset:2048
	ds_read_b128 v[22:25], v200 offset:3072
	ds_read_b128 v[10:13], v201
	ds_read_b128 v[14:17], v201 offset:1024
	ds_read_b128 v[2:5], v201 offset:2048
	ds_read_b128 v[6:9], v201 offset:3072
	s_add_u32 s36, s30, 0x20100
	s_addc_u32 s37, s31, 0
	s_mov_b32 m0, s43
	v_lshl_add_u64 v[178:179], s[36:37], 0, v[168:169]
	ds_read_b128 v[202:205], v197 offset:32768
	ds_read_b128 v[206:209], v197 offset:33792
	ds_read_b128 v[222:225], v197 offset:34816
	ds_read_b128 v[226:229], v197 offset:35840
	ds_read_b128 v[230:233], v197 offset:36864
	ds_read_b128 v[234:237], v197 offset:37888
	ds_read_b128 v[238:241], v197 offset:38912
	ds_read_b128 v[242:245], v197 offset:39936
	global_load_lds_dwordx4 v[178:179], off
	v_lshl_add_u64 v[178:179], s[36:37], 0, v[166:167]
	s_mov_b32 m0, s44
	s_nop 0
	global_load_lds_dwordx4 v[178:179], off
	s_waitcnt vmcnt(8)
	s_waitcnt lgkmcnt(0)
	s_barrier
	s_setprio 1
	s_waitcnt lgkmcnt(0)
	v_mfma_f32_16x16x128_f8f6f4 v[160:163], v[26:33], v[202:209], v[160:163]
	v_mfma_f32_16x16x128_f8f6f4 v[156:159], v[18:25], v[202:209], v[156:159]
	v_mfma_f32_16x16x128_f8f6f4 v[148:151], v[18:25], v[222:229], v[148:151]
	v_mfma_f32_16x16x128_f8f6f4 v[152:155], v[26:33], v[222:229], v[152:155]
	v_mfma_f32_16x16x128_f8f6f4 v[144:147], v[26:33], v[230:237], v[144:147]
	v_mfma_f32_16x16x128_f8f6f4 v[140:143], v[18:25], v[230:237], v[140:143]
	v_mfma_f32_16x16x128_f8f6f4 v[132:135], v[18:25], v[238:245], v[132:135]
	v_mfma_f32_16x16x128_f8f6f4 v[136:139], v[26:33], v[238:245], v[136:139]
	s_setprio 2
	s_setprio 1
	v_mfma_f32_16x16x128_f8f6f4 v[128:131], v[10:17], v[202:209], v[128:131]
	v_mfma_f32_16x16x128_f8f6f4 v[124:127], v[2:9], v[202:209], v[124:127]
	v_mfma_f32_16x16x128_f8f6f4 v[116:119], v[2:9], v[222:229], v[116:119]
	v_mfma_f32_16x16x128_f8f6f4 v[120:123], v[10:17], v[222:229], v[120:123]
	v_mfma_f32_16x16x128_f8f6f4 v[112:115], v[10:17], v[230:237], v[112:115]
	v_mfma_f32_16x16x128_f8f6f4 v[108:111], v[2:9], v[230:237], v[108:111]
	v_mfma_f32_16x16x128_f8f6f4 v[100:103], v[2:9], v[238:245], v[100:103]
	v_mfma_f32_16x16x128_f8f6f4 v[104:107], v[10:17], v[238:245], v[104:107]
	s_setprio 2
	s_barrier
	s_add_i32 s64, s64, s40
	s_mov_b64 s[24:25], 0x180
	s_add_i32 s65, s64, 0x2000
	v_lshl_add_u64 v[174:175], v[174:175], 0, s[24:25]
	s_mov_b32 m0, s64
	s_add_u32 s36, s22, 0x20180
	ds_read_b128 v[202:205], v197 offset:49152
	ds_read_b128 v[206:209], v197 offset:50176
	ds_read_b128 v[222:225], v197 offset:51200
	ds_read_b128 v[226:229], v197 offset:52224
	ds_read_b128 v[230:233], v197 offset:53248
	ds_read_b128 v[234:237], v197 offset:54272
	ds_read_b128 v[238:241], v197 offset:55296
	ds_read_b128 v[242:245], v197 offset:56320
	global_load_lds_dwordx4 v[174:175], off
	v_lshl_add_u64 v[174:175], v[190:191], 0, s[24:25]
	s_mov_b32 m0, s65
	s_addc_u32 s37, s23, 0
	s_add_i32 s66, s66, s40
	global_load_lds_dwordx4 v[174:175], off
	v_lshl_add_u64 v[174:175], s[36:37], 0, v[34:35]
	s_mov_b32 m0, s66
	s_add_i32 s67, s66, 0x2000
	global_load_lds_dwordx4 v[174:175], off
	v_lshl_add_u64 v[174:175], s[36:37], 0, v[164:165]
	s_mov_b32 m0, s67
	s_nop 0
	global_load_lds_dwordx4 v[174:175], off
	v_lshl_add_u64 v[174:175], v[192:193], 0, s[24:25]
	s_mov_b32 m0, s47
	s_nop 0
	global_load_lds_dwordx4 v[174:175], off
	v_lshl_add_u64 v[174:175], v[194:195], 0, s[24:25]
	s_mov_b32 m0, s48
	s_nop 0
	global_load_lds_dwordx4 v[174:175], off
	s_waitcnt vmcnt(8)
	s_waitcnt lgkmcnt(0)
	s_barrier
	s_setprio 1
	s_waitcnt lgkmcnt(0)
	v_mfma_f32_16x16x128_f8f6f4 v[96:99], v[26:33], v[202:209], v[96:99]
	v_mfma_f32_16x16x128_f8f6f4 v[92:95], v[18:25], v[202:209], v[92:95]
	v_mfma_f32_16x16x128_f8f6f4 v[84:87], v[18:25], v[222:229], v[84:87]
	v_mfma_f32_16x16x128_f8f6f4 v[88:91], v[26:33], v[222:229], v[88:91]
	v_mfma_f32_16x16x128_f8f6f4 v[80:83], v[26:33], v[230:237], v[80:83]
	v_mfma_f32_16x16x128_f8f6f4 v[76:79], v[18:25], v[230:237], v[76:79]
	v_mfma_f32_16x16x128_f8f6f4 v[68:71], v[18:25], v[238:245], v[68:71]
	v_mfma_f32_16x16x128_f8f6f4 v[72:75], v[26:33], v[238:245], v[72:75]
	s_setprio 2
	s_setprio 1
	v_mfma_f32_16x16x128_f8f6f4 v[64:67], v[10:17], v[202:209], v[64:67]
	v_mfma_f32_16x16x128_f8f6f4 v[60:63], v[2:9], v[202:209], v[60:63]
	v_mfma_f32_16x16x128_f8f6f4 v[52:55], v[2:9], v[222:229], v[52:55]
	v_mfma_f32_16x16x128_f8f6f4 v[56:59], v[10:17], v[222:229], v[56:59]
	v_mfma_f32_16x16x128_f8f6f4 v[48:51], v[10:17], v[230:237], v[48:51]
	v_mfma_f32_16x16x128_f8f6f4 v[44:47], v[2:9], v[230:237], v[44:47]
	v_mfma_f32_16x16x128_f8f6f4 v[36:39], v[2:9], v[238:245], v[36:39]
	v_mfma_f32_16x16x128_f8f6f4 v[40:43], v[10:17], v[238:245], v[40:43]
	s_setprio 2
	s_barrier
	s_add_u32 s30, s30, 0x20180
	s_addc_u32 s31, s31, 0
	s_add_u32 s68, s22, 0x200
	s_addc_u32 s69, s23, 0
	s_mov_b32 s70, 0
.LBB0_1087:
	ds_read_b128 v[2:5], v198
	ds_read_b128 v[6:9], v198 offset:1024
	ds_read_b128 v[10:13], v198 offset:2048
	ds_read_b128 v[14:17], v198 offset:3072
	ds_read_b128 v[18:21], v199
	ds_read_b128 v[22:25], v199 offset:1024
	ds_read_b128 v[26:29], v199 offset:2048
	ds_read_b128 v[30:33], v199 offset:3072
	s_add_u32 s14, s30, 0xfffe0080
	s_addc_u32 s22, s31, -1
	s_cmp_eq_u32 s70, 4
	s_cselect_b32 s37, s54, s22
	s_cselect_b32 s36, s55, s14
	s_cselect_b32 s23, s56, s69
	s_cselect_b32 s22, s57, s68
	s_mov_b32 m0, s58
	v_lshl_add_u64 v[174:175], s[30:31], 0, v[170:171]
	ds_read_b128 v[202:205], v197
	ds_read_b128 v[206:209], v197 offset:1024
	ds_read_b128 v[222:225], v197 offset:2048
	ds_read_b128 v[226:229], v197 offset:3072
	ds_read_b128 v[230:233], v197 offset:4096
	ds_read_b128 v[234:237], v197 offset:5120
	ds_read_b128 v[238:241], v197 offset:6144
	ds_read_b128 v[242:245], v197 offset:7168
	global_load_lds_dwordx4 v[174:175], off
	v_lshl_add_u64 v[174:175], s[30:31], 0, v[172:173]
	s_mov_b32 m0, s59
	s_nop 0
	global_load_lds_dwordx4 v[174:175], off
	s_waitcnt vmcnt(8)
	s_waitcnt lgkmcnt(0)
	s_barrier
	s_setprio 1
	s_waitcnt lgkmcnt(0)
	v_mfma_f32_16x16x128_f8f6f4 v[160:163], v[2:9], v[202:209], v[160:163]
	v_mfma_f32_16x16x128_f8f6f4 v[156:159], v[10:17], v[202:209], v[156:159]
	v_mfma_f32_16x16x128_f8f6f4 v[148:151], v[10:17], v[222:229], v[148:151]
	v_mfma_f32_16x16x128_f8f6f4 v[152:155], v[2:9], v[222:229], v[152:155]
	v_mfma_f32_16x16x128_f8f6f4 v[144:147], v[2:9], v[230:237], v[144:147]
	v_mfma_f32_16x16x128_f8f6f4 v[140:143], v[10:17], v[230:237], v[140:143]
	v_mfma_f32_16x16x128_f8f6f4 v[132:135], v[10:17], v[238:245], v[132:135]
	v_mfma_f32_16x16x128_f8f6f4 v[136:139], v[2:9], v[238:245], v[136:139]
	s_setprio 2
	s_setprio 1
	v_mfma_f32_16x16x128_f8f6f4 v[128:131], v[18:25], v[202:209], v[128:131]
	v_mfma_f32_16x16x128_f8f6f4 v[124:127], v[26:33], v[202:209], v[124:127]
	v_mfma_f32_16x16x128_f8f6f4 v[116:119], v[26:33], v[222:229], v[116:119]
	v_mfma_f32_16x16x128_f8f6f4 v[120:123], v[18:25], v[222:229], v[120:123]
	v_mfma_f32_16x16x128_f8f6f4 v[112:115], v[18:25], v[230:237], v[112:115]
	v_mfma_f32_16x16x128_f8f6f4 v[108:111], v[26:33], v[230:237], v[108:111]
	v_mfma_f32_16x16x128_f8f6f4 v[100:103], v[26:33], v[238:245], v[100:103]
	v_mfma_f32_16x16x128_f8f6f4 v[104:107], v[18:25], v[238:245], v[104:107]
	s_setprio 2
	s_barrier
	s_mov_b32 m0, s60
	v_lshl_add_u64 v[174:175], s[22:23], 0, v[34:35]
	s_add_u32 s72, s22, 0x20000
	ds_read_b128 v[202:205], v197 offset:16384
	ds_read_b128 v[206:209], v197 offset:17408
	ds_read_b128 v[222:225], v197 offset:18432
	ds_read_b128 v[226:229], v197 offset:19456
	ds_read_b128 v[230:233], v197 offset:20480
	ds_read_b128 v[234:237], v197 offset:21504
	ds_read_b128 v[238:241], v197 offset:22528
	ds_read_b128 v[242:245], v197 offset:23552
	global_load_lds_dwordx4 v[174:175], off
	v_lshl_add_u64 v[190:191], s[22:23], 0, v[164:165]
	s_mov_b32 m0, s61
	s_addc_u32 s73, s23, 0
	global_load_lds_dwordx4 v[190:191], off
	v_lshl_add_u64 v[178:179], s[72:73], 0, v[34:35]
	s_mov_b32 m0, s62
	v_lshl_add_u64 v[192:193], s[36:37], 0, v[168:169]
	global_load_lds_dwordx4 v[178:179], off
	v_lshl_add_u64 v[178:179], s[72:73], 0, v[164:165]
	s_mov_b32 m0, s63
	v_lshl_add_u64 v[194:195], s[36:37], 0, v[166:167]
	global_load_lds_dwordx4 v[178:179], off
	s_mov_b32 m0, s41
	s_nop 0
	global_load_lds_dwordx4 v[192:193], off
	s_mov_b32 m0, s42
	s_nop 0
	global_load_lds_dwordx4 v[194:195], off
	s_waitcnt vmcnt(8)
	s_waitcnt lgkmcnt(0)
	s_barrier
	s_setprio 1
	s_waitcnt lgkmcnt(0)
	v_mfma_f32_16x16x128_f8f6f4 v[96:99], v[2:9], v[202:209], v[96:99]
	v_mfma_f32_16x16x128_f8f6f4 v[92:95], v[10:17], v[202:209], v[92:95]
	v_mfma_f32_16x16x128_f8f6f4 v[84:87], v[10:17], v[222:229], v[84:87]
	v_mfma_f32_16x16x128_f8f6f4 v[88:91], v[2:9], v[222:229], v[88:91]
	v_mfma_f32_16x16x128_f8f6f4 v[80:83], v[2:9], v[230:237], v[80:83]
	v_mfma_f32_16x16x128_f8f6f4 v[76:79], v[10:17], v[230:237], v[76:79]
	v_mfma_f32_16x16x128_f8f6f4 v[68:71], v[10:17], v[238:245], v[68:71]
	v_mfma_f32_16x16x128_f8f6f4 v[72:75], v[2:9], v[238:245], v[72:75]
	s_setprio 2
	s_setprio 1
	v_mfma_f32_16x16x128_f8f6f4 v[64:67], v[18:25], v[202:209], v[64:67]
	v_mfma_f32_16x16x128_f8f6f4 v[60:63], v[26:33], v[202:209], v[60:63]
	v_mfma_f32_16x16x128_f8f6f4 v[52:55], v[26:33], v[222:229], v[52:55]
	v_mfma_f32_16x16x128_f8f6f4 v[56:59], v[18:25], v[222:229], v[56:59]
	v_mfma_f32_16x16x128_f8f6f4 v[48:51], v[18:25], v[230:237], v[48:51]
	v_mfma_f32_16x16x128_f8f6f4 v[44:47], v[26:33], v[230:237], v[44:47]
	v_mfma_f32_16x16x128_f8f6f4 v[36:39], v[26:33], v[238:245], v[36:39]
	v_mfma_f32_16x16x128_f8f6f4 v[40:43], v[18:25], v[238:245], v[40:43]
	s_setprio 2
	s_barrier
	ds_read_b128 v[26:29], v200
	ds_read_b128 v[30:33], v200 offset:1024
	ds_read_b128 v[18:21], v200 offset:2048
	ds_read_b128 v[22:25], v200 offset:3072
	ds_read_b128 v[10:13], v201
	ds_read_b128 v[14:17], v201 offset:1024
	ds_read_b128 v[2:5], v201 offset:2048
	ds_read_b128 v[6:9], v201 offset:3072
	s_add_u32 s36, s36, 0x20000
	s_addc_u32 s37, s37, 0
	s_mov_b32 m0, s43
	v_lshl_add_u64 v[178:179], s[36:37], 0, v[168:169]
	ds_read_b128 v[202:205], v197 offset:32768
	ds_read_b128 v[206:209], v197 offset:33792
	ds_read_b128 v[222:225], v197 offset:34816
	ds_read_b128 v[226:229], v197 offset:35840
	ds_read_b128 v[230:233], v197 offset:36864
	ds_read_b128 v[234:237], v197 offset:37888
	ds_read_b128 v[238:241], v197 offset:38912
	ds_read_b128 v[242:245], v197 offset:39936
	global_load_lds_dwordx4 v[178:179], off
	v_lshl_add_u64 v[178:179], s[36:37], 0, v[166:167]
	s_mov_b32 m0, s44
	s_nop 0
	global_load_lds_dwordx4 v[178:179], off
	s_waitcnt vmcnt(8)
	s_waitcnt lgkmcnt(0)
	s_barrier
	s_setprio 1
	s_waitcnt lgkmcnt(0)
	v_mfma_f32_16x16x128_f8f6f4 v[160:163], v[26:33], v[202:209], v[160:163]
	v_mfma_f32_16x16x128_f8f6f4 v[156:159], v[18:25], v[202:209], v[156:159]
	v_mfma_f32_16x16x128_f8f6f4 v[148:151], v[18:25], v[222:229], v[148:151]
	v_mfma_f32_16x16x128_f8f6f4 v[152:155], v[26:33], v[222:229], v[152:155]
	v_mfma_f32_16x16x128_f8f6f4 v[144:147], v[26:33], v[230:237], v[144:147]
	v_mfma_f32_16x16x128_f8f6f4 v[140:143], v[18:25], v[230:237], v[140:143]
	v_mfma_f32_16x16x128_f8f6f4 v[132:135], v[18:25], v[238:245], v[132:135]
	v_mfma_f32_16x16x128_f8f6f4 v[136:139], v[26:33], v[238:245], v[136:139]
	s_setprio 2
	s_setprio 1
	v_mfma_f32_16x16x128_f8f6f4 v[128:131], v[10:17], v[202:209], v[128:131]
	v_mfma_f32_16x16x128_f8f6f4 v[124:127], v[2:9], v[202:209], v[124:127]
	v_mfma_f32_16x16x128_f8f6f4 v[116:119], v[2:9], v[222:229], v[116:119]
	v_mfma_f32_16x16x128_f8f6f4 v[120:123], v[10:17], v[222:229], v[120:123]
	v_mfma_f32_16x16x128_f8f6f4 v[112:115], v[10:17], v[230:237], v[112:115]
	v_mfma_f32_16x16x128_f8f6f4 v[108:111], v[2:9], v[230:237], v[108:111]
	v_mfma_f32_16x16x128_f8f6f4 v[100:103], v[2:9], v[238:245], v[100:103]
	v_mfma_f32_16x16x128_f8f6f4 v[104:107], v[10:17], v[238:245], v[104:107]
	s_setprio 2
	s_barrier
	s_mov_b32 m0, s64
	v_lshl_add_u64 v[174:175], v[174:175], 0, s[18:19]
	s_add_u32 s22, s22, 0x20080
	ds_read_b128 v[202:205], v197 offset:49152
	ds_read_b128 v[206:209], v197 offset:50176
	ds_read_b128 v[222:225], v197 offset:51200
	ds_read_b128 v[226:229], v197 offset:52224
	ds_read_b128 v[230:233], v197 offset:53248
	ds_read_b128 v[234:237], v197 offset:54272
	ds_read_b128 v[238:241], v197 offset:55296
	ds_read_b128 v[242:245], v197 offset:56320
	global_load_lds_dwordx4 v[174:175], off
	v_lshl_add_u64 v[174:175], v[190:191], 0, s[18:19]
	s_mov_b32 m0, s65
	s_addc_u32 s23, s23, 0
	global_load_lds_dwordx4 v[174:175], off
	v_lshl_add_u64 v[174:175], s[22:23], 0, v[34:35]
	s_mov_b32 m0, s66
	s_nop 0
	global_load_lds_dwordx4 v[174:175], off
	v_lshl_add_u64 v[174:175], s[22:23], 0, v[164:165]
	s_mov_b32 m0, s67
	s_nop 0
	global_load_lds_dwordx4 v[174:175], off
	v_lshl_add_u64 v[174:175], v[192:193], 0, s[18:19]
	s_mov_b32 m0, s47
	s_nop 0
	global_load_lds_dwordx4 v[174:175], off
	v_lshl_add_u64 v[174:175], v[194:195], 0, s[18:19]
	s_mov_b32 m0, s48
	s_nop 0
	global_load_lds_dwordx4 v[174:175], off
	s_waitcnt vmcnt(8)
	s_waitcnt lgkmcnt(0)
	s_barrier
	s_setprio 1
	s_waitcnt lgkmcnt(0)
	v_mfma_f32_16x16x128_f8f6f4 v[96:99], v[26:33], v[202:209], v[96:99]
	v_mfma_f32_16x16x128_f8f6f4 v[92:95], v[18:25], v[202:209], v[92:95]
	v_mfma_f32_16x16x128_f8f6f4 v[84:87], v[18:25], v[222:229], v[84:87]
	v_mfma_f32_16x16x128_f8f6f4 v[88:91], v[26:33], v[222:229], v[88:91]
	v_mfma_f32_16x16x128_f8f6f4 v[80:83], v[26:33], v[230:237], v[80:83]
	v_mfma_f32_16x16x128_f8f6f4 v[76:79], v[18:25], v[230:237], v[76:79]
	v_mfma_f32_16x16x128_f8f6f4 v[68:71], v[18:25], v[238:245], v[68:71]
	v_mfma_f32_16x16x128_f8f6f4 v[72:75], v[26:33], v[238:245], v[72:75]
	s_setprio 2
	s_setprio 1
	v_mfma_f32_16x16x128_f8f6f4 v[64:67], v[10:17], v[202:209], v[64:67]
	v_mfma_f32_16x16x128_f8f6f4 v[60:63], v[2:9], v[202:209], v[60:63]
	v_mfma_f32_16x16x128_f8f6f4 v[52:55], v[2:9], v[222:229], v[52:55]
	v_mfma_f32_16x16x128_f8f6f4 v[56:59], v[10:17], v[222:229], v[56:59]
	v_mfma_f32_16x16x128_f8f6f4 v[48:51], v[10:17], v[230:237], v[48:51]
	v_mfma_f32_16x16x128_f8f6f4 v[44:47], v[2:9], v[230:237], v[44:47]
	v_mfma_f32_16x16x128_f8f6f4 v[36:39], v[2:9], v[238:245], v[36:39]
	v_mfma_f32_16x16x128_f8f6f4 v[40:43], v[10:17], v[238:245], v[40:43]
	s_setprio 2
	s_barrier
	s_add_i32 s70, s70, 2
	s_add_u32 s30, s30, 0x100
	s_addc_u32 s31, s31, 0
	s_add_u32 s68, s68, 0x100
	s_addc_u32 s69, s69, 0
	s_cmp_gt_u32 s70, 5
	s_cbranch_scc0 .LBB0_1087

.LBB0_1160:
	s_add_u32 s22, s30, 0x100
	s_addc_u32 s23, s31, 0
	s_add_i32 s65, 0, 0x10000
	s_cmp_eq_u32 s64, 18
	s_cselect_b32 s41, s58, s23
	s_cselect_b32 s40, s59, s22
	s_cselect_b32 s37, s60, s63
	s_cselect_b32 s36, s61, s62
	s_add_i32 s66, 0, 0x14000
	v_add_u32_e32 v2, s65, v222
	v_add_u32_e32 v6, s66, v222
	ds_read_b128 v[26:29], v2
	ds_read_b128 v[30:33], v2 offset:1024
	ds_read_b128 v[18:21], v2 offset:2048
	ds_read_b128 v[22:25], v2 offset:3072
	ds_read_b128 v[10:13], v6
	ds_read_b128 v[14:17], v6 offset:1024
	ds_read_b128 v[2:5], v6 offset:2048
	ds_read_b128 v[6:9], v6 offset:3072
	v_lshl_add_u64 v[174:175], s[30:31], 0, v[170:171]
	s_add_i32 m0, s43, 0xc000
	ds_read_b128 v[190:193], v223
	ds_read_b128 v[194:197], v223 offset:1024
	ds_read_b128 v[198:201], v223 offset:2048
	ds_read_b128 v[202:205], v223 offset:3072
	ds_read_b128 v[224:227], v223 offset:4096
	ds_read_b128 v[228:231], v223 offset:5120
	ds_read_b128 v[232:235], v223 offset:6144
	ds_read_b128 v[236:239], v223 offset:7168
	global_load_lds_dwordx4 v[174:175], off
	v_lshl_add_u64 v[174:175], s[30:31], 0, v[172:173]
	s_add_i32 m0, s43, 0xe000
	s_nop 0
	global_load_lds_dwordx4 v[174:175], off
	s_waitcnt vmcnt(8)
	s_waitcnt lgkmcnt(0)
	s_barrier
	s_setprio 1
	s_waitcnt lgkmcnt(0)
	v_mfma_f32_16x16x128_f8f6f4 v[160:163], v[26:33], v[190:197], v[160:163]
	v_mfma_f32_16x16x128_f8f6f4 v[156:159], v[18:25], v[190:197], v[156:159]
	v_mfma_f32_16x16x128_f8f6f4 v[140:143], v[18:25], v[198:205], v[140:143]
	v_mfma_f32_16x16x128_f8f6f4 v[144:147], v[26:33], v[198:205], v[144:147]
	v_mfma_f32_16x16x128_f8f6f4 v[132:135], v[26:33], v[224:231], v[132:135]
	v_mfma_f32_16x16x128_f8f6f4 v[124:127], v[18:25], v[224:231], v[124:127]
	v_mfma_f32_16x16x128_f8f6f4 v[108:111], v[18:25], v[232:239], v[108:111]
	v_mfma_f32_16x16x128_f8f6f4 v[116:119], v[26:33], v[232:239], v[116:119]
	s_setprio 2
	s_setprio 1
	v_mfma_f32_16x16x128_f8f6f4 v[152:155], v[10:17], v[190:197], v[152:155]
	v_mfma_f32_16x16x128_f8f6f4 v[148:151], v[2:9], v[190:197], v[148:151]
	v_mfma_f32_16x16x128_f8f6f4 v[128:131], v[2:9], v[198:205], v[128:131]
	v_mfma_f32_16x16x128_f8f6f4 v[136:139], v[10:17], v[198:205], v[136:139]
	v_mfma_f32_16x16x128_f8f6f4 v[120:123], v[10:17], v[224:231], v[120:123]
	v_mfma_f32_16x16x128_f8f6f4 v[112:115], v[2:9], v[224:231], v[112:115]
	v_mfma_f32_16x16x128_f8f6f4 v[100:103], v[2:9], v[232:239], v[100:103]
	v_mfma_f32_16x16x128_f8f6f4 v[104:107], v[10:17], v[232:239], v[104:107]
	s_setprio 2
	s_barrier
	s_add_i32 s14, s65, s42
	v_lshl_add_u64 v[174:175], s[36:37], 0, v[34:35]
	s_mov_b32 m0, s14
	ds_read_b128 v[196:199], v223 offset:16384
	ds_read_b128 v[200:203], v223 offset:17408
	ds_read_b128 v[204:207], v223 offset:18432
	ds_read_b128 v[208:211], v223 offset:19456
	ds_read_b128 v[224:227], v223 offset:20480
	ds_read_b128 v[228:231], v223 offset:21504
	ds_read_b128 v[232:235], v223 offset:22528
	ds_read_b128 v[236:239], v223 offset:23552
	global_load_lds_dwordx4 v[174:175], off
	s_add_i32 m0, s14, 0x2000
	s_add_u32 s30, s36, 0x58000
	v_lshl_add_u64 v[190:191], s[36:37], 0, v[164:165]
	s_addc_u32 s31, s37, 0
	s_add_i32 s14, s66, s42
	global_load_lds_dwordx4 v[190:191], off
	v_lshl_add_u64 v[178:179], s[30:31], 0, v[34:35]
	s_mov_b32 m0, s14
	v_lshl_add_u64 v[192:193], s[40:41], 0, v[168:169]
	global_load_lds_dwordx4 v[178:179], off
	v_lshl_add_u64 v[178:179], s[30:31], 0, v[164:165]
	s_add_i32 m0, s14, 0x2000
	v_lshl_add_u64 v[194:195], s[40:41], 0, v[166:167]
	global_load_lds_dwordx4 v[178:179], off
	s_mov_b32 m0, s43
	s_nop 0
	global_load_lds_dwordx4 v[192:193], off
	s_mov_b32 m0, s44
	s_nop 0
	global_load_lds_dwordx4 v[194:195], off
	s_waitcnt vmcnt(8)
	s_waitcnt lgkmcnt(0)
	s_barrier
	s_setprio 1
	s_waitcnt lgkmcnt(0)
	v_mfma_f32_16x16x128_f8f6f4 v[96:99], v[26:33], v[196:203], v[96:99]
	v_mfma_f32_16x16x128_f8f6f4 v[92:95], v[18:25], v[196:203], v[92:95]
	v_mfma_f32_16x16x128_f8f6f4 v[76:79], v[18:25], v[204:211], v[76:79]
	v_mfma_f32_16x16x128_f8f6f4 v[84:87], v[26:33], v[204:211], v[84:87]
	v_mfma_f32_16x16x128_f8f6f4 v[68:71], v[26:33], v[224:231], v[68:71]
	v_mfma_f32_16x16x128_f8f6f4 v[60:63], v[18:25], v[224:231], v[60:63]
	v_mfma_f32_16x16x128_f8f6f4 v[44:47], v[18:25], v[232:239], v[44:47]
	v_mfma_f32_16x16x128_f8f6f4 v[52:55], v[26:33], v[232:239], v[52:55]
	s_setprio 2
	s_setprio 1
	v_mfma_f32_16x16x128_f8f6f4 v[88:91], v[10:17], v[196:203], v[88:91]
	v_mfma_f32_16x16x128_f8f6f4 v[80:83], v[2:9], v[196:203], v[80:83]
	v_mfma_f32_16x16x128_f8f6f4 v[64:67], v[2:9], v[204:211], v[64:67]
	v_mfma_f32_16x16x128_f8f6f4 v[72:75], v[10:17], v[204:211], v[72:75]
	v_mfma_f32_16x16x128_f8f6f4 v[56:59], v[10:17], v[224:231], v[56:59]
	v_mfma_f32_16x16x128_f8f6f4 v[48:51], v[2:9], v[224:231], v[48:51]
	v_mfma_f32_16x16x128_f8f6f4 v[36:39], v[2:9], v[232:239], v[36:39]
	v_mfma_f32_16x16x128_f8f6f4 v[40:43], v[10:17], v[232:239], v[40:43]
	s_setprio 2
	s_barrier
	s_add_i32 s14, 0, 0x18000
	s_add_i32 s65, 0, 0x1c000
	v_add_u32_e32 v14, s14, v222
	v_add_u32_e32 v30, s65, v222
	ds_read_b128 v[2:5], v14
	ds_read_b128 v[6:9], v14 offset:1024
	ds_read_b128 v[10:13], v14 offset:2048
	ds_read_b128 v[14:17], v14 offset:3072
	ds_read_b128 v[18:21], v30
	ds_read_b128 v[22:25], v30 offset:1024
	ds_read_b128 v[26:29], v30 offset:2048
	ds_read_b128 v[30:33], v30 offset:3072
	s_add_u32 s30, s40, 0x58000
	s_addc_u32 s31, s41, 0
	s_mov_b32 m0, s45
	v_lshl_add_u64 v[178:179], s[30:31], 0, v[168:169]
	ds_read_b128 v[196:199], v223 offset:32768
	ds_read_b128 v[200:203], v223 offset:33792
	ds_read_b128 v[204:207], v223 offset:34816
	ds_read_b128 v[208:211], v223 offset:35840
	ds_read_b128 v[224:227], v223 offset:36864
	ds_read_b128 v[228:231], v223 offset:37888
	ds_read_b128 v[232:235], v223 offset:38912
	ds_read_b128 v[236:239], v223 offset:39936
	global_load_lds_dwordx4 v[178:179], off
	v_lshl_add_u64 v[178:179], s[30:31], 0, v[166:167]
	s_mov_b32 m0, s46
	s_nop 0
	global_load_lds_dwordx4 v[178:179], off
	s_waitcnt vmcnt(8)
	s_waitcnt lgkmcnt(0)
	s_barrier
	s_setprio 1
	s_waitcnt lgkmcnt(0)
	v_mfma_f32_16x16x128_f8f6f4 v[160:163], v[2:9], v[196:203], v[160:163]
	v_mfma_f32_16x16x128_f8f6f4 v[156:159], v[10:17], v[196:203], v[156:159]
	v_mfma_f32_16x16x128_f8f6f4 v[140:143], v[10:17], v[204:211], v[140:143]
	v_mfma_f32_16x16x128_f8f6f4 v[144:147], v[2:9], v[204:211], v[144:147]
	v_mfma_f32_16x16x128_f8f6f4 v[132:135], v[2:9], v[224:231], v[132:135]
	v_mfma_f32_16x16x128_f8f6f4 v[124:127], v[10:17], v[224:231], v[124:127]
	v_mfma_f32_16x16x128_f8f6f4 v[108:111], v[10:17], v[232:239], v[108:111]
	v_mfma_f32_16x16x128_f8f6f4 v[116:119], v[2:9], v[232:239], v[116:119]
	s_setprio 2
	s_setprio 1
	v_mfma_f32_16x16x128_f8f6f4 v[152:155], v[18:25], v[196:203], v[152:155]
	v_mfma_f32_16x16x128_f8f6f4 v[148:151], v[26:33], v[196:203], v[148:151]
	v_mfma_f32_16x16x128_f8f6f4 v[128:131], v[26:33], v[204:211], v[128:131]
	v_mfma_f32_16x16x128_f8f6f4 v[136:139], v[18:25], v[204:211], v[136:139]
	v_mfma_f32_16x16x128_f8f6f4 v[120:123], v[18:25], v[224:231], v[120:123]
	v_mfma_f32_16x16x128_f8f6f4 v[112:115], v[26:33], v[224:231], v[112:115]
	v_mfma_f32_16x16x128_f8f6f4 v[100:103], v[26:33], v[232:239], v[100:103]
	v_mfma_f32_16x16x128_f8f6f4 v[104:107], v[18:25], v[232:239], v[104:107]
	s_setprio 2
	s_barrier
	s_add_i32 s14, s14, s42
	v_lshl_add_u64 v[174:175], v[174:175], 0, s[18:19]
	s_mov_b32 m0, s14
	ds_read_b128 v[196:199], v223 offset:49152
	ds_read_b128 v[200:203], v223 offset:50176
	ds_read_b128 v[204:207], v223 offset:51200
	ds_read_b128 v[208:211], v223 offset:52224
	ds_read_b128 v[224:227], v223 offset:53248
	ds_read_b128 v[228:231], v223 offset:54272
	ds_read_b128 v[232:235], v223 offset:55296
	ds_read_b128 v[236:239], v223 offset:56320
	global_load_lds_dwordx4 v[174:175], off
	s_add_i32 m0, s14, 0x2000
	s_add_u32 s30, s36, 0x58080
	v_lshl_add_u64 v[174:175], v[190:191], 0, s[18:19]
	s_addc_u32 s31, s37, 0
	s_add_i32 s14, s65, s42
	global_load_lds_dwordx4 v[174:175], off
	v_lshl_add_u64 v[174:175], s[30:31], 0, v[34:35]
	s_mov_b32 m0, s14
	s_nop 0
	global_load_lds_dwordx4 v[174:175], off
	v_lshl_add_u64 v[174:175], s[30:31], 0, v[164:165]
	s_add_i32 m0, s14, 0x2000
	s_nop 0
	global_load_lds_dwordx4 v[174:175], off
	v_lshl_add_u64 v[174:175], v[192:193], 0, s[18:19]
	s_mov_b32 m0, s51
	s_nop 0
	global_load_lds_dwordx4 v[174:175], off
	v_lshl_add_u64 v[174:175], v[194:195], 0, s[18:19]
	s_mov_b32 m0, s52
	s_nop 0
	global_load_lds_dwordx4 v[174:175], off
	s_waitcnt vmcnt(8)
	s_waitcnt lgkmcnt(0)
	s_barrier
	s_setprio 1
	s_waitcnt lgkmcnt(0)
	v_mfma_f32_16x16x128_f8f6f4 v[96:99], v[2:9], v[196:203], v[96:99]
	v_mfma_f32_16x16x128_f8f6f4 v[92:95], v[10:17], v[196:203], v[92:95]
	v_mfma_f32_16x16x128_f8f6f4 v[76:79], v[10:17], v[204:211], v[76:79]
	v_mfma_f32_16x16x128_f8f6f4 v[84:87], v[2:9], v[204:211], v[84:87]
	v_mfma_f32_16x16x128_f8f6f4 v[68:71], v[2:9], v[224:231], v[68:71]
	v_mfma_f32_16x16x128_f8f6f4 v[60:63], v[10:17], v[224:231], v[60:63]
	v_mfma_f32_16x16x128_f8f6f4 v[44:47], v[10:17], v[232:239], v[44:47]
	v_mfma_f32_16x16x128_f8f6f4 v[52:55], v[2:9], v[232:239], v[52:55]
	s_setprio 2
	s_setprio 1
	v_mfma_f32_16x16x128_f8f6f4 v[88:91], v[18:25], v[196:203], v[88:91]
	v_mfma_f32_16x16x128_f8f6f4 v[80:83], v[26:33], v[196:203], v[80:83]
	v_mfma_f32_16x16x128_f8f6f4 v[64:67], v[26:33], v[204:211], v[64:67]
	v_mfma_f32_16x16x128_f8f6f4 v[72:75], v[18:25], v[204:211], v[72:75]
	v_mfma_f32_16x16x128_f8f6f4 v[56:59], v[18:25], v[224:231], v[56:59]
	v_mfma_f32_16x16x128_f8f6f4 v[48:51], v[26:33], v[224:231], v[48:51]
	v_mfma_f32_16x16x128_f8f6f4 v[36:39], v[26:33], v[232:239], v[36:39]
	v_mfma_f32_16x16x128_f8f6f4 v[40:43], v[18:25], v[232:239], v[40:43]
	s_setprio 2
	s_barrier
	s_add_i32 s64, s64, 2
	s_add_u32 s62, s62, 0x100
	s_addc_u32 s63, s63, 0
	s_cmp_gt_u32 s64, 19
	s_mov_b64 s[30:31], s[22:23]
	s_cbranch_scc0 .LBB0_1160
	s_and_b64 vcc, exec, s[8:9]
	s_mov_b32 s58, 0x19b00000
	v_readlane_b32 s59, v255, 10
	s_mov_b32 s60, 0xff61b1e6
	s_mov_b64 s[62:63], 0x800
	s_cbranch_vccz .LBB0_1163
	s_barrier
